# v_V without the back-to-back s_setprio 0 / s_setprio 1 pairs between consecutive MFMA groups
# speedup vs baseline: 1.0048x; 1.0004x over previous
.LBB0_216:
	v_add_u32_e32 v130, s88, v196
	v_add_u32_e32 v134, s89, v196
	ds_read_b128 v[158:161], v130
	ds_read_b128 v[150:153], v130 offset:1024
	ds_read_b128 v[154:157], v130 offset:2048
	ds_read_b128 v[146:149], v130 offset:3072
	ds_read_b128 v[142:145], v134
	ds_read_b128 v[130:133], v134 offset:1024
	ds_read_b128 v[138:141], v134 offset:2048
	ds_read_b128 v[134:137], v134 offset:3072
	s_add_u32 s25, s50, 0xfff80080
	s_addc_u32 s56, s51, -1
	s_and_b64 s[18:19], s[18:19], exec
	s_cselect_b32 s59, s31, s56
	s_cselect_b32 s58, s4, s25
	s_cselect_b32 s57, s5, s64
	s_cselect_b32 s56, s29, s92
	s_add_i32 m0, s39, 0xc000
	ds_read_b128 v[186:189], v198
	ds_read_b128 v[190:193], v198 offset:1024
	ds_read_b128 v[200:203], v198 offset:2048
	ds_read_b128 v[204:207], v198 offset:3072
	ds_read_b128 v[208:211], v198 offset:4096
	ds_read_b128 v[212:215], v198 offset:5120
	ds_read_b128 v[216:219], v198 offset:6144
	ds_read_b128 v[220:223], v198 offset:7168
	global_load_lds_dwordx4 v170, s[50:51]
	s_add_i32 m0, s39, 0xe000
	s_nop 0
	global_load_lds_dwordx4 v172, s[50:51]
	s_waitcnt vmcnt(8)
	s_waitcnt lgkmcnt(0)
	s_barrier
	s_setprio 1
	s_waitcnt lgkmcnt(0)
	v_mfma_i32_16x16x64_i8 v[126:129], v[158:161], v[186:189], v[126:129]
	v_mfma_i32_16x16x64_i8 v[122:125], v[154:157], v[186:189], v[122:125]
	v_mfma_i32_16x16x64_i8 v[106:109], v[154:157], v[200:203], v[106:109]
	v_mfma_i32_16x16x64_i8 v[110:113], v[158:161], v[200:203], v[110:113]
	v_mfma_i32_16x16x64_i8 v[94:97], v[158:161], v[208:211], v[94:97]
	v_mfma_i32_16x16x64_i8 v[90:93], v[154:157], v[208:211], v[90:93]
	v_mfma_i32_16x16x64_i8 v[74:77], v[154:157], v[216:219], v[74:77]
	v_mfma_i32_16x16x64_i8 v[78:81], v[158:161], v[216:219], v[78:81]
	s_nop 0
	v_mfma_i32_16x16x64_i8 v[126:129], v[150:153], v[190:193], v[126:129]
	v_mfma_i32_16x16x64_i8 v[122:125], v[146:149], v[190:193], v[122:125]
	v_mfma_i32_16x16x64_i8 v[106:109], v[146:149], v[204:207], v[106:109]
	v_mfma_i32_16x16x64_i8 v[110:113], v[150:153], v[204:207], v[110:113]
	v_mfma_i32_16x16x64_i8 v[94:97], v[150:153], v[212:215], v[94:97]
	v_mfma_i32_16x16x64_i8 v[90:93], v[146:149], v[212:215], v[90:93]
	v_mfma_i32_16x16x64_i8 v[74:77], v[146:149], v[220:223], v[74:77]
	v_mfma_i32_16x16x64_i8 v[78:81], v[150:153], v[220:223], v[78:81]
	v_mfma_i32_16x16x64_i8 v[118:121], v[142:145], v[186:189], v[118:121]
	v_mfma_i32_16x16x64_i8 v[114:117], v[138:141], v[186:189], v[114:117]
	v_mfma_i32_16x16x64_i8 v[98:101], v[138:141], v[200:203], v[98:101]
	v_mfma_i32_16x16x64_i8 v[102:105], v[142:145], v[200:203], v[102:105]
	v_mfma_i32_16x16x64_i8 v[86:89], v[142:145], v[208:211], v[86:89]
	v_mfma_i32_16x16x64_i8 v[82:85], v[138:141], v[208:211], v[82:85]
	v_mfma_i32_16x16x64_i8 v[66:69], v[138:141], v[216:219], v[66:69]
	v_mfma_i32_16x16x64_i8 v[70:73], v[142:145], v[216:219], v[70:73]
	s_nop 0
	v_mfma_i32_16x16x64_i8 v[118:121], v[130:133], v[190:193], v[118:121]
	v_mfma_i32_16x16x64_i8 v[114:117], v[134:137], v[190:193], v[114:117]
	v_mfma_i32_16x16x64_i8 v[98:101], v[134:137], v[204:207], v[98:101]
	v_mfma_i32_16x16x64_i8 v[102:105], v[130:133], v[204:207], v[102:105]
	v_mfma_i32_16x16x64_i8 v[86:89], v[130:133], v[212:215], v[86:89]
	v_mfma_i32_16x16x64_i8 v[82:85], v[134:137], v[212:215], v[82:85]
	v_mfma_i32_16x16x64_i8 v[66:69], v[134:137], v[220:223], v[66:69]
	v_mfma_i32_16x16x64_i8 v[70:73], v[130:133], v[220:223], v[70:73]
	s_setprio 0
	s_barrier
	s_add_i32 s18, s88, s7
	s_mov_b32 m0, s18
	ds_read_b128 v[200:203], v198 offset:16384
	ds_read_b128 v[204:207], v198 offset:17408
	ds_read_b128 v[208:211], v198 offset:18432
	ds_read_b128 v[212:215], v198 offset:19456
	ds_read_b128 v[216:219], v198 offset:20480
	ds_read_b128 v[220:223], v198 offset:21504
	ds_read_b128 v[224:227], v198 offset:22528
	ds_read_b128 v[228:231], v198 offset:23552
	global_load_lds_dwordx4 v164, s[56:57]
	s_add_i32 m0, s18, 0x2000
	s_add_u32 s18, s56, 0x80000
	s_addc_u32 s19, s57, 0
	s_add_i32 s25, s89, s7
	global_load_lds_dwordx4 v168, s[56:57]
	s_mov_b32 m0, s25
	s_nop 0
	global_load_lds_dwordx4 v164, s[18:19]
	s_add_i32 m0, s25, 0x2000
	s_nop 0
	global_load_lds_dwordx4 v168, s[18:19]
	s_mov_b32 m0, s39
	s_nop 0
	global_load_lds_dwordx4 v162, s[58:59]
	s_mov_b32 m0, s43
	s_nop 0
	global_load_lds_dwordx4 v166, s[58:59]
	s_waitcnt vmcnt(8)
	s_waitcnt lgkmcnt(0)
	s_barrier
	s_setprio 1
	s_waitcnt lgkmcnt(0)
	v_mfma_i32_16x16x64_i8 v[62:65], v[158:161], v[200:203], v[62:65]
	v_mfma_i32_16x16x64_i8 v[58:61], v[154:157], v[200:203], v[58:61]
	v_mfma_i32_16x16x64_i8 v[42:45], v[154:157], v[208:211], v[42:45]
	v_mfma_i32_16x16x64_i8 v[46:49], v[158:161], v[208:211], v[46:49]
	v_mfma_i32_16x16x64_i8 v[30:33], v[158:161], v[216:219], v[30:33]
	v_mfma_i32_16x16x64_i8 v[26:29], v[154:157], v[216:219], v[26:29]
	v_mfma_i32_16x16x64_i8 v[10:13], v[154:157], v[224:227], v[10:13]
	v_mfma_i32_16x16x64_i8 v[14:17], v[158:161], v[224:227], v[14:17]
	s_nop 0
	v_mfma_i32_16x16x64_i8 v[62:65], v[150:153], v[204:207], v[62:65]
	v_mfma_i32_16x16x64_i8 v[58:61], v[146:149], v[204:207], v[58:61]
	v_mfma_i32_16x16x64_i8 v[42:45], v[146:149], v[212:215], v[42:45]
	v_mfma_i32_16x16x64_i8 v[46:49], v[150:153], v[212:215], v[46:49]
	v_mfma_i32_16x16x64_i8 v[30:33], v[150:153], v[220:223], v[30:33]
	v_mfma_i32_16x16x64_i8 v[26:29], v[146:149], v[220:223], v[26:29]
	v_mfma_i32_16x16x64_i8 v[10:13], v[146:149], v[228:231], v[10:13]
	v_mfma_i32_16x16x64_i8 v[14:17], v[150:153], v[228:231], v[14:17]
	v_mfma_i32_16x16x64_i8 v[54:57], v[142:145], v[200:203], v[54:57]
	v_mfma_i32_16x16x64_i8 v[50:53], v[138:141], v[200:203], v[50:53]
	v_mfma_i32_16x16x64_i8 v[34:37], v[138:141], v[208:211], v[34:37]
	v_mfma_i32_16x16x64_i8 v[38:41], v[142:145], v[208:211], v[38:41]
	v_mfma_i32_16x16x64_i8 v[22:25], v[142:145], v[216:219], v[22:25]
	v_mfma_i32_16x16x64_i8 v[18:21], v[138:141], v[216:219], v[18:21]
	v_mfma_i32_16x16x64_i8 v[2:5], v[138:141], v[224:227], v[2:5]
	v_mfma_i32_16x16x64_i8 v[6:9], v[142:145], v[224:227], v[6:9]
	s_nop 0
	v_mfma_i32_16x16x64_i8 v[54:57], v[130:133], v[204:207], v[54:57]
	v_mfma_i32_16x16x64_i8 v[50:53], v[134:137], v[204:207], v[50:53]
	v_mfma_i32_16x16x64_i8 v[34:37], v[134:137], v[212:215], v[34:37]
	v_mfma_i32_16x16x64_i8 v[38:41], v[130:133], v[212:215], v[38:41]
	v_mfma_i32_16x16x64_i8 v[22:25], v[130:133], v[220:223], v[22:25]
	v_mfma_i32_16x16x64_i8 v[18:21], v[134:137], v[220:223], v[18:21]
	v_mfma_i32_16x16x64_i8 v[2:5], v[134:137], v[228:231], v[2:5]
	v_mfma_i32_16x16x64_i8 v[6:9], v[130:133], v[228:231], v[6:9]
	s_setprio 0
	s_barrier
	s_add_i32 s25, 0, 0x18000
	s_add_i32 vcc_lo, 0, 0x1c000
	v_add_u32_e32 v142, s25, v196
	v_add_u32_e32 v158, vcc_lo, v196
	ds_read_b128 v[130:133], v142
	ds_read_b128 v[134:137], v142 offset:1024
	ds_read_b128 v[138:141], v142 offset:2048
	ds_read_b128 v[142:145], v142 offset:3072
	ds_read_b128 v[146:149], v158
	ds_read_b128 v[150:153], v158 offset:1024
	ds_read_b128 v[154:157], v158 offset:2048
	ds_read_b128 v[158:161], v158 offset:3072
	s_add_u32 s18, s58, 0x80000
	s_addc_u32 s19, s59, 0
	s_mov_b32 m0, s61
	ds_read_b128 v[200:203], v198 offset:32768
	ds_read_b128 v[204:207], v198 offset:33792
	ds_read_b128 v[208:211], v198 offset:34816
	ds_read_b128 v[212:215], v198 offset:35840
	ds_read_b128 v[216:219], v198 offset:36864
	ds_read_b128 v[220:223], v198 offset:37888
	ds_read_b128 v[224:227], v198 offset:38912
	ds_read_b128 v[228:231], v198 offset:39936
	global_load_lds_dwordx4 v162, s[18:19]
	s_mov_b32 m0, s62
	s_nop 0
	global_load_lds_dwordx4 v166, s[18:19]
	s_waitcnt vmcnt(8)
	s_waitcnt lgkmcnt(0)
	s_barrier
	s_setprio 1
	s_waitcnt lgkmcnt(0)
	v_mfma_i32_16x16x64_i8 v[126:129], v[130:133], v[200:203], v[126:129]
	v_mfma_i32_16x16x64_i8 v[122:125], v[138:141], v[200:203], v[122:125]
	v_mfma_i32_16x16x64_i8 v[106:109], v[138:141], v[208:211], v[106:109]
	v_mfma_i32_16x16x64_i8 v[110:113], v[130:133], v[208:211], v[110:113]
	v_mfma_i32_16x16x64_i8 v[94:97], v[130:133], v[216:219], v[94:97]
	v_mfma_i32_16x16x64_i8 v[90:93], v[138:141], v[216:219], v[90:93]
	v_mfma_i32_16x16x64_i8 v[74:77], v[138:141], v[224:227], v[74:77]
	v_mfma_i32_16x16x64_i8 v[78:81], v[130:133], v[224:227], v[78:81]
	s_nop 0
	v_mfma_i32_16x16x64_i8 v[126:129], v[134:137], v[204:207], v[126:129]
	v_mfma_i32_16x16x64_i8 v[122:125], v[142:145], v[204:207], v[122:125]
	v_mfma_i32_16x16x64_i8 v[106:109], v[142:145], v[212:215], v[106:109]
	v_mfma_i32_16x16x64_i8 v[110:113], v[134:137], v[212:215], v[110:113]
	v_mfma_i32_16x16x64_i8 v[94:97], v[134:137], v[220:223], v[94:97]
	v_mfma_i32_16x16x64_i8 v[90:93], v[142:145], v[220:223], v[90:93]
	v_mfma_i32_16x16x64_i8 v[74:77], v[142:145], v[228:231], v[74:77]
	v_mfma_i32_16x16x64_i8 v[78:81], v[134:137], v[228:231], v[78:81]
	v_mfma_i32_16x16x64_i8 v[118:121], v[146:149], v[200:203], v[118:121]
	v_mfma_i32_16x16x64_i8 v[114:117], v[154:157], v[200:203], v[114:117]
	v_mfma_i32_16x16x64_i8 v[98:101], v[154:157], v[208:211], v[98:101]
	v_mfma_i32_16x16x64_i8 v[102:105], v[146:149], v[208:211], v[102:105]
	v_mfma_i32_16x16x64_i8 v[86:89], v[146:149], v[216:219], v[86:89]
	v_mfma_i32_16x16x64_i8 v[82:85], v[154:157], v[216:219], v[82:85]
	v_mfma_i32_16x16x64_i8 v[66:69], v[154:157], v[224:227], v[66:69]
	v_mfma_i32_16x16x64_i8 v[70:73], v[146:149], v[224:227], v[70:73]
	s_nop 0
	v_mfma_i32_16x16x64_i8 v[118:121], v[150:153], v[204:207], v[118:121]
	v_mfma_i32_16x16x64_i8 v[114:117], v[158:161], v[204:207], v[114:117]
	v_mfma_i32_16x16x64_i8 v[98:101], v[158:161], v[212:215], v[98:101]
	v_mfma_i32_16x16x64_i8 v[102:105], v[150:153], v[212:215], v[102:105]
	v_mfma_i32_16x16x64_i8 v[86:89], v[150:153], v[220:223], v[86:89]
	v_mfma_i32_16x16x64_i8 v[82:85], v[158:161], v[220:223], v[82:85]
	v_mfma_i32_16x16x64_i8 v[66:69], v[158:161], v[228:231], v[66:69]
	v_mfma_i32_16x16x64_i8 v[70:73], v[150:153], v[228:231], v[70:73]
	s_setprio 0
	s_barrier
	s_add_i32 s18, s25, s7
	s_mov_b32 m0, s18
	s_add_u32 s98, s56, 0x80
	s_addc_u32 s99, s57, 0
	s_add_u32 s100, s58, 0x80
	s_addc_u32 s101, s59, 0
	ds_read_b128 v[200:203], v198 offset:49152
	ds_read_b128 v[204:207], v198 offset:50176
	ds_read_b128 v[208:211], v198 offset:51200
	ds_read_b128 v[212:215], v198 offset:52224
	ds_read_b128 v[216:219], v198 offset:53248
	ds_read_b128 v[220:223], v198 offset:54272
	ds_read_b128 v[224:227], v198 offset:55296
	ds_read_b128 v[228:231], v198 offset:56320
	global_load_lds_dwordx4 v164, s[98:99]
	s_add_i32 m0, s18, 0x2000
	s_add_u32 s18, s56, 0x80080
	s_addc_u32 s19, s57, 0
	s_add_i32 s25, vcc_lo, s7
	global_load_lds_dwordx4 v168, s[98:99]
	s_mov_b32 m0, s25
	s_nop 0
	global_load_lds_dwordx4 v164, s[18:19]
	s_add_i32 m0, s25, 0x2000
	s_nop 0
	global_load_lds_dwordx4 v168, s[18:19]
	s_mov_b32 m0, s67
	s_nop 0
	global_load_lds_dwordx4 v162, s[100:101]
	s_mov_b32 m0, s68
	s_nop 0
	global_load_lds_dwordx4 v166, s[100:101]
	s_waitcnt vmcnt(8)
	s_waitcnt lgkmcnt(0)
	s_barrier
	s_setprio 1
	s_waitcnt lgkmcnt(0)
	v_mfma_i32_16x16x64_i8 v[62:65], v[130:133], v[200:203], v[62:65]
	v_mfma_i32_16x16x64_i8 v[58:61], v[138:141], v[200:203], v[58:61]
	v_mfma_i32_16x16x64_i8 v[42:45], v[138:141], v[208:211], v[42:45]
	v_mfma_i32_16x16x64_i8 v[46:49], v[130:133], v[208:211], v[46:49]
	v_mfma_i32_16x16x64_i8 v[30:33], v[130:133], v[216:219], v[30:33]
	v_mfma_i32_16x16x64_i8 v[26:29], v[138:141], v[216:219], v[26:29]
	v_mfma_i32_16x16x64_i8 v[10:13], v[138:141], v[224:227], v[10:13]
	v_mfma_i32_16x16x64_i8 v[14:17], v[130:133], v[224:227], v[14:17]
	s_nop 0
	v_mfma_i32_16x16x64_i8 v[62:65], v[134:137], v[204:207], v[62:65]
	v_mfma_i32_16x16x64_i8 v[58:61], v[142:145], v[204:207], v[58:61]
	v_mfma_i32_16x16x64_i8 v[42:45], v[142:145], v[212:215], v[42:45]
	v_mfma_i32_16x16x64_i8 v[46:49], v[134:137], v[212:215], v[46:49]
	v_mfma_i32_16x16x64_i8 v[30:33], v[134:137], v[220:223], v[30:33]
	v_mfma_i32_16x16x64_i8 v[26:29], v[142:145], v[220:223], v[26:29]
	v_mfma_i32_16x16x64_i8 v[10:13], v[142:145], v[228:231], v[10:13]
	v_mfma_i32_16x16x64_i8 v[14:17], v[134:137], v[228:231], v[14:17]
	v_mfma_i32_16x16x64_i8 v[54:57], v[146:149], v[200:203], v[54:57]
	v_mfma_i32_16x16x64_i8 v[50:53], v[154:157], v[200:203], v[50:53]
	v_mfma_i32_16x16x64_i8 v[34:37], v[154:157], v[208:211], v[34:37]
	v_mfma_i32_16x16x64_i8 v[38:41], v[146:149], v[208:211], v[38:41]
	v_mfma_i32_16x16x64_i8 v[22:25], v[146:149], v[216:219], v[22:25]
	v_mfma_i32_16x16x64_i8 v[18:21], v[154:157], v[216:219], v[18:21]
	v_mfma_i32_16x16x64_i8 v[2:5], v[154:157], v[224:227], v[2:5]
	v_mfma_i32_16x16x64_i8 v[6:9], v[146:149], v[224:227], v[6:9]
	s_nop 0
	v_mfma_i32_16x16x64_i8 v[54:57], v[150:153], v[204:207], v[54:57]
	v_mfma_i32_16x16x64_i8 v[50:53], v[158:161], v[204:207], v[50:53]
	v_mfma_i32_16x16x64_i8 v[34:37], v[158:161], v[212:215], v[34:37]
	v_mfma_i32_16x16x64_i8 v[38:41], v[150:153], v[212:215], v[38:41]
	v_mfma_i32_16x16x64_i8 v[22:25], v[150:153], v[220:223], v[22:25]
	v_mfma_i32_16x16x64_i8 v[18:21], v[158:161], v[220:223], v[18:21]
	v_mfma_i32_16x16x64_i8 v[2:5], v[158:161], v[228:231], v[2:5]
	v_mfma_i32_16x16x64_i8 v[6:9], v[150:153], v[228:231], v[6:9]
	s_setprio 0
	s_barrier
	s_add_i32 s65, s65, 2
	s_add_u32 s50, s50, 0x100
	s_addc_u32 s51, s51, 0
	s_add_u32 s92, s92, 0x100
	s_addc_u32 s64, s64, 0
	s_cmp_gt_u32 s65, 29
	s_cbranch_scc1 .LBB0_219

.LBB0_242:
	ds_read_b128 v[150:153], v146
	ds_read_b128 v[154:157], v146 offset:1024
	ds_read_b128 v[158:161], v146 offset:2048
	ds_read_b128 v[162:165], v146 offset:3072
	ds_read_b128 v[166:169], v147
	ds_read_b128 v[170:173], v147 offset:1024
	ds_read_b128 v[174:177], v147 offset:2048
	ds_read_b128 v[178:181], v147 offset:3072
	s_add_u32 s36, s34, 0xfff00080
	s_addc_u32 s37, s35, -1
	s_cmp_eq_u32 s25, 60
	s_cselect_b32 s39, s5, s37
	s_cselect_b32 s38, s18, s36
	s_cselect_b32 s37, s17, s24
	s_cselect_b32 s36, s19, s21
	v_lshl_add_u64 v[142:143], s[34:35], 0, v[138:139]
	s_add_i32 m0, s31, 0xc000
	ds_read_b128 v[182:185], v148
	ds_read_b128 v[186:189], v148 offset:1024
	ds_read_b128 v[190:193], v148 offset:2048
	ds_read_b128 v[194:197], v148 offset:3072
	ds_read_b128 v[198:201], v148 offset:4096
	ds_read_b128 v[202:205], v148 offset:5120
	ds_read_b128 v[206:209], v148 offset:6144
	ds_read_b128 v[210:213], v148 offset:7168
	global_load_lds_dwordx4 v[142:143], off
	v_lshl_add_u64 v[142:143], s[34:35], 0, v[140:141]
	s_add_i32 m0, s31, 0xe000
	s_nop 0
	global_load_lds_dwordx4 v[142:143], off
	s_waitcnt vmcnt(8)
	s_waitcnt lgkmcnt(0)
	s_barrier
	s_setprio 1
	s_waitcnt lgkmcnt(0)
	v_mfma_f32_16x16x32_bf16 v[126:129], v[150:153], v[182:185], v[126:129]
	v_mfma_f32_16x16x32_bf16 v[122:125], v[158:161], v[182:185], v[122:125]
	v_mfma_f32_16x16x32_bf16 v[114:117], v[150:153], v[190:193], v[114:117]
	v_mfma_f32_16x16x32_bf16 v[106:109], v[158:161], v[190:193], v[106:109]
	v_mfma_f32_16x16x32_bf16 v[98:101], v[150:153], v[198:201], v[98:101]
	v_mfma_f32_16x16x32_bf16 v[90:93], v[158:161], v[198:201], v[90:93]
	v_mfma_f32_16x16x32_bf16 v[78:81], v[150:153], v[206:209], v[78:81]
	v_mfma_f32_16x16x32_bf16 v[74:77], v[158:161], v[206:209], v[74:77]
	v_mfma_f32_16x16x32_bf16 v[126:129], v[154:157], v[186:189], v[126:129]
	v_mfma_f32_16x16x32_bf16 v[122:125], v[162:165], v[186:189], v[122:125]
	v_mfma_f32_16x16x32_bf16 v[114:117], v[154:157], v[194:197], v[114:117]
	v_mfma_f32_16x16x32_bf16 v[106:109], v[162:165], v[194:197], v[106:109]
	v_mfma_f32_16x16x32_bf16 v[98:101], v[154:157], v[202:205], v[98:101]
	v_mfma_f32_16x16x32_bf16 v[90:93], v[162:165], v[202:205], v[90:93]
	v_mfma_f32_16x16x32_bf16 v[78:81], v[154:157], v[210:213], v[78:81]
	v_mfma_f32_16x16x32_bf16 v[74:77], v[162:165], v[210:213], v[74:77]
	v_mfma_f32_16x16x32_bf16 v[118:121], v[166:169], v[182:185], v[118:121]
	v_mfma_f32_16x16x32_bf16 v[110:113], v[174:177], v[182:185], v[110:113]
	v_mfma_f32_16x16x32_bf16 v[102:105], v[166:169], v[190:193], v[102:105]
	v_mfma_f32_16x16x32_bf16 v[94:97], v[174:177], v[190:193], v[94:97]
	v_mfma_f32_16x16x32_bf16 v[86:89], v[166:169], v[198:201], v[86:89]
	v_mfma_f32_16x16x32_bf16 v[82:85], v[174:177], v[198:201], v[82:85]
	v_mfma_f32_16x16x32_bf16 v[70:73], v[166:169], v[206:209], v[70:73]
	v_mfma_f32_16x16x32_bf16 v[66:69], v[174:177], v[206:209], v[66:69]
	v_mfma_f32_16x16x32_bf16 v[118:121], v[170:173], v[186:189], v[118:121]
	v_mfma_f32_16x16x32_bf16 v[110:113], v[178:181], v[186:189], v[110:113]
	v_mfma_f32_16x16x32_bf16 v[102:105], v[170:173], v[194:197], v[102:105]
	v_mfma_f32_16x16x32_bf16 v[94:97], v[178:181], v[194:197], v[94:97]
	v_mfma_f32_16x16x32_bf16 v[86:89], v[170:173], v[202:205], v[86:89]
	v_mfma_f32_16x16x32_bf16 v[82:85], v[178:181], v[202:205], v[82:85]
	v_mfma_f32_16x16x32_bf16 v[70:73], v[170:173], v[210:213], v[70:73]
	v_mfma_f32_16x16x32_bf16 v[66:69], v[178:181], v[210:213], v[66:69]
	s_setprio 0
	s_barrier
	s_add_i32 s61, s59, s42
	v_lshl_add_u64 v[142:143], s[36:37], 0, v[132:133]
	s_mov_b32 m0, s61
	ds_read_b128 v[182:185], v148 offset:16384
	ds_read_b128 v[186:189], v148 offset:17408
	ds_read_b128 v[190:193], v148 offset:18432
	ds_read_b128 v[194:197], v148 offset:19456
	ds_read_b128 v[198:201], v148 offset:20480
	ds_read_b128 v[202:205], v148 offset:21504
	ds_read_b128 v[206:209], v148 offset:22528
	ds_read_b128 v[210:213], v148 offset:23552
	global_load_lds_dwordx4 v[142:143], off
	s_add_i32 m0, s61, 0x2000
	s_add_u32 s62, s36, 0x100000
	v_lshl_add_u64 v[214:215], s[36:37], 0, v[136:137]
	s_addc_u32 s63, s37, 0
	s_add_i32 s61, s60, s42
	global_load_lds_dwordx4 v[214:215], off
	v_lshl_add_u64 v[216:217], s[62:63], 0, v[132:133]
	s_mov_b32 m0, s61
	v_lshl_add_u64 v[218:219], s[38:39], 0, v[134:135]
	global_load_lds_dwordx4 v[216:217], off
	v_lshl_add_u64 v[216:217], s[62:63], 0, v[136:137]
	s_add_i32 m0, s61, 0x2000
	s_nop 0
	global_load_lds_dwordx4 v[216:217], off
	v_lshl_add_u64 v[216:217], s[38:39], 0, v[130:131]
	s_mov_b32 m0, s31
	s_nop 0
	global_load_lds_dwordx4 v[216:217], off
	s_mov_b32 m0, s49
	s_nop 0
	global_load_lds_dwordx4 v[218:219], off
	s_waitcnt vmcnt(8)
	s_waitcnt lgkmcnt(0)
	s_barrier
	s_setprio 1
	s_waitcnt lgkmcnt(0)
	v_mfma_f32_16x16x32_bf16 v[62:65], v[150:153], v[182:185], v[62:65]
	v_mfma_f32_16x16x32_bf16 v[58:61], v[158:161], v[182:185], v[58:61]
	v_mfma_f32_16x16x32_bf16 v[50:53], v[150:153], v[190:193], v[50:53]
	v_mfma_f32_16x16x32_bf16 v[42:45], v[158:161], v[190:193], v[42:45]
	v_mfma_f32_16x16x32_bf16 v[34:37], v[150:153], v[198:201], v[34:37]
	v_mfma_f32_16x16x32_bf16 v[26:29], v[158:161], v[198:201], v[26:29]
	v_mfma_f32_16x16x32_bf16 v[18:21], v[150:153], v[206:209], v[18:21]
	v_mfma_f32_16x16x32_bf16 v[10:13], v[158:161], v[206:209], v[10:13]
	v_mfma_f32_16x16x32_bf16 v[62:65], v[154:157], v[186:189], v[62:65]
	v_mfma_f32_16x16x32_bf16 v[58:61], v[162:165], v[186:189], v[58:61]
	v_mfma_f32_16x16x32_bf16 v[50:53], v[154:157], v[194:197], v[50:53]
	v_mfma_f32_16x16x32_bf16 v[42:45], v[162:165], v[194:197], v[42:45]
	v_mfma_f32_16x16x32_bf16 v[34:37], v[154:157], v[202:205], v[34:37]
	v_mfma_f32_16x16x32_bf16 v[26:29], v[162:165], v[202:205], v[26:29]
	v_mfma_f32_16x16x32_bf16 v[18:21], v[154:157], v[210:213], v[18:21]
	v_mfma_f32_16x16x32_bf16 v[10:13], v[162:165], v[210:213], v[10:13]
	v_mfma_f32_16x16x32_bf16 v[54:57], v[166:169], v[182:185], v[54:57]
	v_mfma_f32_16x16x32_bf16 v[46:49], v[174:177], v[182:185], v[46:49]
	v_mfma_f32_16x16x32_bf16 v[38:41], v[166:169], v[190:193], v[38:41]
	v_mfma_f32_16x16x32_bf16 v[30:33], v[174:177], v[190:193], v[30:33]
	v_mfma_f32_16x16x32_bf16 v[22:25], v[166:169], v[198:201], v[22:25]
	v_mfma_f32_16x16x32_bf16 v[14:17], v[174:177], v[198:201], v[14:17]
	v_mfma_f32_16x16x32_bf16 v[6:9], v[166:169], v[206:209], v[6:9]
	v_mfma_f32_16x16x32_bf16 v[2:5], v[174:177], v[206:209], v[2:5]
	v_mfma_f32_16x16x32_bf16 v[54:57], v[170:173], v[186:189], v[54:57]
	v_mfma_f32_16x16x32_bf16 v[46:49], v[178:181], v[186:189], v[46:49]
	v_mfma_f32_16x16x32_bf16 v[38:41], v[170:173], v[194:197], v[38:41]
	v_mfma_f32_16x16x32_bf16 v[30:33], v[178:181], v[194:197], v[30:33]
	v_mfma_f32_16x16x32_bf16 v[22:25], v[170:173], v[202:205], v[22:25]
	v_mfma_f32_16x16x32_bf16 v[14:17], v[178:181], v[202:205], v[14:17]
	v_mfma_f32_16x16x32_bf16 v[6:9], v[170:173], v[210:213], v[6:9]
	v_mfma_f32_16x16x32_bf16 v[2:5], v[178:181], v[210:213], v[2:5]
	s_setprio 0
	s_barrier
	s_add_i32 s61, 0, 0x18000
	v_add_u32_e32 v149, s61, v144
	s_add_i32 s62, 0, 0x1c000
	ds_read_b128 v[150:153], v149
	ds_read_b128 v[154:157], v149 offset:1024
	ds_read_b128 v[158:161], v149 offset:2048
	ds_read_b128 v[162:165], v149 offset:3072
	v_add_u32_e32 v149, s62, v144
	ds_read_b128 v[166:169], v149
	ds_read_b128 v[170:173], v149 offset:1024
	ds_read_b128 v[174:177], v149 offset:2048
	ds_read_b128 v[178:181], v149 offset:3072
	s_add_u32 s38, s38, 0x100000
	s_addc_u32 s39, s39, 0
	s_mov_b32 m0, s50
	v_lshl_add_u64 v[220:221], s[38:39], 0, v[130:131]
	ds_read_b128 v[182:185], v148 offset:32768
	ds_read_b128 v[186:189], v148 offset:33792
	ds_read_b128 v[190:193], v148 offset:34816
	ds_read_b128 v[194:197], v148 offset:35840
	ds_read_b128 v[198:201], v148 offset:36864
	ds_read_b128 v[202:205], v148 offset:37888
	ds_read_b128 v[206:209], v148 offset:38912
	ds_read_b128 v[210:213], v148 offset:39936
	global_load_lds_dwordx4 v[220:221], off
	v_lshl_add_u64 v[220:221], s[38:39], 0, v[134:135]
	s_mov_b32 m0, s51
	s_nop 0
	global_load_lds_dwordx4 v[220:221], off
	s_waitcnt vmcnt(8)
	s_waitcnt lgkmcnt(0)
	s_barrier
	s_setprio 1
	s_waitcnt lgkmcnt(0)
	v_mfma_f32_16x16x32_bf16 v[126:129], v[150:153], v[182:185], v[126:129]
	v_mfma_f32_16x16x32_bf16 v[122:125], v[158:161], v[182:185], v[122:125]
	v_mfma_f32_16x16x32_bf16 v[114:117], v[150:153], v[190:193], v[114:117]
	v_mfma_f32_16x16x32_bf16 v[106:109], v[158:161], v[190:193], v[106:109]
	v_mfma_f32_16x16x32_bf16 v[98:101], v[150:153], v[198:201], v[98:101]
	v_mfma_f32_16x16x32_bf16 v[90:93], v[158:161], v[198:201], v[90:93]
	v_mfma_f32_16x16x32_bf16 v[78:81], v[150:153], v[206:209], v[78:81]
	v_mfma_f32_16x16x32_bf16 v[74:77], v[158:161], v[206:209], v[74:77]
	v_mfma_f32_16x16x32_bf16 v[126:129], v[154:157], v[186:189], v[126:129]
	v_mfma_f32_16x16x32_bf16 v[122:125], v[162:165], v[186:189], v[122:125]
	v_mfma_f32_16x16x32_bf16 v[114:117], v[154:157], v[194:197], v[114:117]
	v_mfma_f32_16x16x32_bf16 v[106:109], v[162:165], v[194:197], v[106:109]
	v_mfma_f32_16x16x32_bf16 v[98:101], v[154:157], v[202:205], v[98:101]
	v_mfma_f32_16x16x32_bf16 v[90:93], v[162:165], v[202:205], v[90:93]
	v_mfma_f32_16x16x32_bf16 v[78:81], v[154:157], v[210:213], v[78:81]
	v_mfma_f32_16x16x32_bf16 v[74:77], v[162:165], v[210:213], v[74:77]
	v_mfma_f32_16x16x32_bf16 v[118:121], v[166:169], v[182:185], v[118:121]
	v_mfma_f32_16x16x32_bf16 v[110:113], v[174:177], v[182:185], v[110:113]
	v_mfma_f32_16x16x32_bf16 v[102:105], v[166:169], v[190:193], v[102:105]
	v_mfma_f32_16x16x32_bf16 v[94:97], v[174:177], v[190:193], v[94:97]
	v_mfma_f32_16x16x32_bf16 v[86:89], v[166:169], v[198:201], v[86:89]
	v_mfma_f32_16x16x32_bf16 v[82:85], v[174:177], v[198:201], v[82:85]
	v_mfma_f32_16x16x32_bf16 v[70:73], v[166:169], v[206:209], v[70:73]
	v_mfma_f32_16x16x32_bf16 v[66:69], v[174:177], v[206:209], v[66:69]
	v_mfma_f32_16x16x32_bf16 v[118:121], v[170:173], v[186:189], v[118:121]
	v_mfma_f32_16x16x32_bf16 v[110:113], v[178:181], v[186:189], v[110:113]
	v_mfma_f32_16x16x32_bf16 v[102:105], v[170:173], v[194:197], v[102:105]
	v_mfma_f32_16x16x32_bf16 v[94:97], v[178:181], v[194:197], v[94:97]
	v_mfma_f32_16x16x32_bf16 v[86:89], v[170:173], v[202:205], v[86:89]
	v_mfma_f32_16x16x32_bf16 v[82:85], v[178:181], v[202:205], v[82:85]
	v_mfma_f32_16x16x32_bf16 v[70:73], v[170:173], v[210:213], v[70:73]
	v_mfma_f32_16x16x32_bf16 v[66:69], v[178:181], v[210:213], v[66:69]
	s_setprio 0
	s_barrier
	s_add_i32 s38, s61, s42
	v_lshl_add_u64 v[142:143], v[142:143], 0, s[10:11]
	s_mov_b32 m0, s38
	ds_read_b128 v[182:185], v148 offset:49152
	ds_read_b128 v[186:189], v148 offset:50176
	ds_read_b128 v[190:193], v148 offset:51200
	ds_read_b128 v[194:197], v148 offset:52224
	ds_read_b128 v[198:201], v148 offset:53248
	ds_read_b128 v[202:205], v148 offset:54272
	ds_read_b128 v[206:209], v148 offset:55296
	ds_read_b128 v[210:213], v148 offset:56320
	global_load_lds_dwordx4 v[142:143], off
	s_add_i32 m0, s38, 0x2000
	s_add_u32 s36, s36, 0x100080
	v_lshl_add_u64 v[142:143], v[214:215], 0, s[10:11]
	s_addc_u32 s37, s37, 0
	s_add_i32 s38, s62, s42
	global_load_lds_dwordx4 v[142:143], off
	v_lshl_add_u64 v[142:143], s[36:37], 0, v[132:133]
	s_mov_b32 m0, s38
	s_nop 0
	global_load_lds_dwordx4 v[142:143], off
	v_lshl_add_u64 v[142:143], s[36:37], 0, v[136:137]
	s_add_i32 m0, s38, 0x2000
	s_nop 0
	global_load_lds_dwordx4 v[142:143], off
	v_lshl_add_u64 v[142:143], v[216:217], 0, s[10:11]
	s_mov_b32 m0, s57
	s_nop 0
	global_load_lds_dwordx4 v[142:143], off
	v_lshl_add_u64 v[142:143], v[218:219], 0, s[10:11]
	s_mov_b32 m0, s58
	s_nop 0
	global_load_lds_dwordx4 v[142:143], off
	s_waitcnt vmcnt(8)
	s_waitcnt lgkmcnt(0)
	s_barrier
	s_setprio 1
	s_waitcnt lgkmcnt(0)
	v_mfma_f32_16x16x32_bf16 v[62:65], v[150:153], v[182:185], v[62:65]
	v_mfma_f32_16x16x32_bf16 v[58:61], v[158:161], v[182:185], v[58:61]
	v_mfma_f32_16x16x32_bf16 v[50:53], v[150:153], v[190:193], v[50:53]
	v_mfma_f32_16x16x32_bf16 v[42:45], v[158:161], v[190:193], v[42:45]
	v_mfma_f32_16x16x32_bf16 v[34:37], v[150:153], v[198:201], v[34:37]
	v_mfma_f32_16x16x32_bf16 v[26:29], v[158:161], v[198:201], v[26:29]
	v_mfma_f32_16x16x32_bf16 v[18:21], v[150:153], v[206:209], v[18:21]
	v_mfma_f32_16x16x32_bf16 v[10:13], v[158:161], v[206:209], v[10:13]
	v_mfma_f32_16x16x32_bf16 v[62:65], v[154:157], v[186:189], v[62:65]
	v_mfma_f32_16x16x32_bf16 v[58:61], v[162:165], v[186:189], v[58:61]
	v_mfma_f32_16x16x32_bf16 v[50:53], v[154:157], v[194:197], v[50:53]
	v_mfma_f32_16x16x32_bf16 v[42:45], v[162:165], v[194:197], v[42:45]
	v_mfma_f32_16x16x32_bf16 v[34:37], v[154:157], v[202:205], v[34:37]
	v_mfma_f32_16x16x32_bf16 v[26:29], v[162:165], v[202:205], v[26:29]
	v_mfma_f32_16x16x32_bf16 v[18:21], v[154:157], v[210:213], v[18:21]
	v_mfma_f32_16x16x32_bf16 v[10:13], v[162:165], v[210:213], v[10:13]
	v_mfma_f32_16x16x32_bf16 v[54:57], v[166:169], v[182:185], v[54:57]
	v_mfma_f32_16x16x32_bf16 v[46:49], v[174:177], v[182:185], v[46:49]
	v_mfma_f32_16x16x32_bf16 v[38:41], v[166:169], v[190:193], v[38:41]
	v_mfma_f32_16x16x32_bf16 v[30:33], v[174:177], v[190:193], v[30:33]
	v_mfma_f32_16x16x32_bf16 v[22:25], v[166:169], v[198:201], v[22:25]
	v_mfma_f32_16x16x32_bf16 v[14:17], v[174:177], v[198:201], v[14:17]
	v_mfma_f32_16x16x32_bf16 v[6:9], v[166:169], v[206:209], v[6:9]
	v_mfma_f32_16x16x32_bf16 v[2:5], v[174:177], v[206:209], v[2:5]
	v_mfma_f32_16x16x32_bf16 v[54:57], v[170:173], v[186:189], v[54:57]
	v_mfma_f32_16x16x32_bf16 v[46:49], v[178:181], v[186:189], v[46:49]
	v_mfma_f32_16x16x32_bf16 v[38:41], v[170:173], v[194:197], v[38:41]
	v_mfma_f32_16x16x32_bf16 v[30:33], v[178:181], v[194:197], v[30:33]
	v_mfma_f32_16x16x32_bf16 v[22:25], v[170:173], v[202:205], v[22:25]
	v_mfma_f32_16x16x32_bf16 v[14:17], v[178:181], v[202:205], v[14:17]
	v_mfma_f32_16x16x32_bf16 v[6:9], v[170:173], v[210:213], v[6:9]
	v_mfma_f32_16x16x32_bf16 v[2:5], v[178:181], v[210:213], v[2:5]
	s_setprio 0
	s_barrier
	s_add_i32 s25, s25, 2
	s_add_u32 s34, s34, 0x100
	s_addc_u32 s35, s35, 0
	s_add_u32 s21, s21, 0x100
	s_addc_u32 s24, s24, 0
	s_cmp_gt_u32 s25, 61
	s_cbranch_scc0 .LBB0_242
	s_and_b64 vcc, exec, s[12:13]
	s_cbranch_vccz .LBB0_245
	s_barrier

.LBB0_318:
	ds_read_b128 v[26:29], v185
	ds_read_b128 v[30:33], v185 offset:1024
	ds_read_b128 v[18:21], v185 offset:2048
	ds_read_b128 v[22:25], v185 offset:3072
	ds_read_b128 v[10:13], v186
	ds_read_b128 v[14:17], v186 offset:1024
	ds_read_b128 v[2:5], v186 offset:2048
	ds_read_b128 v[6:9], v186 offset:3072
	s_add_u32 s24, s26, 0xffea8080
	s_addc_u32 s25, s27, -1
	s_cmpk_eq_i32 s58, 0x52
	s_cselect_b32 s31, s5, s25
	s_cselect_b32 s30, s4, s24
	s_cselect_b32 s29, s21, s51
	s_cselect_b32 s28, s20, s50
	v_lshl_add_u64 v[212:213], s[26:27], 0, v[166:167]
	s_add_i32 m0, s7, 0xc000
	ds_read_b128 v[174:177], v187
	ds_read_b128 v[178:181], v187 offset:1024
	ds_read_b128 v[188:191], v187 offset:2048
	ds_read_b128 v[192:195], v187 offset:3072
	ds_read_b128 v[196:199], v187 offset:4096
	ds_read_b128 v[200:203], v187 offset:5120
	ds_read_b128 v[204:207], v187 offset:6144
	ds_read_b128 v[208:211], v187 offset:7168
	global_load_lds_dwordx4 v[212:213], off
	v_lshl_add_u64 v[212:213], s[26:27], 0, v[168:169]
	s_add_i32 m0, s7, 0xe000
	s_nop 0
	global_load_lds_dwordx4 v[212:213], off
	s_waitcnt vmcnt(8)
	s_waitcnt lgkmcnt(0)
	s_barrier
	s_setprio 1
	s_waitcnt lgkmcnt(0)
	v_mfma_f32_16x16x128_f8f6f4 v[158:161], v[26:33], v[174:181], v[158:161]
	v_mfma_f32_16x16x128_f8f6f4 v[154:157], v[18:25], v[174:181], v[154:157]
	v_mfma_f32_16x16x128_f8f6f4 v[138:141], v[18:25], v[188:195], v[138:141]
	v_mfma_f32_16x16x128_f8f6f4 v[142:145], v[26:33], v[188:195], v[142:145]
	v_mfma_f32_16x16x128_f8f6f4 v[126:129], v[26:33], v[196:203], v[126:129]
	v_mfma_f32_16x16x128_f8f6f4 v[122:125], v[18:25], v[196:203], v[122:125]
	v_mfma_f32_16x16x128_f8f6f4 v[106:109], v[18:25], v[204:211], v[106:109]
	v_mfma_f32_16x16x128_f8f6f4 v[110:113], v[26:33], v[204:211], v[110:113]
	v_mfma_f32_16x16x128_f8f6f4 v[102:105], v[10:17], v[204:211], v[102:105]
	v_mfma_f32_16x16x128_f8f6f4 v[98:101], v[2:9], v[204:211], v[98:101]
	v_mfma_f32_16x16x128_f8f6f4 v[146:149], v[2:9], v[174:181], v[146:149]
	v_mfma_f32_16x16x128_f8f6f4 v[150:153], v[10:17], v[174:181], v[150:153]
	v_mfma_f32_16x16x128_f8f6f4 v[134:137], v[10:17], v[188:195], v[134:137]
	v_mfma_f32_16x16x128_f8f6f4 v[130:133], v[2:9], v[188:195], v[130:133]
	v_mfma_f32_16x16x128_f8f6f4 v[114:117], v[2:9], v[196:203], v[114:117]
	v_mfma_f32_16x16x128_f8f6f4 v[118:121], v[10:17], v[196:203], v[118:121]
	s_setprio 0
	s_barrier
	s_add_i32 s24, s42, s3
	v_lshl_add_u64 v[174:175], s[28:29], 0, v[164:165]
	s_mov_b32 m0, s24
	ds_read_b128 v[188:191], v187 offset:16384
	ds_read_b128 v[192:195], v187 offset:17408
	ds_read_b128 v[196:199], v187 offset:18432
	ds_read_b128 v[200:203], v187 offset:19456
	ds_read_b128 v[204:207], v187 offset:20480
	ds_read_b128 v[208:211], v187 offset:21504
	ds_read_b128 v[212:215], v187 offset:22528
	ds_read_b128 v[216:219], v187 offset:23552
	global_load_lds_dwordx4 v[174:175], off
	s_add_i32 m0, s24, 0x2000
	s_add_u32 s24, s28, 0x158000
	v_lshl_add_u64 v[176:177], s[28:29], 0, v[162:163]
	s_addc_u32 s25, s29, 0
	s_add_i32 s59, s43, s3
	global_load_lds_dwordx4 v[176:177], off
	v_lshl_add_u64 v[178:179], s[24:25], 0, v[164:165]
	s_mov_b32 m0, s59
	v_lshl_add_u64 v[180:181], s[30:31], 0, v[162:163]
	global_load_lds_dwordx4 v[178:179], off
	v_lshl_add_u64 v[178:179], s[24:25], 0, v[162:163]
	s_add_i32 m0, s59, 0x2000
	s_nop 0
	global_load_lds_dwordx4 v[178:179], off
	v_lshl_add_u64 v[178:179], s[30:31], 0, v[164:165]
	s_mov_b32 m0, s7
	s_nop 0
	global_load_lds_dwordx4 v[178:179], off
	s_mov_b32 m0, s17
	s_nop 0
	global_load_lds_dwordx4 v[180:181], off
	s_waitcnt vmcnt(8)
	s_waitcnt lgkmcnt(0)
	s_barrier
	s_setprio 1
	s_waitcnt lgkmcnt(0)
	v_mfma_f32_16x16x128_f8f6f4 v[78:81], v[26:33], v[196:203], v[78:81]
	v_mfma_f32_16x16x128_f8f6f4 v[74:77], v[18:25], v[196:203], v[74:77]
	v_mfma_f32_16x16x128_f8f6f4 v[90:93], v[18:25], v[188:195], v[90:93]
	v_mfma_f32_16x16x128_f8f6f4 v[94:97], v[26:33], v[188:195], v[94:97]
	v_mfma_f32_16x16x128_f8f6f4 v[62:65], v[26:33], v[204:211], v[62:65]
	v_mfma_f32_16x16x128_f8f6f4 v[58:61], v[18:25], v[204:211], v[58:61]
	v_mfma_f32_16x16x128_f8f6f4 v[42:45], v[18:25], v[212:219], v[42:45]
	v_mfma_f32_16x16x128_f8f6f4 v[46:49], v[26:33], v[212:219], v[46:49]
	v_mfma_f32_16x16x128_f8f6f4 v[38:41], v[10:17], v[212:219], v[38:41]
	v_mfma_f32_16x16x128_f8f6f4 v[34:37], v[2:9], v[212:219], v[34:37]
	v_mfma_f32_16x16x128_f8f6f4 v[82:85], v[2:9], v[188:195], v[82:85]
	v_mfma_f32_16x16x128_f8f6f4 v[86:89], v[10:17], v[188:195], v[86:89]
	v_mfma_f32_16x16x128_f8f6f4 v[70:73], v[10:17], v[196:203], v[70:73]
	v_mfma_f32_16x16x128_f8f6f4 v[66:69], v[2:9], v[196:203], v[66:69]
	v_mfma_f32_16x16x128_f8f6f4 v[50:53], v[2:9], v[204:211], v[50:53]
	v_mfma_f32_16x16x128_f8f6f4 v[54:57], v[10:17], v[204:211], v[54:57]
	s_setprio 0
	s_barrier
	s_add_i32 s59, 0, 0x18000
	s_add_i32 s60, 0, 0x1c000
	v_add_u32_e32 v14, s59, v183
	v_add_u32_e32 v30, s60, v183
	ds_read_b128 v[2:5], v14
	ds_read_b128 v[6:9], v14 offset:1024
	ds_read_b128 v[10:13], v14 offset:2048
	ds_read_b128 v[14:17], v14 offset:3072
	ds_read_b128 v[18:21], v30
	ds_read_b128 v[22:25], v30 offset:1024
	ds_read_b128 v[26:29], v30 offset:2048
	ds_read_b128 v[30:33], v30 offset:3072
	s_add_u32 s24, s30, 0x158000
	s_addc_u32 s25, s31, 0
	s_mov_b32 m0, s34
	v_lshl_add_u64 v[220:221], s[24:25], 0, v[164:165]
	ds_read_b128 v[188:191], v187 offset:32768
	ds_read_b128 v[192:195], v187 offset:33792
	ds_read_b128 v[196:199], v187 offset:34816
	ds_read_b128 v[200:203], v187 offset:35840
	ds_read_b128 v[204:207], v187 offset:36864
	ds_read_b128 v[208:211], v187 offset:37888
	ds_read_b128 v[212:215], v187 offset:38912
	ds_read_b128 v[216:219], v187 offset:39936
	global_load_lds_dwordx4 v[220:221], off
	v_lshl_add_u64 v[220:221], s[24:25], 0, v[162:163]
	s_mov_b32 m0, s35
	s_nop 0
	global_load_lds_dwordx4 v[220:221], off
	s_waitcnt vmcnt(8)
	s_waitcnt lgkmcnt(0)
	s_barrier
	s_setprio 1
	s_waitcnt lgkmcnt(0)
	v_mfma_f32_16x16x128_f8f6f4 v[122:125], v[10:17], v[204:211], v[122:125]
	v_mfma_f32_16x16x128_f8f6f4 v[126:129], v[2:9], v[204:211], v[126:129]
	v_mfma_f32_16x16x128_f8f6f4 v[158:161], v[2:9], v[188:195], v[158:161]
	v_mfma_f32_16x16x128_f8f6f4 v[154:157], v[10:17], v[188:195], v[154:157]
	v_mfma_f32_16x16x128_f8f6f4 v[138:141], v[10:17], v[196:203], v[138:141]
	v_mfma_f32_16x16x128_f8f6f4 v[142:145], v[2:9], v[196:203], v[142:145]
	v_mfma_f32_16x16x128_f8f6f4 v[110:113], v[2:9], v[212:219], v[110:113]
	v_mfma_f32_16x16x128_f8f6f4 v[106:109], v[10:17], v[212:219], v[106:109]
	v_mfma_f32_16x16x128_f8f6f4 v[102:105], v[18:25], v[212:219], v[102:105]
	v_mfma_f32_16x16x128_f8f6f4 v[98:101], v[26:33], v[212:219], v[98:101]
	v_mfma_f32_16x16x128_f8f6f4 v[146:149], v[26:33], v[188:195], v[146:149]
	v_mfma_f32_16x16x128_f8f6f4 v[150:153], v[18:25], v[188:195], v[150:153]
	v_mfma_f32_16x16x128_f8f6f4 v[134:137], v[18:25], v[196:203], v[134:137]
	v_mfma_f32_16x16x128_f8f6f4 v[130:133], v[26:33], v[196:203], v[130:133]
	v_mfma_f32_16x16x128_f8f6f4 v[114:117], v[26:33], v[204:211], v[114:117]
	v_mfma_f32_16x16x128_f8f6f4 v[118:121], v[18:25], v[204:211], v[118:121]
	s_setprio 0
	s_barrier
	s_add_i32 s24, s59, s3
	v_lshl_add_u64 v[174:175], v[174:175], 0, s[12:13]
	s_mov_b32 m0, s24
	ds_read_b128 v[188:191], v187 offset:49152
	ds_read_b128 v[192:195], v187 offset:50176
	ds_read_b128 v[196:199], v187 offset:51200
	ds_read_b128 v[200:203], v187 offset:52224
	ds_read_b128 v[204:207], v187 offset:53248
	ds_read_b128 v[208:211], v187 offset:54272
	ds_read_b128 v[212:215], v187 offset:55296
	ds_read_b128 v[216:219], v187 offset:56320
	global_load_lds_dwordx4 v[174:175], off
	s_add_i32 m0, s24, 0x2000
	s_add_u32 s24, s28, 0x158080
	v_lshl_add_u64 v[174:175], v[176:177], 0, s[12:13]
	s_addc_u32 s25, s29, 0
	s_add_i32 s28, s60, s3
	global_load_lds_dwordx4 v[174:175], off
	v_lshl_add_u64 v[174:175], s[24:25], 0, v[164:165]
	s_mov_b32 m0, s28
	s_nop 0
	global_load_lds_dwordx4 v[174:175], off
	v_lshl_add_u64 v[174:175], s[24:25], 0, v[162:163]
	s_add_i32 m0, s28, 0x2000
	s_nop 0
	global_load_lds_dwordx4 v[174:175], off
	v_lshl_add_u64 v[174:175], v[178:179], 0, s[12:13]
	s_mov_b32 m0, s38
	s_nop 0
	global_load_lds_dwordx4 v[174:175], off
	v_lshl_add_u64 v[174:175], v[180:181], 0, s[12:13]
	s_mov_b32 m0, s39
	s_nop 0
	global_load_lds_dwordx4 v[174:175], off
	s_waitcnt vmcnt(8)
	s_waitcnt lgkmcnt(0)
	s_barrier
	s_setprio 1
	s_waitcnt lgkmcnt(0)
	v_mfma_f32_16x16x128_f8f6f4 v[62:65], v[2:9], v[204:211], v[62:65]
	v_mfma_f32_16x16x128_f8f6f4 v[58:61], v[10:17], v[204:211], v[58:61]
	v_mfma_f32_16x16x128_f8f6f4 v[90:93], v[10:17], v[188:195], v[90:93]
	v_mfma_f32_16x16x128_f8f6f4 v[94:97], v[2:9], v[188:195], v[94:97]
	v_mfma_f32_16x16x128_f8f6f4 v[78:81], v[2:9], v[196:203], v[78:81]
	v_mfma_f32_16x16x128_f8f6f4 v[74:77], v[10:17], v[196:203], v[74:77]
	v_mfma_f32_16x16x128_f8f6f4 v[42:45], v[10:17], v[212:219], v[42:45]
	v_mfma_f32_16x16x128_f8f6f4 v[46:49], v[2:9], v[212:219], v[46:49]
	v_mfma_f32_16x16x128_f8f6f4 v[38:41], v[18:25], v[212:219], v[38:41]
	v_mfma_f32_16x16x128_f8f6f4 v[34:37], v[26:33], v[212:219], v[34:37]
	v_mfma_f32_16x16x128_f8f6f4 v[82:85], v[26:33], v[188:195], v[82:85]
	v_mfma_f32_16x16x128_f8f6f4 v[86:89], v[18:25], v[188:195], v[86:89]
	v_mfma_f32_16x16x128_f8f6f4 v[70:73], v[18:25], v[196:203], v[70:73]
	v_mfma_f32_16x16x128_f8f6f4 v[66:69], v[26:33], v[196:203], v[66:69]
	v_mfma_f32_16x16x128_f8f6f4 v[50:53], v[26:33], v[204:211], v[50:53]
	v_mfma_f32_16x16x128_f8f6f4 v[54:57], v[18:25], v[204:211], v[54:57]
	s_setprio 0
	s_barrier
	s_add_i32 s58, s58, 2
	s_add_u32 s26, s26, 0x100
	s_addc_u32 s27, s27, 0
	s_add_u32 s50, s50, 0x100
	s_addc_u32 s51, s51, 0
	s_cmpk_gt_u32 s58, 0x53
	s_cbranch_scc0 .LBB0_318
	s_and_b64 vcc, exec, s[14:15]
	s_cbranch_vccz .LBB0_321
	s_barrier

.LBB0_332:
	s_add_u32 s6, s61, s4
	s_addc_u32 s7, s62, s5
	s_add_u32 s6, s6, 0x32800100
	s_addc_u32 s7, s7, 0
	s_add_u32 s24, s63, s4
	s_addc_u32 s25, s68, s5
	s_add_i32 s64, 0, 0x10000
	s_cmpk_eq_i32 s4, 0x2a00
	s_cselect_b32 s13, s1, s7
	s_cselect_b32 s12, s0, s6
	s_cselect_b32 s7, s29, s25
	s_cselect_b32 s6, s28, s24
	s_add_i32 s65, 0, 0x14000
	v_add_u32_e32 v2, s64, v188
	v_add_u32_e32 v6, s65, v188
	ds_read_b128 v[26:29], v2
	ds_read_b128 v[30:33], v2 offset:1024
	ds_read_b128 v[18:21], v2 offset:2048
	ds_read_b128 v[22:25], v2 offset:3072
	ds_read_b128 v[10:13], v6
	ds_read_b128 v[14:17], v6 offset:1024
	ds_read_b128 v[2:5], v6 offset:2048
	ds_read_b128 v[6:9], v6 offset:3072
	v_lshl_add_u64 v[214:215], v[168:169], 0, s[4:5]
	s_add_i32 m0, s18, 0xc000
	ds_read_b128 v[172:175], v189
	ds_read_b128 v[176:179], v189 offset:1024
	ds_read_b128 v[190:193], v189 offset:2048
	ds_read_b128 v[194:197], v189 offset:3072
	ds_read_b128 v[198:201], v189 offset:4096
	ds_read_b128 v[202:205], v189 offset:5120
	ds_read_b128 v[206:209], v189 offset:6144
	ds_read_b128 v[210:213], v189 offset:7168
	global_load_lds_dwordx4 v[214:215], off
	v_lshl_add_u64 v[214:215], v[170:171], 0, s[4:5]
	s_add_i32 m0, s18, 0xe000
	s_nop 0
	global_load_lds_dwordx4 v[214:215], off
	s_waitcnt vmcnt(8)
	s_waitcnt lgkmcnt(0)
	s_barrier
	s_setprio 1
	s_waitcnt lgkmcnt(0)
	v_mfma_f32_16x16x128_f8f6f4 v[70:73], v[26:33], v[172:179], v[70:73]
	v_mfma_f32_16x16x128_f8f6f4 v[66:69], v[18:25], v[172:179], v[66:69]
	v_mfma_f32_16x16x128_f8f6f4 v[74:77], v[18:25], v[190:197], v[74:77]
	v_mfma_f32_16x16x128_f8f6f4 v[78:81], v[26:33], v[190:197], v[78:81]
	v_mfma_f32_16x16x128_f8f6f4 v[86:89], v[26:33], v[198:205], v[86:89]
	v_mfma_f32_16x16x128_f8f6f4 v[82:85], v[18:25], v[198:205], v[82:85]
	v_mfma_f32_16x16x128_f8f6f4 v[90:93], v[18:25], v[206:213], v[90:93]
	v_mfma_f32_16x16x128_f8f6f4 v[94:97], v[26:33], v[206:213], v[94:97]
	v_mfma_f32_16x16x128_f8f6f4 v[134:137], v[10:17], v[206:213], v[134:137]
	v_mfma_f32_16x16x128_f8f6f4 v[130:133], v[2:9], v[206:213], v[130:133]
	v_mfma_f32_16x16x128_f8f6f4 v[154:157], v[2:9], v[172:179], v[154:157]
	v_mfma_f32_16x16x128_f8f6f4 v[158:161], v[10:17], v[172:179], v[158:161]
	v_mfma_f32_16x16x128_f8f6f4 v[150:153], v[10:17], v[190:197], v[150:153]
	v_mfma_f32_16x16x128_f8f6f4 v[146:149], v[2:9], v[190:197], v[146:149]
	v_mfma_f32_16x16x128_f8f6f4 v[138:141], v[2:9], v[198:205], v[138:141]
	v_mfma_f32_16x16x128_f8f6f4 v[142:145], v[10:17], v[198:205], v[142:145]
	s_setprio 0
	s_barrier
	s_add_i32 s24, s64, s17
	v_lshl_add_u64 v[172:173], s[6:7], 0, v[162:163]
	s_mov_b32 m0, s24
	ds_read_b128 v[190:193], v189 offset:16384
	ds_read_b128 v[194:197], v189 offset:17408
	ds_read_b128 v[198:201], v189 offset:18432
	ds_read_b128 v[202:205], v189 offset:19456
	ds_read_b128 v[206:209], v189 offset:20480
	ds_read_b128 v[210:213], v189 offset:21504
	ds_read_b128 v[214:217], v189 offset:22528
	ds_read_b128 v[218:221], v189 offset:23552
	global_load_lds_dwordx4 v[172:173], off
	s_add_i32 m0, s24, 0x2000
	s_add_u32 s24, s6, 0x158000
	v_lshl_add_u64 v[174:175], s[6:7], 0, v[166:167]
	s_addc_u32 s25, s7, 0
	s_add_i32 s64, s65, s17
	global_load_lds_dwordx4 v[174:175], off
	v_lshl_add_u64 v[176:177], s[24:25], 0, v[162:163]
	s_mov_b32 m0, s64
	v_lshl_add_u64 v[178:179], s[12:13], 0, v[166:167]
	global_load_lds_dwordx4 v[176:177], off
	v_lshl_add_u64 v[176:177], s[24:25], 0, v[166:167]
	s_add_i32 m0, s64, 0x2000
	s_nop 0
	global_load_lds_dwordx4 v[176:177], off
	v_lshl_add_u64 v[176:177], s[12:13], 0, v[162:163]
	s_mov_b32 m0, s18
	s_nop 0
	global_load_lds_dwordx4 v[176:177], off
	s_mov_b32 m0, s19
	s_nop 0
	global_load_lds_dwordx4 v[178:179], off
	s_waitcnt vmcnt(8)
	s_waitcnt lgkmcnt(0)
	s_barrier
	s_setprio 1
	s_waitcnt lgkmcnt(0)
	v_mfma_f32_16x16x128_f8f6f4 v[110:113], v[26:33], v[198:205], v[110:113]
	v_mfma_f32_16x16x128_f8f6f4 v[106:109], v[18:25], v[198:205], v[106:109]
	v_mfma_f32_16x16x128_f8f6f4 v[98:101], v[18:25], v[190:197], v[98:101]
	v_mfma_f32_16x16x128_f8f6f4 v[102:105], v[26:33], v[190:197], v[102:105]
	v_mfma_f32_16x16x128_f8f6f4 v[118:121], v[26:33], v[206:213], v[118:121]
	v_mfma_f32_16x16x128_f8f6f4 v[114:117], v[18:25], v[206:213], v[114:117]
	v_mfma_f32_16x16x128_f8f6f4 v[122:125], v[18:25], v[214:221], v[122:125]
	v_mfma_f32_16x16x128_f8f6f4 v[126:129], v[26:33], v[214:221], v[126:129]
	v_mfma_f32_16x16x128_f8f6f4 v[62:65], v[10:17], v[214:221], v[62:65]
	v_mfma_f32_16x16x128_f8f6f4 v[58:61], v[2:9], v[214:221], v[58:61]
	v_mfma_f32_16x16x128_f8f6f4 v[34:37], v[2:9], v[190:197], v[34:37]
	v_mfma_f32_16x16x128_f8f6f4 v[38:41], v[10:17], v[190:197], v[38:41]
	v_mfma_f32_16x16x128_f8f6f4 v[46:49], v[10:17], v[198:205], v[46:49]
	v_mfma_f32_16x16x128_f8f6f4 v[42:45], v[2:9], v[198:205], v[42:45]
	v_mfma_f32_16x16x128_f8f6f4 v[50:53], v[2:9], v[206:213], v[50:53]
	v_mfma_f32_16x16x128_f8f6f4 v[54:57], v[10:17], v[206:213], v[54:57]
	s_setprio 0
	s_barrier
	s_add_i32 s24, 0, 0x18000
	s_add_i32 s25, 0, 0x1c000
	v_add_u32_e32 v14, s24, v188
	v_add_u32_e32 v30, s25, v188
	ds_read_b128 v[2:5], v14
	ds_read_b128 v[6:9], v14 offset:1024
	ds_read_b128 v[10:13], v14 offset:2048
	ds_read_b128 v[14:17], v14 offset:3072
	ds_read_b128 v[18:21], v30
	ds_read_b128 v[22:25], v30 offset:1024
	ds_read_b128 v[26:29], v30 offset:2048
	ds_read_b128 v[30:33], v30 offset:3072
	s_add_u32 s12, s12, 0x158000
	s_addc_u32 s13, s13, 0
	s_mov_b32 m0, s93
	v_lshl_add_u64 v[222:223], s[12:13], 0, v[162:163]
	ds_read_b128 v[190:193], v189 offset:32768
	ds_read_b128 v[194:197], v189 offset:33792
	ds_read_b128 v[198:201], v189 offset:34816
	ds_read_b128 v[202:205], v189 offset:35840
	ds_read_b128 v[206:209], v189 offset:36864
	ds_read_b128 v[210:213], v189 offset:37888
	ds_read_b128 v[214:217], v189 offset:38912
	ds_read_b128 v[218:221], v189 offset:39936
	global_load_lds_dwordx4 v[222:223], off
	v_lshl_add_u64 v[222:223], s[12:13], 0, v[166:167]
	s_mov_b32 m0, s94
	s_nop 0
	global_load_lds_dwordx4 v[222:223], off
	s_waitcnt vmcnt(8)
	s_waitcnt lgkmcnt(0)
	s_barrier
	s_setprio 1
	s_waitcnt lgkmcnt(0)
	v_mfma_f32_16x16x128_f8f6f4 v[82:85], v[10:17], v[206:213], v[82:85]
	v_mfma_f32_16x16x128_f8f6f4 v[86:89], v[2:9], v[206:213], v[86:89]
	v_mfma_f32_16x16x128_f8f6f4 v[70:73], v[2:9], v[190:197], v[70:73]
	v_mfma_f32_16x16x128_f8f6f4 v[66:69], v[10:17], v[190:197], v[66:69]
	v_mfma_f32_16x16x128_f8f6f4 v[74:77], v[10:17], v[198:205], v[74:77]
	v_mfma_f32_16x16x128_f8f6f4 v[78:81], v[2:9], v[198:205], v[78:81]
	v_mfma_f32_16x16x128_f8f6f4 v[94:97], v[2:9], v[214:221], v[94:97]
	v_mfma_f32_16x16x128_f8f6f4 v[90:93], v[10:17], v[214:221], v[90:93]
	v_mfma_f32_16x16x128_f8f6f4 v[134:137], v[18:25], v[214:221], v[134:137]
	v_mfma_f32_16x16x128_f8f6f4 v[130:133], v[26:33], v[214:221], v[130:133]
	v_mfma_f32_16x16x128_f8f6f4 v[154:157], v[26:33], v[190:197], v[154:157]
	v_mfma_f32_16x16x128_f8f6f4 v[158:161], v[18:25], v[190:197], v[158:161]
	v_mfma_f32_16x16x128_f8f6f4 v[150:153], v[18:25], v[198:205], v[150:153]
	v_mfma_f32_16x16x128_f8f6f4 v[146:149], v[26:33], v[198:205], v[146:149]
	v_mfma_f32_16x16x128_f8f6f4 v[138:141], v[26:33], v[206:213], v[138:141]
	v_mfma_f32_16x16x128_f8f6f4 v[142:145], v[18:25], v[206:213], v[142:145]
	s_setprio 0
	s_barrier
	s_add_i32 s12, s24, s17
	v_lshl_add_u64 v[172:173], v[172:173], 0, s[76:77]
	s_mov_b32 m0, s12
	ds_read_b128 v[190:193], v189 offset:49152
	ds_read_b128 v[194:197], v189 offset:50176
	ds_read_b128 v[198:201], v189 offset:51200
	ds_read_b128 v[202:205], v189 offset:52224
	ds_read_b128 v[206:209], v189 offset:53248
	ds_read_b128 v[210:213], v189 offset:54272
	ds_read_b128 v[214:217], v189 offset:55296
	ds_read_b128 v[218:221], v189 offset:56320
	global_load_lds_dwordx4 v[172:173], off
	s_add_i32 m0, s12, 0x2000
	s_add_u32 s6, s6, 0x158080
	v_lshl_add_u64 v[172:173], v[174:175], 0, s[76:77]
	s_addc_u32 s7, s7, 0
	s_add_i32 s12, s25, s17
	global_load_lds_dwordx4 v[172:173], off
	v_lshl_add_u64 v[172:173], s[6:7], 0, v[162:163]
	s_mov_b32 m0, s12
	s_nop 0
	global_load_lds_dwordx4 v[172:173], off
	v_lshl_add_u64 v[172:173], s[6:7], 0, v[166:167]
	s_add_i32 m0, s12, 0x2000
	s_nop 0
	global_load_lds_dwordx4 v[172:173], off
	v_lshl_add_u64 v[172:173], v[176:177], 0, s[76:77]
	s_mov_b32 m0, s95
	s_nop 0
	global_load_lds_dwordx4 v[172:173], off
	v_lshl_add_u64 v[172:173], v[178:179], 0, s[76:77]
	s_mov_b32 m0, vcc_lo
	s_nop 0
	global_load_lds_dwordx4 v[172:173], off
	s_waitcnt vmcnt(8)
	s_waitcnt lgkmcnt(0)
	s_barrier
	s_setprio 1
	s_waitcnt lgkmcnt(0)
	v_mfma_f32_16x16x128_f8f6f4 v[118:121], v[2:9], v[206:213], v[118:121]
	v_mfma_f32_16x16x128_f8f6f4 v[114:117], v[10:17], v[206:213], v[114:117]
	v_mfma_f32_16x16x128_f8f6f4 v[98:101], v[10:17], v[190:197], v[98:101]
	v_mfma_f32_16x16x128_f8f6f4 v[102:105], v[2:9], v[190:197], v[102:105]
	v_mfma_f32_16x16x128_f8f6f4 v[110:113], v[2:9], v[198:205], v[110:113]
	v_mfma_f32_16x16x128_f8f6f4 v[106:109], v[10:17], v[198:205], v[106:109]
	v_mfma_f32_16x16x128_f8f6f4 v[122:125], v[10:17], v[214:221], v[122:125]
	v_mfma_f32_16x16x128_f8f6f4 v[126:129], v[2:9], v[214:221], v[126:129]
	v_mfma_f32_16x16x128_f8f6f4 v[62:65], v[18:25], v[214:221], v[62:65]
	v_mfma_f32_16x16x128_f8f6f4 v[58:61], v[26:33], v[214:221], v[58:61]
	v_mfma_f32_16x16x128_f8f6f4 v[34:37], v[26:33], v[190:197], v[34:37]
	v_mfma_f32_16x16x128_f8f6f4 v[38:41], v[18:25], v[190:197], v[38:41]
	v_mfma_f32_16x16x128_f8f6f4 v[46:49], v[18:25], v[198:205], v[46:49]
	v_mfma_f32_16x16x128_f8f6f4 v[42:45], v[26:33], v[198:205], v[42:45]
	v_mfma_f32_16x16x128_f8f6f4 v[50:53], v[26:33], v[206:213], v[50:53]
	v_mfma_f32_16x16x128_f8f6f4 v[54:57], v[18:25], v[206:213], v[54:57]
	s_setprio 0
	s_barrier
	s_add_i32 vcc_hi, vcc_hi, 2
	s_add_u32 s4, s4, 0x100
	s_addc_u32 s5, s5, 0
	s_cmpk_lt_u32 vcc_hi, 0x54
	s_cbranch_scc1 .LBB0_332
	s_waitcnt vmcnt(0)
	s_mov_b64 s[12:13], s[54:55]
	s_cmpk_gt_u32 s89, 0xff
	s_cbranch_scc1 .LBB0_335
	s_barrier

.LBB0_758:
	ds_read_b128 v[148:151], v146
	ds_read_b128 v[152:155], v146 offset:1024
	ds_read_b128 v[156:159], v146 offset:2048
	ds_read_b128 v[160:163], v146 offset:3072
	ds_read_b128 v[164:167], v147
	ds_read_b128 v[168:171], v147 offset:1024
	ds_read_b128 v[172:175], v147 offset:2048
	ds_read_b128 v[176:179], v147 offset:3072
	s_add_u32 s16, s42, s14
	s_addc_u32 s17, s43, s15
	s_add_u32 s16, s16, 0x2a800100
	s_addc_u32 s17, s17, 0
	s_add_u32 s60, s48, s14
	s_addc_u32 s61, s49, s15
	s_cmpk_eq_i32 s14, 0x700
	s_cselect_b32 s21, s13, s17
	s_cselect_b32 s20, s12, s16
	s_cselect_b32 s17, s11, s61
	s_cselect_b32 s16, s10, s60
	s_mov_b32 m0, s51
	v_lshl_add_u64 v[212:213], v[138:139], 0, s[14:15]
	ds_read_b128 v[180:183], v145
	ds_read_b128 v[184:187], v145 offset:1024
	ds_read_b128 v[188:191], v145 offset:2048
	ds_read_b128 v[192:195], v145 offset:3072
	ds_read_b128 v[196:199], v145 offset:4096
	ds_read_b128 v[200:203], v145 offset:5120
	ds_read_b128 v[204:207], v145 offset:6144
	ds_read_b128 v[208:211], v145 offset:7168
	global_load_lds_dwordx4 v[212:213], off
	v_lshl_add_u64 v[212:213], v[140:141], 0, s[14:15]
	s_mov_b32 m0, s58
	s_nop 0
	global_load_lds_dwordx4 v[212:213], off
	s_waitcnt vmcnt(8)
	s_waitcnt lgkmcnt(0)
	s_barrier
	s_setprio 1
	s_waitcnt lgkmcnt(0)
	v_mfma_f32_16x16x32_bf16 v[126:129], v[148:151], v[180:183], v[126:129]
	v_mfma_f32_16x16x32_bf16 v[122:125], v[156:159], v[180:183], v[122:125]
	v_mfma_f32_16x16x32_bf16 v[118:121], v[148:151], v[188:191], v[118:121]
	v_mfma_f32_16x16x32_bf16 v[114:117], v[156:159], v[188:191], v[114:117]
	v_mfma_f32_16x16x32_bf16 v[106:109], v[148:151], v[196:199], v[106:109]
	v_mfma_f32_16x16x32_bf16 v[98:101], v[156:159], v[196:199], v[98:101]
	v_mfma_f32_16x16x32_bf16 v[90:93], v[148:151], v[204:207], v[90:93]
	v_mfma_f32_16x16x32_bf16 v[82:85], v[156:159], v[204:207], v[82:85]
	v_mfma_f32_16x16x32_bf16 v[126:129], v[152:155], v[184:187], v[126:129]
	v_mfma_f32_16x16x32_bf16 v[122:125], v[160:163], v[184:187], v[122:125]
	v_mfma_f32_16x16x32_bf16 v[118:121], v[152:155], v[192:195], v[118:121]
	v_mfma_f32_16x16x32_bf16 v[114:117], v[160:163], v[192:195], v[114:117]
	v_mfma_f32_16x16x32_bf16 v[106:109], v[152:155], v[200:203], v[106:109]
	v_mfma_f32_16x16x32_bf16 v[98:101], v[160:163], v[200:203], v[98:101]
	v_mfma_f32_16x16x32_bf16 v[90:93], v[152:155], v[208:211], v[90:93]
	v_mfma_f32_16x16x32_bf16 v[82:85], v[160:163], v[208:211], v[82:85]
	v_mfma_f32_16x16x32_bf16 v[110:113], v[164:167], v[180:183], v[110:113]
	v_mfma_f32_16x16x32_bf16 v[102:105], v[172:175], v[180:183], v[102:105]
	v_mfma_f32_16x16x32_bf16 v[94:97], v[164:167], v[188:191], v[94:97]
	v_mfma_f32_16x16x32_bf16 v[86:89], v[172:175], v[188:191], v[86:89]
	v_mfma_f32_16x16x32_bf16 v[78:81], v[164:167], v[196:199], v[78:81]
	v_mfma_f32_16x16x32_bf16 v[74:77], v[172:175], v[196:199], v[74:77]
	v_mfma_f32_16x16x32_bf16 v[70:73], v[164:167], v[204:207], v[70:73]
	v_mfma_f32_16x16x32_bf16 v[66:69], v[172:175], v[204:207], v[66:69]
	v_mfma_f32_16x16x32_bf16 v[110:113], v[168:171], v[184:187], v[110:113]
	v_mfma_f32_16x16x32_bf16 v[102:105], v[176:179], v[184:187], v[102:105]
	v_mfma_f32_16x16x32_bf16 v[94:97], v[168:171], v[192:195], v[94:97]
	v_mfma_f32_16x16x32_bf16 v[86:89], v[176:179], v[192:195], v[86:89]
	v_mfma_f32_16x16x32_bf16 v[78:81], v[168:171], v[200:203], v[78:81]
	v_mfma_f32_16x16x32_bf16 v[74:77], v[176:179], v[200:203], v[74:77]
	v_mfma_f32_16x16x32_bf16 v[70:73], v[168:171], v[208:211], v[70:73]
	v_mfma_f32_16x16x32_bf16 v[66:69], v[176:179], v[208:211], v[66:69]
	s_setprio 0
	s_barrier
	s_mov_b32 m0, s59
	v_lshl_add_u64 v[212:213], s[16:17], 0, v[130:131]
	ds_read_b128 v[180:183], v145 offset:16384
	ds_read_b128 v[184:187], v145 offset:17408
	ds_read_b128 v[188:191], v145 offset:18432
	ds_read_b128 v[192:195], v145 offset:19456
	ds_read_b128 v[196:199], v145 offset:20480
	ds_read_b128 v[200:203], v145 offset:21504
	ds_read_b128 v[204:207], v145 offset:22528
	ds_read_b128 v[208:211], v145 offset:23552
	global_load_lds_dwordx4 v[212:213], off
	s_add_i32 m0, s59, 0x2000
	s_add_u32 s60, s16, 0x100000
	v_lshl_add_u64 v[214:215], s[16:17], 0, v[136:137]
	s_addc_u32 s61, s17, 0
	s_add_i32 s62, s26, s31
	global_load_lds_dwordx4 v[214:215], off
	v_lshl_add_u64 v[216:217], s[60:61], 0, v[130:131]
	s_mov_b32 m0, s62
	v_lshl_add_u64 v[218:219], s[20:21], 0, v[134:135]
	global_load_lds_dwordx4 v[216:217], off
	v_lshl_add_u64 v[216:217], s[60:61], 0, v[136:137]
	s_add_i32 m0, s62, 0x2000
	s_nop 0
	global_load_lds_dwordx4 v[216:217], off
	v_lshl_add_u64 v[216:217], s[20:21], 0, v[132:133]
	s_mov_b32 m0, s7
	s_nop 0
	global_load_lds_dwordx4 v[216:217], off
	s_mov_b32 m0, s34
	s_nop 0
	global_load_lds_dwordx4 v[218:219], off
	s_waitcnt vmcnt(8)
	s_waitcnt lgkmcnt(0)
	s_barrier
	s_setprio 1
	s_waitcnt lgkmcnt(0)
	v_mfma_f32_16x16x32_bf16 v[62:65], v[148:151], v[180:183], v[62:65]
	v_mfma_f32_16x16x32_bf16 v[58:61], v[156:159], v[180:183], v[58:61]
	v_mfma_f32_16x16x32_bf16 v[54:57], v[148:151], v[188:191], v[54:57]
	v_mfma_f32_16x16x32_bf16 v[50:53], v[156:159], v[188:191], v[50:53]
	v_mfma_f32_16x16x32_bf16 v[42:45], v[148:151], v[196:199], v[42:45]
	v_mfma_f32_16x16x32_bf16 v[34:37], v[156:159], v[196:199], v[34:37]
	v_mfma_f32_16x16x32_bf16 v[26:29], v[148:151], v[204:207], v[26:29]
	v_mfma_f32_16x16x32_bf16 v[18:21], v[156:159], v[204:207], v[18:21]
	v_mfma_f32_16x16x32_bf16 v[62:65], v[152:155], v[184:187], v[62:65]
	v_mfma_f32_16x16x32_bf16 v[58:61], v[160:163], v[184:187], v[58:61]
	v_mfma_f32_16x16x32_bf16 v[54:57], v[152:155], v[192:195], v[54:57]
	v_mfma_f32_16x16x32_bf16 v[50:53], v[160:163], v[192:195], v[50:53]
	v_mfma_f32_16x16x32_bf16 v[42:45], v[152:155], v[200:203], v[42:45]
	v_mfma_f32_16x16x32_bf16 v[34:37], v[160:163], v[200:203], v[34:37]
	v_mfma_f32_16x16x32_bf16 v[26:29], v[152:155], v[208:211], v[26:29]
	v_mfma_f32_16x16x32_bf16 v[18:21], v[160:163], v[208:211], v[18:21]
	v_mfma_f32_16x16x32_bf16 v[46:49], v[164:167], v[180:183], v[46:49]
	v_mfma_f32_16x16x32_bf16 v[38:41], v[172:175], v[180:183], v[38:41]
	v_mfma_f32_16x16x32_bf16 v[30:33], v[164:167], v[188:191], v[30:33]
	v_mfma_f32_16x16x32_bf16 v[22:25], v[172:175], v[188:191], v[22:25]
	v_mfma_f32_16x16x32_bf16 v[14:17], v[164:167], v[196:199], v[14:17]
	v_mfma_f32_16x16x32_bf16 v[10:13], v[172:175], v[196:199], v[10:13]
	v_mfma_f32_16x16x32_bf16 v[6:9], v[164:167], v[204:207], v[6:9]
	v_mfma_f32_16x16x32_bf16 v[2:5], v[172:175], v[204:207], v[2:5]
	v_mfma_f32_16x16x32_bf16 v[46:49], v[168:171], v[184:187], v[46:49]
	v_mfma_f32_16x16x32_bf16 v[38:41], v[176:179], v[184:187], v[38:41]
	v_mfma_f32_16x16x32_bf16 v[30:33], v[168:171], v[192:195], v[30:33]
	v_mfma_f32_16x16x32_bf16 v[22:25], v[176:179], v[192:195], v[22:25]
	v_mfma_f32_16x16x32_bf16 v[14:17], v[168:171], v[200:203], v[14:17]
	v_mfma_f32_16x16x32_bf16 v[10:13], v[176:179], v[200:203], v[10:13]
	v_mfma_f32_16x16x32_bf16 v[6:9], v[168:171], v[208:211], v[6:9]
	v_mfma_f32_16x16x32_bf16 v[2:5], v[176:179], v[208:211], v[2:5]
	s_setprio 0
	s_barrier
	s_add_i32 s60, 0, 0x18000
	s_add_i32 s61, 0, 0x1c000
	v_add_u32_e32 v160, s60, v144
	v_add_u32_e32 v176, s61, v144
	ds_read_b128 v[148:151], v160
	ds_read_b128 v[152:155], v160 offset:1024
	ds_read_b128 v[156:159], v160 offset:2048
	ds_read_b128 v[160:163], v160 offset:3072
	ds_read_b128 v[164:167], v176
	ds_read_b128 v[168:171], v176 offset:1024
	ds_read_b128 v[172:175], v176 offset:2048
	ds_read_b128 v[176:179], v176 offset:3072
	s_add_u32 s20, s20, 0x100000
	s_addc_u32 s21, s21, 0
	s_mov_b32 m0, s35
	v_lshl_add_u64 v[220:221], s[20:21], 0, v[132:133]
	ds_read_b128 v[180:183], v145 offset:32768
	ds_read_b128 v[184:187], v145 offset:33792
	ds_read_b128 v[188:191], v145 offset:34816
	ds_read_b128 v[192:195], v145 offset:35840
	ds_read_b128 v[196:199], v145 offset:36864
	ds_read_b128 v[200:203], v145 offset:37888
	ds_read_b128 v[204:207], v145 offset:38912
	ds_read_b128 v[208:211], v145 offset:39936
	global_load_lds_dwordx4 v[220:221], off
	v_lshl_add_u64 v[220:221], s[20:21], 0, v[134:135]
	s_mov_b32 m0, s38
	s_nop 0
	global_load_lds_dwordx4 v[220:221], off
	s_waitcnt vmcnt(8)
	s_waitcnt lgkmcnt(0)
	s_barrier
	s_setprio 1
	s_waitcnt lgkmcnt(0)
	v_mfma_f32_16x16x32_bf16 v[126:129], v[148:151], v[180:183], v[126:129]
	v_mfma_f32_16x16x32_bf16 v[122:125], v[156:159], v[180:183], v[122:125]
	v_mfma_f32_16x16x32_bf16 v[118:121], v[148:151], v[188:191], v[118:121]
	v_mfma_f32_16x16x32_bf16 v[114:117], v[156:159], v[188:191], v[114:117]
	v_mfma_f32_16x16x32_bf16 v[106:109], v[148:151], v[196:199], v[106:109]
	v_mfma_f32_16x16x32_bf16 v[98:101], v[156:159], v[196:199], v[98:101]
	v_mfma_f32_16x16x32_bf16 v[90:93], v[148:151], v[204:207], v[90:93]
	v_mfma_f32_16x16x32_bf16 v[82:85], v[156:159], v[204:207], v[82:85]
	v_mfma_f32_16x16x32_bf16 v[126:129], v[152:155], v[184:187], v[126:129]
	v_mfma_f32_16x16x32_bf16 v[122:125], v[160:163], v[184:187], v[122:125]
	v_mfma_f32_16x16x32_bf16 v[118:121], v[152:155], v[192:195], v[118:121]
	v_mfma_f32_16x16x32_bf16 v[114:117], v[160:163], v[192:195], v[114:117]
	v_mfma_f32_16x16x32_bf16 v[106:109], v[152:155], v[200:203], v[106:109]
	v_mfma_f32_16x16x32_bf16 v[98:101], v[160:163], v[200:203], v[98:101]
	v_mfma_f32_16x16x32_bf16 v[90:93], v[152:155], v[208:211], v[90:93]
	v_mfma_f32_16x16x32_bf16 v[82:85], v[160:163], v[208:211], v[82:85]
	v_mfma_f32_16x16x32_bf16 v[110:113], v[164:167], v[180:183], v[110:113]
	v_mfma_f32_16x16x32_bf16 v[102:105], v[172:175], v[180:183], v[102:105]
	v_mfma_f32_16x16x32_bf16 v[94:97], v[164:167], v[188:191], v[94:97]
	v_mfma_f32_16x16x32_bf16 v[86:89], v[172:175], v[188:191], v[86:89]
	v_mfma_f32_16x16x32_bf16 v[78:81], v[164:167], v[196:199], v[78:81]
	v_mfma_f32_16x16x32_bf16 v[74:77], v[172:175], v[196:199], v[74:77]
	v_mfma_f32_16x16x32_bf16 v[70:73], v[164:167], v[204:207], v[70:73]
	v_mfma_f32_16x16x32_bf16 v[66:69], v[172:175], v[204:207], v[66:69]
	v_mfma_f32_16x16x32_bf16 v[110:113], v[168:171], v[184:187], v[110:113]
	v_mfma_f32_16x16x32_bf16 v[102:105], v[176:179], v[184:187], v[102:105]
	v_mfma_f32_16x16x32_bf16 v[94:97], v[168:171], v[192:195], v[94:97]
	v_mfma_f32_16x16x32_bf16 v[86:89], v[176:179], v[192:195], v[86:89]
	v_mfma_f32_16x16x32_bf16 v[78:81], v[168:171], v[200:203], v[78:81]
	v_mfma_f32_16x16x32_bf16 v[74:77], v[176:179], v[200:203], v[74:77]
	v_mfma_f32_16x16x32_bf16 v[70:73], v[168:171], v[208:211], v[70:73]
	v_mfma_f32_16x16x32_bf16 v[66:69], v[176:179], v[208:211], v[66:69]
	s_setprio 0
	s_barrier
	s_add_i32 s20, s60, s31
	v_lshl_add_u64 v[212:213], v[212:213], 0, s[4:5]
	s_mov_b32 m0, s20
	ds_read_b128 v[180:183], v145 offset:49152
	ds_read_b128 v[184:187], v145 offset:50176
	ds_read_b128 v[188:191], v145 offset:51200
	ds_read_b128 v[192:195], v145 offset:52224
	ds_read_b128 v[196:199], v145 offset:53248
	ds_read_b128 v[200:203], v145 offset:54272
	ds_read_b128 v[204:207], v145 offset:55296
	ds_read_b128 v[208:211], v145 offset:56320
	global_load_lds_dwordx4 v[212:213], off
	s_add_i32 m0, s20, 0x2000
	s_add_u32 s16, s16, 0x100080
	v_lshl_add_u64 v[212:213], v[214:215], 0, s[4:5]
	s_addc_u32 s17, s17, 0
	s_add_i32 s20, s61, s31
	global_load_lds_dwordx4 v[212:213], off
	v_lshl_add_u64 v[212:213], s[16:17], 0, v[130:131]
	s_mov_b32 m0, s20
	s_nop 0
	global_load_lds_dwordx4 v[212:213], off
	v_lshl_add_u64 v[212:213], s[16:17], 0, v[136:137]
	s_add_i32 m0, s20, 0x2000
	s_nop 0
	global_load_lds_dwordx4 v[212:213], off
	v_lshl_add_u64 v[212:213], v[216:217], 0, s[4:5]
	s_mov_b32 m0, s40
	s_nop 0
	global_load_lds_dwordx4 v[212:213], off
	v_lshl_add_u64 v[212:213], v[218:219], 0, s[4:5]
	s_mov_b32 m0, s41
	s_nop 0
	global_load_lds_dwordx4 v[212:213], off
	s_waitcnt vmcnt(8)
	s_waitcnt lgkmcnt(0)
	s_barrier
	s_setprio 1
	s_waitcnt lgkmcnt(0)
	v_mfma_f32_16x16x32_bf16 v[62:65], v[148:151], v[180:183], v[62:65]
	v_mfma_f32_16x16x32_bf16 v[58:61], v[156:159], v[180:183], v[58:61]
	v_mfma_f32_16x16x32_bf16 v[54:57], v[148:151], v[188:191], v[54:57]
	v_mfma_f32_16x16x32_bf16 v[50:53], v[156:159], v[188:191], v[50:53]
	v_mfma_f32_16x16x32_bf16 v[42:45], v[148:151], v[196:199], v[42:45]
	v_mfma_f32_16x16x32_bf16 v[34:37], v[156:159], v[196:199], v[34:37]
	v_mfma_f32_16x16x32_bf16 v[26:29], v[148:151], v[204:207], v[26:29]
	v_mfma_f32_16x16x32_bf16 v[18:21], v[156:159], v[204:207], v[18:21]
	v_mfma_f32_16x16x32_bf16 v[62:65], v[152:155], v[184:187], v[62:65]
	v_mfma_f32_16x16x32_bf16 v[58:61], v[160:163], v[184:187], v[58:61]
	v_mfma_f32_16x16x32_bf16 v[54:57], v[152:155], v[192:195], v[54:57]
	v_mfma_f32_16x16x32_bf16 v[50:53], v[160:163], v[192:195], v[50:53]
	v_mfma_f32_16x16x32_bf16 v[42:45], v[152:155], v[200:203], v[42:45]
	v_mfma_f32_16x16x32_bf16 v[34:37], v[160:163], v[200:203], v[34:37]
	v_mfma_f32_16x16x32_bf16 v[26:29], v[152:155], v[208:211], v[26:29]
	v_mfma_f32_16x16x32_bf16 v[18:21], v[160:163], v[208:211], v[18:21]
	v_mfma_f32_16x16x32_bf16 v[46:49], v[164:167], v[180:183], v[46:49]
	v_mfma_f32_16x16x32_bf16 v[38:41], v[172:175], v[180:183], v[38:41]
	v_mfma_f32_16x16x32_bf16 v[30:33], v[164:167], v[188:191], v[30:33]
	v_mfma_f32_16x16x32_bf16 v[22:25], v[172:175], v[188:191], v[22:25]
	v_mfma_f32_16x16x32_bf16 v[14:17], v[164:167], v[196:199], v[14:17]
	v_mfma_f32_16x16x32_bf16 v[10:13], v[172:175], v[196:199], v[10:13]
	v_mfma_f32_16x16x32_bf16 v[6:9], v[164:167], v[204:207], v[6:9]
	v_mfma_f32_16x16x32_bf16 v[2:5], v[172:175], v[204:207], v[2:5]
	v_mfma_f32_16x16x32_bf16 v[46:49], v[168:171], v[184:187], v[46:49]
	v_mfma_f32_16x16x32_bf16 v[38:41], v[176:179], v[184:187], v[38:41]
	v_mfma_f32_16x16x32_bf16 v[30:33], v[168:171], v[192:195], v[30:33]
	v_mfma_f32_16x16x32_bf16 v[22:25], v[176:179], v[192:195], v[22:25]
	v_mfma_f32_16x16x32_bf16 v[14:17], v[168:171], v[200:203], v[14:17]
	v_mfma_f32_16x16x32_bf16 v[10:13], v[176:179], v[200:203], v[10:13]
	v_mfma_f32_16x16x32_bf16 v[6:9], v[168:171], v[208:211], v[6:9]
	v_mfma_f32_16x16x32_bf16 v[2:5], v[176:179], v[208:211], v[2:5]
	s_setprio 0
	s_barrier
	s_add_i32 s50, s50, 2
	s_add_u32 s14, s14, 0x100
	s_addc_u32 s15, s15, 0
	s_cmp_gt_u32 s50, 13
	s_cbranch_scc0 .LBB0_758
	s_cmpk_lt_u32 s30, 0x100
	s_cbranch_scc0 .LBB0_754
	s_barrier
	s_branch .LBB0_754

.LBB0_768:
	ds_read_b128 v[130:133], v1
	ds_read_b128 v[134:137], v1 offset:1024
	ds_read_b128 v[138:141], v1 offset:2048
	ds_read_b128 v[142:145], v1 offset:3072
	ds_read_b128 v[180:183], v176
	ds_read_b128 v[184:187], v176 offset:1024
	ds_read_b128 v[188:191], v176 offset:2048
	ds_read_b128 v[192:195], v176 offset:3072
	s_add_u32 s1, s16, 0xfff00080
	s_addc_u32 s20, s17, -1
	s_add_u32 s49, s16, 0xdb300080
	s_addc_u32 s21, s17, -1
	s_cmp_eq_u32 s0, 60
	s_cselect_b32 s25, s55, s20
	s_cselect_b32 s24, s54, s1
	s_cselect_b32 s21, s9, s21
	s_cselect_b32 s20, s8, s49
	s_mov_b32 m0, s35
	v_lshl_add_u64 v[228:229], s[16:17], 0, v[172:173]
	ds_read_b128 v[196:199], v177
	ds_read_b128 v[200:203], v177 offset:1024
	ds_read_b128 v[204:207], v177 offset:2048
	ds_read_b128 v[208:211], v177 offset:3072
	ds_read_b128 v[212:215], v177 offset:4096
	ds_read_b128 v[216:219], v177 offset:5120
	ds_read_b128 v[220:223], v177 offset:6144
	ds_read_b128 v[224:227], v177 offset:7168
	global_load_lds_dwordx4 v[228:229], off
	v_lshl_add_u64 v[228:229], s[16:17], 0, v[174:175]
	s_mov_b32 m0, s36
	s_nop 0
	global_load_lds_dwordx4 v[228:229], off
	s_waitcnt vmcnt(8)
	s_waitcnt lgkmcnt(0)
	s_barrier
	s_setprio 1
	s_waitcnt lgkmcnt(0)
	v_mfma_f32_16x16x32_bf16 v[126:129], v[130:133], v[196:199], v[126:129]
	v_mfma_f32_16x16x32_bf16 v[122:125], v[138:141], v[196:199], v[122:125]
	v_mfma_f32_16x16x32_bf16 v[114:117], v[130:133], v[204:207], v[114:117]
	v_mfma_f32_16x16x32_bf16 v[106:109], v[138:141], v[204:207], v[106:109]
	v_mfma_f32_16x16x32_bf16 v[98:101], v[130:133], v[212:215], v[98:101]
	v_mfma_f32_16x16x32_bf16 v[90:93], v[138:141], v[212:215], v[90:93]
	v_mfma_f32_16x16x32_bf16 v[82:85], v[130:133], v[220:223], v[82:85]
	v_mfma_f32_16x16x32_bf16 v[74:77], v[138:141], v[220:223], v[74:77]
	v_mfma_f32_16x16x32_bf16 v[126:129], v[134:137], v[200:203], v[126:129]
	v_mfma_f32_16x16x32_bf16 v[122:125], v[142:145], v[200:203], v[122:125]
	v_mfma_f32_16x16x32_bf16 v[114:117], v[134:137], v[208:211], v[114:117]
	v_mfma_f32_16x16x32_bf16 v[106:109], v[142:145], v[208:211], v[106:109]
	v_mfma_f32_16x16x32_bf16 v[98:101], v[134:137], v[216:219], v[98:101]
	v_mfma_f32_16x16x32_bf16 v[90:93], v[142:145], v[216:219], v[90:93]
	v_mfma_f32_16x16x32_bf16 v[82:85], v[134:137], v[224:227], v[82:85]
	v_mfma_f32_16x16x32_bf16 v[74:77], v[142:145], v[224:227], v[74:77]
	v_mfma_f32_16x16x32_bf16 v[118:121], v[180:183], v[196:199], v[118:121]
	v_mfma_f32_16x16x32_bf16 v[110:113], v[188:191], v[196:199], v[110:113]
	v_mfma_f32_16x16x32_bf16 v[102:105], v[180:183], v[204:207], v[102:105]
	v_mfma_f32_16x16x32_bf16 v[94:97], v[188:191], v[204:207], v[94:97]
	v_mfma_f32_16x16x32_bf16 v[86:89], v[180:183], v[212:215], v[86:89]
	v_mfma_f32_16x16x32_bf16 v[78:81], v[188:191], v[212:215], v[78:81]
	v_mfma_f32_16x16x32_bf16 v[70:73], v[180:183], v[220:223], v[70:73]
	v_mfma_f32_16x16x32_bf16 v[66:69], v[188:191], v[220:223], v[66:69]
	v_mfma_f32_16x16x32_bf16 v[118:121], v[184:187], v[200:203], v[118:121]
	v_mfma_f32_16x16x32_bf16 v[110:113], v[192:195], v[200:203], v[110:113]
	v_mfma_f32_16x16x32_bf16 v[102:105], v[184:187], v[208:211], v[102:105]
	v_mfma_f32_16x16x32_bf16 v[94:97], v[192:195], v[208:211], v[94:97]
	v_mfma_f32_16x16x32_bf16 v[86:89], v[184:187], v[216:219], v[86:89]
	v_mfma_f32_16x16x32_bf16 v[78:81], v[192:195], v[216:219], v[78:81]
	v_mfma_f32_16x16x32_bf16 v[70:73], v[184:187], v[224:227], v[70:73]
	v_mfma_f32_16x16x32_bf16 v[66:69], v[192:195], v[224:227], v[66:69]
	s_setprio 0
	s_barrier
	s_mov_b32 m0, s37
	v_lshl_add_u64 v[228:229], s[20:21], 0, v[150:151]
	s_add_u32 s50, s20, 0x100000
	ds_read_b128 v[196:199], v177 offset:16384
	ds_read_b128 v[200:203], v177 offset:17408
	ds_read_b128 v[204:207], v177 offset:18432
	ds_read_b128 v[208:211], v177 offset:19456
	ds_read_b128 v[212:215], v177 offset:20480
	ds_read_b128 v[216:219], v177 offset:21504
	ds_read_b128 v[220:223], v177 offset:22528
	ds_read_b128 v[224:227], v177 offset:23552
	global_load_lds_dwordx4 v[228:229], off
	v_lshl_add_u64 v[230:231], s[20:21], 0, v[146:147]
	s_mov_b32 m0, s38
	s_addc_u32 s51, s21, 0
	global_load_lds_dwordx4 v[230:231], off
	v_lshl_add_u64 v[232:233], s[50:51], 0, v[150:151]
	s_mov_b32 m0, s39
	v_lshl_add_u64 v[234:235], s[24:25], 0, v[148:149]
	global_load_lds_dwordx4 v[232:233], off
	v_lshl_add_u64 v[232:233], s[50:51], 0, v[146:147]
	s_mov_b32 m0, s40
	s_nop 0
	global_load_lds_dwordx4 v[232:233], off
	v_lshl_add_u64 v[232:233], s[24:25], 0, v[152:153]
	s_mov_b32 m0, s26
	s_nop 0
	global_load_lds_dwordx4 v[232:233], off
	s_mov_b32 m0, s27
	s_nop 0
	global_load_lds_dwordx4 v[234:235], off
	s_waitcnt vmcnt(8)
	s_waitcnt lgkmcnt(0)
	s_barrier
	s_setprio 1
	s_waitcnt lgkmcnt(0)
	v_mfma_f32_16x16x32_bf16 v[62:65], v[130:133], v[196:199], v[62:65]
	v_mfma_f32_16x16x32_bf16 v[58:61], v[138:141], v[196:199], v[58:61]
	v_mfma_f32_16x16x32_bf16 v[50:53], v[130:133], v[204:207], v[50:53]
	v_mfma_f32_16x16x32_bf16 v[42:45], v[138:141], v[204:207], v[42:45]
	v_mfma_f32_16x16x32_bf16 v[34:37], v[130:133], v[212:215], v[34:37]
	v_mfma_f32_16x16x32_bf16 v[26:29], v[138:141], v[212:215], v[26:29]
	v_mfma_f32_16x16x32_bf16 v[18:21], v[130:133], v[220:223], v[18:21]
	v_mfma_f32_16x16x32_bf16 v[10:13], v[138:141], v[220:223], v[10:13]
	v_mfma_f32_16x16x32_bf16 v[62:65], v[134:137], v[200:203], v[62:65]
	v_mfma_f32_16x16x32_bf16 v[58:61], v[142:145], v[200:203], v[58:61]
	v_mfma_f32_16x16x32_bf16 v[50:53], v[134:137], v[208:211], v[50:53]
	v_mfma_f32_16x16x32_bf16 v[42:45], v[142:145], v[208:211], v[42:45]
	v_mfma_f32_16x16x32_bf16 v[34:37], v[134:137], v[216:219], v[34:37]
	v_mfma_f32_16x16x32_bf16 v[26:29], v[142:145], v[216:219], v[26:29]
	v_mfma_f32_16x16x32_bf16 v[18:21], v[134:137], v[224:227], v[18:21]
	v_mfma_f32_16x16x32_bf16 v[10:13], v[142:145], v[224:227], v[10:13]
	v_mfma_f32_16x16x32_bf16 v[54:57], v[180:183], v[196:199], v[54:57]
	v_mfma_f32_16x16x32_bf16 v[46:49], v[188:191], v[196:199], v[46:49]
	v_mfma_f32_16x16x32_bf16 v[38:41], v[180:183], v[204:207], v[38:41]
	v_mfma_f32_16x16x32_bf16 v[30:33], v[188:191], v[204:207], v[30:33]
	v_mfma_f32_16x16x32_bf16 v[22:25], v[180:183], v[212:215], v[22:25]
	v_mfma_f32_16x16x32_bf16 v[14:17], v[188:191], v[212:215], v[14:17]
	v_mfma_f32_16x16x32_bf16 v[6:9], v[180:183], v[220:223], v[6:9]
	v_mfma_f32_16x16x32_bf16 v[2:5], v[188:191], v[220:223], v[2:5]
	v_mfma_f32_16x16x32_bf16 v[54:57], v[184:187], v[200:203], v[54:57]
	v_mfma_f32_16x16x32_bf16 v[46:49], v[192:195], v[200:203], v[46:49]
	v_mfma_f32_16x16x32_bf16 v[38:41], v[184:187], v[208:211], v[38:41]
	v_mfma_f32_16x16x32_bf16 v[30:33], v[192:195], v[208:211], v[30:33]
	v_mfma_f32_16x16x32_bf16 v[22:25], v[184:187], v[216:219], v[22:25]
	v_mfma_f32_16x16x32_bf16 v[14:17], v[192:195], v[216:219], v[14:17]
	v_mfma_f32_16x16x32_bf16 v[6:9], v[184:187], v[224:227], v[6:9]
	v_mfma_f32_16x16x32_bf16 v[2:5], v[192:195], v[224:227], v[2:5]
	s_setprio 0
	s_barrier
	ds_read_b128 v[130:133], v178
	ds_read_b128 v[134:137], v178 offset:1024
	ds_read_b128 v[138:141], v178 offset:2048
	ds_read_b128 v[142:145], v178 offset:3072
	ds_read_b128 v[180:183], v179
	ds_read_b128 v[184:187], v179 offset:1024
	ds_read_b128 v[188:191], v179 offset:2048
	ds_read_b128 v[192:195], v179 offset:3072
	s_add_u32 s24, s24, 0x100000
	s_addc_u32 s25, s25, 0
	s_mov_b32 m0, s28
	v_lshl_add_u64 v[236:237], s[24:25], 0, v[152:153]
	ds_read_b128 v[196:199], v177 offset:32768
	ds_read_b128 v[200:203], v177 offset:33792
	ds_read_b128 v[204:207], v177 offset:34816
	ds_read_b128 v[208:211], v177 offset:35840
	ds_read_b128 v[212:215], v177 offset:36864
	ds_read_b128 v[216:219], v177 offset:37888
	ds_read_b128 v[220:223], v177 offset:38912
	ds_read_b128 v[224:227], v177 offset:39936
	global_load_lds_dwordx4 v[236:237], off
	v_lshl_add_u64 v[236:237], s[24:25], 0, v[148:149]
	s_mov_b32 m0, s29
	s_nop 0
	global_load_lds_dwordx4 v[236:237], off
	s_waitcnt vmcnt(8)
	s_waitcnt lgkmcnt(0)
	s_barrier
	s_setprio 1
	s_waitcnt lgkmcnt(0)
	v_mfma_f32_16x16x32_bf16 v[126:129], v[130:133], v[196:199], v[126:129]
	v_mfma_f32_16x16x32_bf16 v[122:125], v[138:141], v[196:199], v[122:125]
	v_mfma_f32_16x16x32_bf16 v[114:117], v[130:133], v[204:207], v[114:117]
	v_mfma_f32_16x16x32_bf16 v[106:109], v[138:141], v[204:207], v[106:109]
	v_mfma_f32_16x16x32_bf16 v[98:101], v[130:133], v[212:215], v[98:101]
	v_mfma_f32_16x16x32_bf16 v[90:93], v[138:141], v[212:215], v[90:93]
	v_mfma_f32_16x16x32_bf16 v[82:85], v[130:133], v[220:223], v[82:85]
	v_mfma_f32_16x16x32_bf16 v[74:77], v[138:141], v[220:223], v[74:77]
	v_mfma_f32_16x16x32_bf16 v[126:129], v[134:137], v[200:203], v[126:129]
	v_mfma_f32_16x16x32_bf16 v[122:125], v[142:145], v[200:203], v[122:125]
	v_mfma_f32_16x16x32_bf16 v[114:117], v[134:137], v[208:211], v[114:117]
	v_mfma_f32_16x16x32_bf16 v[106:109], v[142:145], v[208:211], v[106:109]
	v_mfma_f32_16x16x32_bf16 v[98:101], v[134:137], v[216:219], v[98:101]
	v_mfma_f32_16x16x32_bf16 v[90:93], v[142:145], v[216:219], v[90:93]
	v_mfma_f32_16x16x32_bf16 v[82:85], v[134:137], v[224:227], v[82:85]
	v_mfma_f32_16x16x32_bf16 v[74:77], v[142:145], v[224:227], v[74:77]
	v_mfma_f32_16x16x32_bf16 v[118:121], v[180:183], v[196:199], v[118:121]
	v_mfma_f32_16x16x32_bf16 v[110:113], v[188:191], v[196:199], v[110:113]
	v_mfma_f32_16x16x32_bf16 v[102:105], v[180:183], v[204:207], v[102:105]
	v_mfma_f32_16x16x32_bf16 v[94:97], v[188:191], v[204:207], v[94:97]
	v_mfma_f32_16x16x32_bf16 v[86:89], v[180:183], v[212:215], v[86:89]
	v_mfma_f32_16x16x32_bf16 v[78:81], v[188:191], v[212:215], v[78:81]
	v_mfma_f32_16x16x32_bf16 v[70:73], v[180:183], v[220:223], v[70:73]
	v_mfma_f32_16x16x32_bf16 v[66:69], v[188:191], v[220:223], v[66:69]
	v_mfma_f32_16x16x32_bf16 v[118:121], v[184:187], v[200:203], v[118:121]
	v_mfma_f32_16x16x32_bf16 v[110:113], v[192:195], v[200:203], v[110:113]
	v_mfma_f32_16x16x32_bf16 v[102:105], v[184:187], v[208:211], v[102:105]
	v_mfma_f32_16x16x32_bf16 v[94:97], v[192:195], v[208:211], v[94:97]
	v_mfma_f32_16x16x32_bf16 v[86:89], v[184:187], v[216:219], v[86:89]
	v_mfma_f32_16x16x32_bf16 v[78:81], v[192:195], v[216:219], v[78:81]
	v_mfma_f32_16x16x32_bf16 v[70:73], v[184:187], v[224:227], v[70:73]
	v_mfma_f32_16x16x32_bf16 v[66:69], v[192:195], v[224:227], v[66:69]
	s_setprio 0
	s_barrier
	s_mov_b32 m0, s41
	v_lshl_add_u64 v[228:229], v[228:229], 0, s[14:15]
	s_add_u32 s20, s20, 0x100080
	ds_read_b128 v[196:199], v177 offset:49152
	ds_read_b128 v[200:203], v177 offset:50176
	ds_read_b128 v[204:207], v177 offset:51200
	ds_read_b128 v[208:211], v177 offset:52224
	ds_read_b128 v[212:215], v177 offset:53248
	ds_read_b128 v[216:219], v177 offset:54272
	ds_read_b128 v[220:223], v177 offset:55296
	ds_read_b128 v[224:227], v177 offset:56320
	global_load_lds_dwordx4 v[228:229], off
	v_lshl_add_u64 v[228:229], v[230:231], 0, s[14:15]
	s_mov_b32 m0, s42
	s_addc_u32 s21, s21, 0
	global_load_lds_dwordx4 v[228:229], off
	v_lshl_add_u64 v[228:229], s[20:21], 0, v[150:151]
	s_mov_b32 m0, s43
	s_nop 0
	global_load_lds_dwordx4 v[228:229], off
	v_lshl_add_u64 v[228:229], s[20:21], 0, v[146:147]
	s_mov_b32 m0, s48
	s_nop 0
	global_load_lds_dwordx4 v[228:229], off
	v_lshl_add_u64 v[228:229], v[232:233], 0, s[14:15]
	s_mov_b32 m0, s31
	s_nop 0
	global_load_lds_dwordx4 v[228:229], off
	v_lshl_add_u64 v[228:229], v[234:235], 0, s[14:15]
	s_mov_b32 m0, s34
	s_nop 0
	global_load_lds_dwordx4 v[228:229], off
	s_waitcnt vmcnt(8)
	s_waitcnt lgkmcnt(0)
	s_barrier
	s_setprio 1
	s_waitcnt lgkmcnt(0)
	v_mfma_f32_16x16x32_bf16 v[62:65], v[130:133], v[196:199], v[62:65]
	v_mfma_f32_16x16x32_bf16 v[58:61], v[138:141], v[196:199], v[58:61]
	v_mfma_f32_16x16x32_bf16 v[50:53], v[130:133], v[204:207], v[50:53]
	v_mfma_f32_16x16x32_bf16 v[42:45], v[138:141], v[204:207], v[42:45]
	v_mfma_f32_16x16x32_bf16 v[34:37], v[130:133], v[212:215], v[34:37]
	v_mfma_f32_16x16x32_bf16 v[26:29], v[138:141], v[212:215], v[26:29]
	v_mfma_f32_16x16x32_bf16 v[18:21], v[130:133], v[220:223], v[18:21]
	v_mfma_f32_16x16x32_bf16 v[10:13], v[138:141], v[220:223], v[10:13]
	v_mfma_f32_16x16x32_bf16 v[62:65], v[134:137], v[200:203], v[62:65]
	v_mfma_f32_16x16x32_bf16 v[58:61], v[142:145], v[200:203], v[58:61]
	v_mfma_f32_16x16x32_bf16 v[50:53], v[134:137], v[208:211], v[50:53]
	v_mfma_f32_16x16x32_bf16 v[42:45], v[142:145], v[208:211], v[42:45]
	v_mfma_f32_16x16x32_bf16 v[34:37], v[134:137], v[216:219], v[34:37]
	v_mfma_f32_16x16x32_bf16 v[26:29], v[142:145], v[216:219], v[26:29]
	v_mfma_f32_16x16x32_bf16 v[18:21], v[134:137], v[224:227], v[18:21]
	v_mfma_f32_16x16x32_bf16 v[10:13], v[142:145], v[224:227], v[10:13]
	v_mfma_f32_16x16x32_bf16 v[54:57], v[180:183], v[196:199], v[54:57]
	v_mfma_f32_16x16x32_bf16 v[46:49], v[188:191], v[196:199], v[46:49]
	v_mfma_f32_16x16x32_bf16 v[38:41], v[180:183], v[204:207], v[38:41]
	v_mfma_f32_16x16x32_bf16 v[30:33], v[188:191], v[204:207], v[30:33]
	v_mfma_f32_16x16x32_bf16 v[22:25], v[180:183], v[212:215], v[22:25]
	v_mfma_f32_16x16x32_bf16 v[14:17], v[188:191], v[212:215], v[14:17]
	v_mfma_f32_16x16x32_bf16 v[6:9], v[180:183], v[220:223], v[6:9]
	v_mfma_f32_16x16x32_bf16 v[2:5], v[188:191], v[220:223], v[2:5]
	v_mfma_f32_16x16x32_bf16 v[54:57], v[184:187], v[200:203], v[54:57]
	v_mfma_f32_16x16x32_bf16 v[46:49], v[192:195], v[200:203], v[46:49]
	v_mfma_f32_16x16x32_bf16 v[38:41], v[184:187], v[208:211], v[38:41]
	v_mfma_f32_16x16x32_bf16 v[30:33], v[192:195], v[208:211], v[30:33]
	v_mfma_f32_16x16x32_bf16 v[22:25], v[184:187], v[216:219], v[22:25]
	v_mfma_f32_16x16x32_bf16 v[14:17], v[192:195], v[216:219], v[14:17]
	v_mfma_f32_16x16x32_bf16 v[6:9], v[184:187], v[224:227], v[6:9]
	v_mfma_f32_16x16x32_bf16 v[2:5], v[192:195], v[224:227], v[2:5]
	s_setprio 0
	s_barrier
	s_add_i32 s0, s0, 2
	s_add_u32 s16, s16, 0x100
	s_addc_u32 s17, s17, 0
	s_cmp_gt_u32 s0, 61
	s_cbranch_scc0 .LBB0_768
	s_and_b64 vcc, exec, s[10:11]
	s_cbranch_vccz .LBB0_771
	s_barrier

.LBB0_788:
	v_add_u32_e32 v130, s15, v190
	v_add_u32_e32 v134, s50, v190
	ds_read_b128 v[158:161], v130
	ds_read_b128 v[150:153], v130 offset:1024
	ds_read_b128 v[154:157], v130 offset:2048
	ds_read_b128 v[146:149], v130 offset:3072
	ds_read_b128 v[142:145], v134
	ds_read_b128 v[130:133], v134 offset:1024
	ds_read_b128 v[138:141], v134 offset:2048
	ds_read_b128 v[134:137], v134 offset:3072
	s_add_u32 s36, s34, 0xfff80080
	s_addc_u32 s37, s35, -1
	s_and_b64 s[0:1], s[0:1], exec
	s_cselect_b32 s39, s21, s37
	s_cselect_b32 s38, s60, s36
	s_cselect_b32 s37, s17, s63
	s_cselect_b32 s36, s61, s62
	s_add_i32 m0, s29, 0xc000
	ds_read_b128 v[182:185], v193
	ds_read_b128 v[186:189], v193 offset:1024
	ds_read_b128 v[194:197], v193 offset:2048
	ds_read_b128 v[198:201], v193 offset:3072
	ds_read_b128 v[202:205], v193 offset:4096
	ds_read_b128 v[206:209], v193 offset:5120
	ds_read_b128 v[210:213], v193 offset:6144
	ds_read_b128 v[214:217], v193 offset:7168
	global_load_lds_dwordx4 v172, s[34:35]
	s_add_i32 m0, s29, 0xe000
	s_nop 0
	global_load_lds_dwordx4 v174, s[34:35]
	s_waitcnt vmcnt(8)
	s_waitcnt lgkmcnt(0)
	s_barrier
	s_setprio 1
	s_waitcnt lgkmcnt(0)
	v_mfma_i32_16x16x64_i8 v[126:129], v[158:161], v[182:185], v[126:129]
	v_mfma_i32_16x16x64_i8 v[122:125], v[154:157], v[182:185], v[122:125]
	v_mfma_i32_16x16x64_i8 v[106:109], v[154:157], v[194:197], v[106:109]
	v_mfma_i32_16x16x64_i8 v[114:117], v[158:161], v[194:197], v[114:117]
	v_mfma_i32_16x16x64_i8 v[98:101], v[158:161], v[202:205], v[98:101]
	v_mfma_i32_16x16x64_i8 v[90:93], v[154:157], v[202:205], v[90:93]
	v_mfma_i32_16x16x64_i8 v[74:77], v[154:157], v[210:213], v[74:77]
	v_mfma_i32_16x16x64_i8 v[82:85], v[158:161], v[210:213], v[82:85]
	s_nop 0
	v_mfma_i32_16x16x64_i8 v[126:129], v[150:153], v[186:189], v[126:129]
	v_mfma_i32_16x16x64_i8 v[122:125], v[146:149], v[186:189], v[122:125]
	v_mfma_i32_16x16x64_i8 v[106:109], v[146:149], v[198:201], v[106:109]
	v_mfma_i32_16x16x64_i8 v[114:117], v[150:153], v[198:201], v[114:117]
	v_mfma_i32_16x16x64_i8 v[98:101], v[150:153], v[206:209], v[98:101]
	v_mfma_i32_16x16x64_i8 v[90:93], v[146:149], v[206:209], v[90:93]
	v_mfma_i32_16x16x64_i8 v[74:77], v[146:149], v[214:217], v[74:77]
	v_mfma_i32_16x16x64_i8 v[82:85], v[150:153], v[214:217], v[82:85]
	v_mfma_i32_16x16x64_i8 v[118:121], v[142:145], v[182:185], v[118:121]
	v_mfma_i32_16x16x64_i8 v[110:113], v[138:141], v[182:185], v[110:113]
	v_mfma_i32_16x16x64_i8 v[94:97], v[138:141], v[194:197], v[94:97]
	v_mfma_i32_16x16x64_i8 v[102:105], v[142:145], v[194:197], v[102:105]
	v_mfma_i32_16x16x64_i8 v[86:89], v[142:145], v[202:205], v[86:89]
	v_mfma_i32_16x16x64_i8 v[78:81], v[138:141], v[202:205], v[78:81]
	v_mfma_i32_16x16x64_i8 v[66:69], v[138:141], v[210:213], v[66:69]
	v_mfma_i32_16x16x64_i8 v[70:73], v[142:145], v[210:213], v[70:73]
	s_nop 0
	v_mfma_i32_16x16x64_i8 v[118:121], v[130:133], v[186:189], v[118:121]
	v_mfma_i32_16x16x64_i8 v[110:113], v[134:137], v[186:189], v[110:113]
	v_mfma_i32_16x16x64_i8 v[94:97], v[134:137], v[198:201], v[94:97]
	v_mfma_i32_16x16x64_i8 v[102:105], v[130:133], v[198:201], v[102:105]
	v_mfma_i32_16x16x64_i8 v[86:89], v[130:133], v[206:209], v[86:89]
	v_mfma_i32_16x16x64_i8 v[78:81], v[134:137], v[206:209], v[78:81]
	v_mfma_i32_16x16x64_i8 v[66:69], v[134:137], v[214:217], v[66:69]
	v_mfma_i32_16x16x64_i8 v[70:73], v[130:133], v[214:217], v[70:73]
	s_setprio 0
	s_barrier
	s_add_i32 s0, s15, s40
	s_mov_b32 m0, s0
	ds_read_b128 v[194:197], v193 offset:16384
	ds_read_b128 v[198:201], v193 offset:17408
	ds_read_b128 v[202:205], v193 offset:18432
	ds_read_b128 v[206:209], v193 offset:19456
	ds_read_b128 v[210:213], v193 offset:20480
	ds_read_b128 v[214:217], v193 offset:21504
	ds_read_b128 v[218:221], v193 offset:22528
	ds_read_b128 v[222:225], v193 offset:23552
	global_load_lds_dwordx4 v164, s[36:37]
	s_add_i32 m0, s0, 0x2000
	s_add_u32 s0, s36, 0x80000
	s_addc_u32 s1, s37, 0
	s_add_i32 s66, s50, s40
	global_load_lds_dwordx4 v168, s[36:37]
	s_mov_b32 m0, s66
	s_nop 0
	global_load_lds_dwordx4 v164, s[0:1]
	s_add_i32 m0, s66, 0x2000
	s_nop 0
	global_load_lds_dwordx4 v168, s[0:1]
	s_mov_b32 m0, s29
	s_nop 0
	global_load_lds_dwordx4 v162, s[38:39]
	s_mov_b32 m0, s31
	s_nop 0
	global_load_lds_dwordx4 v166, s[38:39]
	s_waitcnt vmcnt(8)
	s_waitcnt lgkmcnt(0)
	s_barrier
	s_setprio 1
	s_waitcnt lgkmcnt(0)
	v_mfma_i32_16x16x64_i8 v[62:65], v[158:161], v[194:197], v[62:65]
	v_mfma_i32_16x16x64_i8 v[58:61], v[154:157], v[194:197], v[58:61]
	v_mfma_i32_16x16x64_i8 v[42:45], v[154:157], v[202:205], v[42:45]
	v_mfma_i32_16x16x64_i8 v[50:53], v[158:161], v[202:205], v[50:53]
	v_mfma_i32_16x16x64_i8 v[34:37], v[158:161], v[210:213], v[34:37]
	v_mfma_i32_16x16x64_i8 v[26:29], v[154:157], v[210:213], v[26:29]
	v_mfma_i32_16x16x64_i8 v[10:13], v[154:157], v[218:221], v[10:13]
	v_mfma_i32_16x16x64_i8 v[18:21], v[158:161], v[218:221], v[18:21]
	s_nop 0
	v_mfma_i32_16x16x64_i8 v[62:65], v[150:153], v[198:201], v[62:65]
	v_mfma_i32_16x16x64_i8 v[58:61], v[146:149], v[198:201], v[58:61]
	v_mfma_i32_16x16x64_i8 v[42:45], v[146:149], v[206:209], v[42:45]
	v_mfma_i32_16x16x64_i8 v[50:53], v[150:153], v[206:209], v[50:53]
	v_mfma_i32_16x16x64_i8 v[34:37], v[150:153], v[214:217], v[34:37]
	v_mfma_i32_16x16x64_i8 v[26:29], v[146:149], v[214:217], v[26:29]
	v_mfma_i32_16x16x64_i8 v[10:13], v[146:149], v[222:225], v[10:13]
	v_mfma_i32_16x16x64_i8 v[18:21], v[150:153], v[222:225], v[18:21]
	v_mfma_i32_16x16x64_i8 v[54:57], v[142:145], v[194:197], v[54:57]
	v_mfma_i32_16x16x64_i8 v[46:49], v[138:141], v[194:197], v[46:49]
	v_mfma_i32_16x16x64_i8 v[30:33], v[138:141], v[202:205], v[30:33]
	v_mfma_i32_16x16x64_i8 v[38:41], v[142:145], v[202:205], v[38:41]
	v_mfma_i32_16x16x64_i8 v[22:25], v[142:145], v[210:213], v[22:25]
	v_mfma_i32_16x16x64_i8 v[14:17], v[138:141], v[210:213], v[14:17]
	v_mfma_i32_16x16x64_i8 v[2:5], v[138:141], v[218:221], v[2:5]
	v_mfma_i32_16x16x64_i8 v[6:9], v[142:145], v[218:221], v[6:9]
	s_nop 0
	v_mfma_i32_16x16x64_i8 v[54:57], v[130:133], v[198:201], v[54:57]
	v_mfma_i32_16x16x64_i8 v[46:49], v[134:137], v[198:201], v[46:49]
	v_mfma_i32_16x16x64_i8 v[30:33], v[134:137], v[206:209], v[30:33]
	v_mfma_i32_16x16x64_i8 v[38:41], v[130:133], v[206:209], v[38:41]
	v_mfma_i32_16x16x64_i8 v[22:25], v[130:133], v[214:217], v[22:25]
	v_mfma_i32_16x16x64_i8 v[14:17], v[134:137], v[214:217], v[14:17]
	v_mfma_i32_16x16x64_i8 v[2:5], v[134:137], v[222:225], v[2:5]
	v_mfma_i32_16x16x64_i8 v[6:9], v[130:133], v[222:225], v[6:9]
	s_setprio 0
	s_barrier
	s_add_i32 s66, 0, 0x18000
	s_add_i32 s67, 0, 0x1c000
	v_add_u32_e32 v142, s66, v190
	v_add_u32_e32 v158, s67, v190
	ds_read_b128 v[130:133], v142
	ds_read_b128 v[134:137], v142 offset:1024
	ds_read_b128 v[138:141], v142 offset:2048
	ds_read_b128 v[142:145], v142 offset:3072
	ds_read_b128 v[146:149], v158
	ds_read_b128 v[150:153], v158 offset:1024
	ds_read_b128 v[154:157], v158 offset:2048
	ds_read_b128 v[158:161], v158 offset:3072
	s_add_u32 s0, s38, 0x80000
	s_addc_u32 s1, s39, 0
	s_mov_b32 m0, s42
	ds_read_b128 v[194:197], v193 offset:32768
	ds_read_b128 v[198:201], v193 offset:33792
	ds_read_b128 v[202:205], v193 offset:34816
	ds_read_b128 v[206:209], v193 offset:35840
	ds_read_b128 v[210:213], v193 offset:36864
	ds_read_b128 v[214:217], v193 offset:37888
	ds_read_b128 v[218:221], v193 offset:38912
	ds_read_b128 v[222:225], v193 offset:39936
	global_load_lds_dwordx4 v162, s[0:1]
	s_mov_b32 m0, s43
	s_nop 0
	global_load_lds_dwordx4 v166, s[0:1]
	s_waitcnt vmcnt(8)
	s_waitcnt lgkmcnt(0)
	s_barrier
	s_setprio 1
	s_waitcnt lgkmcnt(0)
	v_mfma_i32_16x16x64_i8 v[126:129], v[130:133], v[194:197], v[126:129]
	v_mfma_i32_16x16x64_i8 v[122:125], v[138:141], v[194:197], v[122:125]
	v_mfma_i32_16x16x64_i8 v[106:109], v[138:141], v[202:205], v[106:109]
	v_mfma_i32_16x16x64_i8 v[114:117], v[130:133], v[202:205], v[114:117]
	v_mfma_i32_16x16x64_i8 v[98:101], v[130:133], v[210:213], v[98:101]
	v_mfma_i32_16x16x64_i8 v[90:93], v[138:141], v[210:213], v[90:93]
	v_mfma_i32_16x16x64_i8 v[74:77], v[138:141], v[218:221], v[74:77]
	v_mfma_i32_16x16x64_i8 v[82:85], v[130:133], v[218:221], v[82:85]
	s_nop 0
	v_mfma_i32_16x16x64_i8 v[126:129], v[134:137], v[198:201], v[126:129]
	v_mfma_i32_16x16x64_i8 v[122:125], v[142:145], v[198:201], v[122:125]
	v_mfma_i32_16x16x64_i8 v[106:109], v[142:145], v[206:209], v[106:109]
	v_mfma_i32_16x16x64_i8 v[114:117], v[134:137], v[206:209], v[114:117]
	v_mfma_i32_16x16x64_i8 v[98:101], v[134:137], v[214:217], v[98:101]
	v_mfma_i32_16x16x64_i8 v[90:93], v[142:145], v[214:217], v[90:93]
	v_mfma_i32_16x16x64_i8 v[74:77], v[142:145], v[222:225], v[74:77]
	v_mfma_i32_16x16x64_i8 v[82:85], v[134:137], v[222:225], v[82:85]
	v_mfma_i32_16x16x64_i8 v[118:121], v[146:149], v[194:197], v[118:121]
	v_mfma_i32_16x16x64_i8 v[110:113], v[154:157], v[194:197], v[110:113]
	v_mfma_i32_16x16x64_i8 v[94:97], v[154:157], v[202:205], v[94:97]
	v_mfma_i32_16x16x64_i8 v[102:105], v[146:149], v[202:205], v[102:105]
	v_mfma_i32_16x16x64_i8 v[86:89], v[146:149], v[210:213], v[86:89]
	v_mfma_i32_16x16x64_i8 v[78:81], v[154:157], v[210:213], v[78:81]
	v_mfma_i32_16x16x64_i8 v[66:69], v[154:157], v[218:221], v[66:69]
	v_mfma_i32_16x16x64_i8 v[70:73], v[146:149], v[218:221], v[70:73]
	s_nop 0
	v_mfma_i32_16x16x64_i8 v[118:121], v[150:153], v[198:201], v[118:121]
	v_mfma_i32_16x16x64_i8 v[110:113], v[158:161], v[198:201], v[110:113]
	v_mfma_i32_16x16x64_i8 v[94:97], v[158:161], v[206:209], v[94:97]
	v_mfma_i32_16x16x64_i8 v[102:105], v[150:153], v[206:209], v[102:105]
	v_mfma_i32_16x16x64_i8 v[86:89], v[150:153], v[214:217], v[86:89]
	v_mfma_i32_16x16x64_i8 v[78:81], v[158:161], v[214:217], v[78:81]
	v_mfma_i32_16x16x64_i8 v[66:69], v[158:161], v[222:225], v[66:69]
	v_mfma_i32_16x16x64_i8 v[70:73], v[150:153], v[222:225], v[70:73]
	s_setprio 0
	s_barrier
	s_add_i32 s0, s66, s40
	s_mov_b32 m0, s0
	s_add_u32 s98, s36, 0x80
	s_addc_u32 s99, s37, 0
	s_add_u32 s100, s38, 0x80
	s_addc_u32 s101, s39, 0
	ds_read_b128 v[194:197], v193 offset:49152
	ds_read_b128 v[198:201], v193 offset:50176
	ds_read_b128 v[202:205], v193 offset:51200
	ds_read_b128 v[206:209], v193 offset:52224
	ds_read_b128 v[210:213], v193 offset:53248
	ds_read_b128 v[214:217], v193 offset:54272
	ds_read_b128 v[218:221], v193 offset:55296
	ds_read_b128 v[222:225], v193 offset:56320
	global_load_lds_dwordx4 v164, s[98:99]
	s_add_i32 m0, s0, 0x2000
	s_add_u32 s0, s36, 0x80080
	s_addc_u32 s1, s37, 0
	s_add_i32 s36, s67, s40
	global_load_lds_dwordx4 v168, s[98:99]
	s_mov_b32 m0, s36
	s_nop 0
	global_load_lds_dwordx4 v164, s[0:1]
	s_add_i32 m0, s36, 0x2000
	s_nop 0
	global_load_lds_dwordx4 v168, s[0:1]
	s_mov_b32 m0, s48
	s_nop 0
	global_load_lds_dwordx4 v162, s[100:101]
	s_mov_b32 m0, s49
	s_nop 0
	global_load_lds_dwordx4 v166, s[100:101]
	s_waitcnt vmcnt(8)
	s_waitcnt lgkmcnt(0)
	s_barrier
	s_setprio 1
	s_waitcnt lgkmcnt(0)
	v_mfma_i32_16x16x64_i8 v[62:65], v[130:133], v[194:197], v[62:65]
	v_mfma_i32_16x16x64_i8 v[58:61], v[138:141], v[194:197], v[58:61]
	v_mfma_i32_16x16x64_i8 v[42:45], v[138:141], v[202:205], v[42:45]
	v_mfma_i32_16x16x64_i8 v[50:53], v[130:133], v[202:205], v[50:53]
	v_mfma_i32_16x16x64_i8 v[34:37], v[130:133], v[210:213], v[34:37]
	v_mfma_i32_16x16x64_i8 v[26:29], v[138:141], v[210:213], v[26:29]
	v_mfma_i32_16x16x64_i8 v[10:13], v[138:141], v[218:221], v[10:13]
	v_mfma_i32_16x16x64_i8 v[18:21], v[130:133], v[218:221], v[18:21]
	s_nop 0
	v_mfma_i32_16x16x64_i8 v[62:65], v[134:137], v[198:201], v[62:65]
	v_mfma_i32_16x16x64_i8 v[58:61], v[142:145], v[198:201], v[58:61]
	v_mfma_i32_16x16x64_i8 v[42:45], v[142:145], v[206:209], v[42:45]
	v_mfma_i32_16x16x64_i8 v[50:53], v[134:137], v[206:209], v[50:53]
	v_mfma_i32_16x16x64_i8 v[34:37], v[134:137], v[214:217], v[34:37]
	v_mfma_i32_16x16x64_i8 v[26:29], v[142:145], v[214:217], v[26:29]
	v_mfma_i32_16x16x64_i8 v[10:13], v[142:145], v[222:225], v[10:13]
	v_mfma_i32_16x16x64_i8 v[18:21], v[134:137], v[222:225], v[18:21]
	v_mfma_i32_16x16x64_i8 v[54:57], v[146:149], v[194:197], v[54:57]
	v_mfma_i32_16x16x64_i8 v[46:49], v[154:157], v[194:197], v[46:49]
	v_mfma_i32_16x16x64_i8 v[30:33], v[154:157], v[202:205], v[30:33]
	v_mfma_i32_16x16x64_i8 v[38:41], v[146:149], v[202:205], v[38:41]
	v_mfma_i32_16x16x64_i8 v[22:25], v[146:149], v[210:213], v[22:25]
	v_mfma_i32_16x16x64_i8 v[14:17], v[154:157], v[210:213], v[14:17]
	v_mfma_i32_16x16x64_i8 v[2:5], v[154:157], v[218:221], v[2:5]
	v_mfma_i32_16x16x64_i8 v[6:9], v[146:149], v[218:221], v[6:9]
	s_nop 0
	v_mfma_i32_16x16x64_i8 v[54:57], v[150:153], v[198:201], v[54:57]
	v_mfma_i32_16x16x64_i8 v[46:49], v[158:161], v[198:201], v[46:49]
	v_mfma_i32_16x16x64_i8 v[30:33], v[158:161], v[206:209], v[30:33]
	v_mfma_i32_16x16x64_i8 v[38:41], v[150:153], v[206:209], v[38:41]
	v_mfma_i32_16x16x64_i8 v[22:25], v[150:153], v[214:217], v[22:25]
	v_mfma_i32_16x16x64_i8 v[14:17], v[158:161], v[214:217], v[14:17]
	v_mfma_i32_16x16x64_i8 v[2:5], v[158:161], v[222:225], v[2:5]
	v_mfma_i32_16x16x64_i8 v[6:9], v[150:153], v[222:225], v[6:9]
	s_setprio 0
	s_barrier
	s_add_i32 s64, s64, 2
	s_add_u32 s34, s34, 0x100
	s_addc_u32 s35, s35, 0
	s_add_u32 s62, s62, 0x100
	s_addc_u32 s63, s63, 0
	s_cmp_gt_u32 s64, 29
	s_cbranch_scc1 .LBB0_791

.LBB0_1051:
	s_add_u32 s8, s17, s6
	s_addc_u32 s9, s48, s7
	s_add_u32 s8, s8, 0x32800100
	s_addc_u32 s9, s9, 0
	s_add_u32 s65, s49, s6
	s_addc_u32 s68, s50, s7
	s_add_i32 s69, 0, 0x10000
	s_cmpk_eq_i32 s6, 0xf00
	s_cselect_b32 s41, s5, s9
	s_cselect_b32 s40, s4, s8
	s_cselect_b32 s9, s21, s68
	s_cselect_b32 s8, s20, s65
	s_add_i32 s65, 0, 0x14000
	v_add_u32_e32 v130, s69, v187
	v_add_u32_e32 v134, s65, v187
	ds_read_b128 v[158:161], v130
	ds_read_b128 v[150:153], v130 offset:1024
	ds_read_b128 v[154:157], v130 offset:2048
	ds_read_b128 v[146:149], v130 offset:3072
	ds_read_b128 v[142:145], v134
	ds_read_b128 v[130:133], v134 offset:1024
	ds_read_b128 v[138:141], v134 offset:2048
	ds_read_b128 v[134:137], v134 offset:3072
	v_lshl_add_u64 v[214:215], v[168:169], 0, s[6:7]
	s_add_i32 m0, s43, 0xc000
	ds_read_b128 v[172:175], v188
	ds_read_b128 v[176:179], v188 offset:1024
	ds_read_b128 v[190:193], v188 offset:2048
	ds_read_b128 v[194:197], v188 offset:3072
	ds_read_b128 v[198:201], v188 offset:4096
	ds_read_b128 v[202:205], v188 offset:5120
	ds_read_b128 v[206:209], v188 offset:6144
	ds_read_b128 v[210:213], v188 offset:7168
	global_load_lds_dwordx4 v[214:215], off
	v_lshl_add_u64 v[214:215], v[170:171], 0, s[6:7]
	s_add_i32 m0, s43, 0xe000
	s_nop 0
	global_load_lds_dwordx4 v[214:215], off
	s_waitcnt vmcnt(8)
	s_waitcnt lgkmcnt(0)
	s_barrier
	s_setprio 1
	s_waitcnt lgkmcnt(0)
	v_mfma_i32_16x16x64_i8 v[70:73], v[158:161], v[172:175], v[70:73]
	v_mfma_i32_16x16x64_i8 v[34:37], v[154:157], v[172:175], v[34:37]
	v_mfma_i32_16x16x64_i8 v[54:57], v[154:157], v[190:193], v[54:57]
	v_mfma_i32_16x16x64_i8 v[102:105], v[158:161], v[190:193], v[102:105]
	v_mfma_i32_16x16x64_i8 v[114:117], v[158:161], v[198:201], v[114:117]
	v_mfma_i32_16x16x64_i8 v[86:89], v[154:157], v[198:201], v[86:89]
	v_mfma_i32_16x16x64_i8 v[110:113], v[154:157], v[206:209], v[110:113]
	v_mfma_i32_16x16x64_i8 v[126:129], v[158:161], v[206:209], v[126:129]
	s_nop 0
	v_mfma_i32_16x16x64_i8 v[70:73], v[150:153], v[176:179], v[70:73]
	v_mfma_i32_16x16x64_i8 v[34:37], v[146:149], v[176:179], v[34:37]
	v_mfma_i32_16x16x64_i8 v[54:57], v[146:149], v[194:197], v[54:57]
	v_mfma_i32_16x16x64_i8 v[102:105], v[150:153], v[194:197], v[102:105]
	v_mfma_i32_16x16x64_i8 v[114:117], v[150:153], v[202:205], v[114:117]
	v_mfma_i32_16x16x64_i8 v[86:89], v[146:149], v[202:205], v[86:89]
	v_mfma_i32_16x16x64_i8 v[110:113], v[146:149], v[210:213], v[110:113]
	v_mfma_i32_16x16x64_i8 v[126:129], v[150:153], v[210:213], v[126:129]
	v_mfma_i32_16x16x64_i8 v[18:21], v[142:145], v[172:175], v[18:21]
	v_mfma_i32_16x16x64_i8 v[2:5], v[138:141], v[172:175], v[2:5]
	v_mfma_i32_16x16x64_i8 v[6:9], v[138:141], v[190:193], v[6:9]
	v_mfma_i32_16x16x64_i8 v[38:41], v[142:145], v[190:193], v[38:41]
	v_mfma_i32_16x16x64_i8 v[66:69], v[142:145], v[198:201], v[66:69]
	v_mfma_i32_16x16x64_i8 v[26:29], v[138:141], v[198:201], v[26:29]
	v_mfma_i32_16x16x64_i8 v[50:53], v[138:141], v[206:209], v[50:53]
	v_mfma_i32_16x16x64_i8 v[90:93], v[142:145], v[206:209], v[90:93]
	s_nop 0
	v_mfma_i32_16x16x64_i8 v[18:21], v[130:133], v[176:179], v[18:21]
	v_mfma_i32_16x16x64_i8 v[2:5], v[134:137], v[176:179], v[2:5]
	v_mfma_i32_16x16x64_i8 v[6:9], v[134:137], v[194:197], v[6:9]
	v_mfma_i32_16x16x64_i8 v[38:41], v[130:133], v[194:197], v[38:41]
	v_mfma_i32_16x16x64_i8 v[66:69], v[130:133], v[202:205], v[66:69]
	v_mfma_i32_16x16x64_i8 v[26:29], v[134:137], v[202:205], v[26:29]
	v_mfma_i32_16x16x64_i8 v[50:53], v[134:137], v[210:213], v[50:53]
	v_mfma_i32_16x16x64_i8 v[90:93], v[130:133], v[210:213], v[90:93]
	s_setprio 0
	s_barrier
	s_add_i32 s68, s69, s42
	s_mov_b32 m0, s68
	ds_read_b128 v[190:193], v188 offset:16384
	ds_read_b128 v[194:197], v188 offset:17408
	ds_read_b128 v[198:201], v188 offset:18432
	ds_read_b128 v[202:205], v188 offset:19456
	ds_read_b128 v[206:209], v188 offset:20480
	ds_read_b128 v[210:213], v188 offset:21504
	ds_read_b128 v[214:217], v188 offset:22528
	ds_read_b128 v[218:221], v188 offset:23552
	global_load_lds_dwordx4 v162, s[8:9]
	s_add_i32 m0, s68, 0x2000
	s_add_u32 s68, s8, 0x80000
	s_addc_u32 s69, s9, 0
	s_add_i32 s65, s65, s42
	global_load_lds_dwordx4 v166, s[8:9]
	s_mov_b32 m0, s65
	s_nop 0
	global_load_lds_dwordx4 v162, s[68:69]
	s_add_i32 m0, s65, 0x2000
	s_nop 0
	global_load_lds_dwordx4 v166, s[68:69]
	s_mov_b32 m0, s43
	s_nop 0
	global_load_lds_dwordx4 v162, s[40:41]
	s_mov_b32 m0, s60
	s_nop 0
	global_load_lds_dwordx4 v166, s[40:41]
	s_waitcnt vmcnt(8)
	s_waitcnt lgkmcnt(0)
	s_barrier
	s_setprio 1
	s_waitcnt lgkmcnt(0)
	v_mfma_i32_16x16x64_i8 v[122:125], v[158:161], v[190:193], v[122:125]
	v_mfma_i32_16x16x64_i8 v[118:121], v[154:157], v[190:193], v[118:121]
	v_mfma_i32_16x16x64_i8 v[94:97], v[154:157], v[198:201], v[94:97]
	v_mfma_i32_16x16x64_i8 v[98:101], v[158:161], v[198:201], v[98:101]
	v_mfma_i32_16x16x64_i8 v[62:65], v[158:161], v[206:209], v[62:65]
	v_mfma_i32_16x16x64_i8 v[58:61], v[154:157], v[206:209], v[58:61]
	v_mfma_i32_16x16x64_i8 v[22:25], v[154:157], v[214:217], v[22:25]
	v_mfma_i32_16x16x64_i8 v[30:33], v[158:161], v[214:217], v[30:33]
	s_nop 0
	v_mfma_i32_16x16x64_i8 v[122:125], v[150:153], v[194:197], v[122:125]
	v_mfma_i32_16x16x64_i8 v[118:121], v[146:149], v[194:197], v[118:121]
	v_mfma_i32_16x16x64_i8 v[94:97], v[146:149], v[202:205], v[94:97]
	v_mfma_i32_16x16x64_i8 v[98:101], v[150:153], v[202:205], v[98:101]
	v_mfma_i32_16x16x64_i8 v[62:65], v[150:153], v[210:213], v[62:65]
	v_mfma_i32_16x16x64_i8 v[58:61], v[146:149], v[210:213], v[58:61]
	v_mfma_i32_16x16x64_i8 v[22:25], v[146:149], v[218:221], v[22:25]
	v_mfma_i32_16x16x64_i8 v[30:33], v[150:153], v[218:221], v[30:33]
	v_mfma_i32_16x16x64_i8 v[106:109], v[142:145], v[190:193], v[106:109]
	v_mfma_i32_16x16x64_i8 v[82:85], v[138:141], v[190:193], v[82:85]
	v_mfma_i32_16x16x64_i8 v[74:77], v[138:141], v[198:201], v[74:77]
	v_mfma_i32_16x16x64_i8 v[78:81], v[142:145], v[198:201], v[78:81]
	v_mfma_i32_16x16x64_i8 v[46:49], v[142:145], v[206:209], v[46:49]
	v_mfma_i32_16x16x64_i8 v[42:45], v[138:141], v[206:209], v[42:45]
	v_mfma_i32_16x16x64_i8 v[10:13], v[138:141], v[214:217], v[10:13]
	v_mfma_i32_16x16x64_i8 v[14:17], v[142:145], v[214:217], v[14:17]
	s_nop 0
	v_mfma_i32_16x16x64_i8 v[106:109], v[130:133], v[194:197], v[106:109]
	v_mfma_i32_16x16x64_i8 v[82:85], v[134:137], v[194:197], v[82:85]
	v_mfma_i32_16x16x64_i8 v[74:77], v[134:137], v[202:205], v[74:77]
	v_mfma_i32_16x16x64_i8 v[78:81], v[130:133], v[202:205], v[78:81]
	v_mfma_i32_16x16x64_i8 v[46:49], v[130:133], v[210:213], v[46:49]
	v_mfma_i32_16x16x64_i8 v[42:45], v[134:137], v[210:213], v[42:45]
	v_mfma_i32_16x16x64_i8 v[10:13], v[134:137], v[218:221], v[10:13]
	v_mfma_i32_16x16x64_i8 v[14:17], v[130:133], v[218:221], v[14:17]
	s_setprio 0
	s_barrier
	s_add_i32 s65, 0, 0x18000
	s_add_i32 s68, 0, 0x1c000
	v_add_u32_e32 v142, s65, v187
	v_add_u32_e32 v158, s68, v187
	ds_read_b128 v[130:133], v142
	ds_read_b128 v[134:137], v142 offset:1024
	ds_read_b128 v[138:141], v142 offset:2048
	ds_read_b128 v[142:145], v142 offset:3072
	ds_read_b128 v[146:149], v158
	ds_read_b128 v[150:153], v158 offset:1024
	ds_read_b128 v[154:157], v158 offset:2048
	ds_read_b128 v[158:161], v158 offset:3072
	s_add_u32 s40, s40, 0x80000
	s_addc_u32 s41, s41, 0
	s_add_u32 s100, s40, 0xfff80080
	s_addc_u32 s101, s41, -1
	s_mov_b32 m0, s61
	ds_read_b128 v[190:193], v188 offset:32768
	ds_read_b128 v[194:197], v188 offset:33792
	ds_read_b128 v[198:201], v188 offset:34816
	ds_read_b128 v[202:205], v188 offset:35840
	ds_read_b128 v[206:209], v188 offset:36864
	ds_read_b128 v[210:213], v188 offset:37888
	ds_read_b128 v[214:217], v188 offset:38912
	ds_read_b128 v[218:221], v188 offset:39936
	global_load_lds_dwordx4 v162, s[40:41]
	s_mov_b32 m0, s62
	s_nop 0
	global_load_lds_dwordx4 v166, s[40:41]
	s_waitcnt vmcnt(8)
	s_waitcnt lgkmcnt(0)
	s_barrier
	s_setprio 1
	s_waitcnt lgkmcnt(0)
	v_mfma_i32_16x16x64_i8 v[70:73], v[130:133], v[190:193], v[70:73]
	v_mfma_i32_16x16x64_i8 v[34:37], v[138:141], v[190:193], v[34:37]
	v_mfma_i32_16x16x64_i8 v[54:57], v[138:141], v[198:201], v[54:57]
	v_mfma_i32_16x16x64_i8 v[102:105], v[130:133], v[198:201], v[102:105]
	v_mfma_i32_16x16x64_i8 v[114:117], v[130:133], v[206:209], v[114:117]
	v_mfma_i32_16x16x64_i8 v[86:89], v[138:141], v[206:209], v[86:89]
	v_mfma_i32_16x16x64_i8 v[110:113], v[138:141], v[214:217], v[110:113]
	v_mfma_i32_16x16x64_i8 v[126:129], v[130:133], v[214:217], v[126:129]
	s_nop 0
	v_mfma_i32_16x16x64_i8 v[70:73], v[134:137], v[194:197], v[70:73]
	v_mfma_i32_16x16x64_i8 v[34:37], v[142:145], v[194:197], v[34:37]
	v_mfma_i32_16x16x64_i8 v[54:57], v[142:145], v[202:205], v[54:57]
	v_mfma_i32_16x16x64_i8 v[102:105], v[134:137], v[202:205], v[102:105]
	v_mfma_i32_16x16x64_i8 v[114:117], v[134:137], v[210:213], v[114:117]
	v_mfma_i32_16x16x64_i8 v[86:89], v[142:145], v[210:213], v[86:89]
	v_mfma_i32_16x16x64_i8 v[110:113], v[142:145], v[218:221], v[110:113]
	v_mfma_i32_16x16x64_i8 v[126:129], v[134:137], v[218:221], v[126:129]
	v_mfma_i32_16x16x64_i8 v[18:21], v[146:149], v[190:193], v[18:21]
	v_mfma_i32_16x16x64_i8 v[2:5], v[154:157], v[190:193], v[2:5]
	v_mfma_i32_16x16x64_i8 v[6:9], v[154:157], v[198:201], v[6:9]
	v_mfma_i32_16x16x64_i8 v[38:41], v[146:149], v[198:201], v[38:41]
	v_mfma_i32_16x16x64_i8 v[66:69], v[146:149], v[206:209], v[66:69]
	v_mfma_i32_16x16x64_i8 v[26:29], v[154:157], v[206:209], v[26:29]
	v_mfma_i32_16x16x64_i8 v[50:53], v[154:157], v[214:217], v[50:53]
	v_mfma_i32_16x16x64_i8 v[90:93], v[146:149], v[214:217], v[90:93]
	s_nop 0
	v_mfma_i32_16x16x64_i8 v[18:21], v[150:153], v[194:197], v[18:21]
	v_mfma_i32_16x16x64_i8 v[2:5], v[158:161], v[194:197], v[2:5]
	v_mfma_i32_16x16x64_i8 v[6:9], v[158:161], v[202:205], v[6:9]
	v_mfma_i32_16x16x64_i8 v[38:41], v[150:153], v[202:205], v[38:41]
	v_mfma_i32_16x16x64_i8 v[66:69], v[150:153], v[210:213], v[66:69]
	v_mfma_i32_16x16x64_i8 v[26:29], v[158:161], v[210:213], v[26:29]
	v_mfma_i32_16x16x64_i8 v[50:53], v[158:161], v[218:221], v[50:53]
	v_mfma_i32_16x16x64_i8 v[90:93], v[150:153], v[218:221], v[90:93]
	s_setprio 0
	s_barrier
	s_add_i32 s40, s65, s42
	s_mov_b32 m0, s40
	s_add_u32 s98, s8, 0x80
	s_addc_u32 s99, s9, 0
	ds_read_b128 v[190:193], v188 offset:49152
	ds_read_b128 v[194:197], v188 offset:50176
	ds_read_b128 v[198:201], v188 offset:51200
	ds_read_b128 v[202:205], v188 offset:52224
	ds_read_b128 v[206:209], v188 offset:53248
	ds_read_b128 v[210:213], v188 offset:54272
	ds_read_b128 v[214:217], v188 offset:55296
	ds_read_b128 v[218:221], v188 offset:56320
	global_load_lds_dwordx4 v162, s[98:99]
	s_add_i32 m0, s40, 0x2000
	s_add_u32 s8, s8, 0x80080
	s_addc_u32 s9, s9, 0
	s_add_i32 s40, s68, s42
	global_load_lds_dwordx4 v166, s[98:99]
	s_mov_b32 m0, s40
	s_nop 0
	global_load_lds_dwordx4 v162, s[8:9]
	s_add_i32 m0, s40, 0x2000
	s_nop 0
	global_load_lds_dwordx4 v166, s[8:9]
	s_mov_b32 m0, s66
	s_nop 0
	global_load_lds_dwordx4 v162, s[100:101]
	s_mov_b32 m0, s67
	s_nop 0
	global_load_lds_dwordx4 v166, s[100:101]
	s_waitcnt vmcnt(8)
	s_waitcnt lgkmcnt(0)
	s_barrier
	s_setprio 1
	s_waitcnt lgkmcnt(0)
	v_mfma_i32_16x16x64_i8 v[122:125], v[130:133], v[190:193], v[122:125]
	v_mfma_i32_16x16x64_i8 v[118:121], v[138:141], v[190:193], v[118:121]
	v_mfma_i32_16x16x64_i8 v[94:97], v[138:141], v[198:201], v[94:97]
	v_mfma_i32_16x16x64_i8 v[98:101], v[130:133], v[198:201], v[98:101]
	v_mfma_i32_16x16x64_i8 v[62:65], v[130:133], v[206:209], v[62:65]
	v_mfma_i32_16x16x64_i8 v[58:61], v[138:141], v[206:209], v[58:61]
	v_mfma_i32_16x16x64_i8 v[22:25], v[138:141], v[214:217], v[22:25]
	v_mfma_i32_16x16x64_i8 v[30:33], v[130:133], v[214:217], v[30:33]
	s_nop 0
	v_mfma_i32_16x16x64_i8 v[122:125], v[134:137], v[194:197], v[122:125]
	v_mfma_i32_16x16x64_i8 v[118:121], v[142:145], v[194:197], v[118:121]
	v_mfma_i32_16x16x64_i8 v[94:97], v[142:145], v[202:205], v[94:97]
	v_mfma_i32_16x16x64_i8 v[98:101], v[134:137], v[202:205], v[98:101]
	v_mfma_i32_16x16x64_i8 v[62:65], v[134:137], v[210:213], v[62:65]
	v_mfma_i32_16x16x64_i8 v[58:61], v[142:145], v[210:213], v[58:61]
	v_mfma_i32_16x16x64_i8 v[22:25], v[142:145], v[218:221], v[22:25]
	v_mfma_i32_16x16x64_i8 v[30:33], v[134:137], v[218:221], v[30:33]
	v_mfma_i32_16x16x64_i8 v[106:109], v[146:149], v[190:193], v[106:109]
	v_mfma_i32_16x16x64_i8 v[82:85], v[154:157], v[190:193], v[82:85]
	v_mfma_i32_16x16x64_i8 v[74:77], v[154:157], v[198:201], v[74:77]
	v_mfma_i32_16x16x64_i8 v[78:81], v[146:149], v[198:201], v[78:81]
	v_mfma_i32_16x16x64_i8 v[46:49], v[146:149], v[206:209], v[46:49]
	v_mfma_i32_16x16x64_i8 v[42:45], v[154:157], v[206:209], v[42:45]
	v_mfma_i32_16x16x64_i8 v[10:13], v[154:157], v[214:217], v[10:13]
	v_mfma_i32_16x16x64_i8 v[14:17], v[146:149], v[214:217], v[14:17]
	s_nop 0
	v_mfma_i32_16x16x64_i8 v[106:109], v[150:153], v[194:197], v[106:109]
	v_mfma_i32_16x16x64_i8 v[82:85], v[158:161], v[194:197], v[82:85]
	v_mfma_i32_16x16x64_i8 v[74:77], v[158:161], v[202:205], v[74:77]
	v_mfma_i32_16x16x64_i8 v[78:81], v[150:153], v[202:205], v[78:81]
	v_mfma_i32_16x16x64_i8 v[46:49], v[150:153], v[210:213], v[46:49]
	v_mfma_i32_16x16x64_i8 v[42:45], v[158:161], v[210:213], v[42:45]
	v_mfma_i32_16x16x64_i8 v[10:13], v[158:161], v[218:221], v[10:13]
	v_mfma_i32_16x16x64_i8 v[14:17], v[150:153], v[218:221], v[14:17]
	s_setprio 0
	s_barrier
	s_add_i32 s64, s64, 2
	s_add_u32 s6, s6, 0x100
	s_addc_u32 s7, s7, 0
	s_cmp_gt_u32 s64, 29
	s_cbranch_scc0 .LBB0_1051
	s_waitcnt vmcnt(0)
	s_cmpk_lt_u32 s59, 0x100
	s_cbranch_scc0 .LBB0_1054
	s_barrier

.LBB0_1173:
	ds_read_b128 v[158:161], v184
	ds_read_b128 v[150:153], v184 offset:1024
	ds_read_b128 v[154:157], v184 offset:2048
	ds_read_b128 v[146:149], v184 offset:3072
	ds_read_b128 v[142:145], v185
	ds_read_b128 v[130:133], v185 offset:1024
	ds_read_b128 v[138:141], v185 offset:2048
	ds_read_b128 v[134:137], v185 offset:3072
	s_add_u32 s38, s36, 0xfff80080
	s_addc_u32 s39, s37, -1
	s_cmp_eq_u32 s65, 28
	s_cselect_b32 s41, s18, s39
	s_cselect_b32 s40, s19, s38
	s_cselect_b32 s39, s25, s64
	s_cselect_b32 s38, s27, s63
	v_lshl_add_u64 v[212:213], s[36:37], 0, v[166:167]
	s_add_i32 m0, s35, 0xc000
	ds_read_b128 v[174:177], v186
	ds_read_b128 v[178:181], v186 offset:1024
	ds_read_b128 v[188:191], v186 offset:2048
	ds_read_b128 v[192:195], v186 offset:3072
	ds_read_b128 v[196:199], v186 offset:4096
	ds_read_b128 v[200:203], v186 offset:5120
	ds_read_b128 v[204:207], v186 offset:6144
	ds_read_b128 v[208:211], v186 offset:7168
	global_load_lds_dwordx4 v[212:213], off
	v_lshl_add_u64 v[212:213], s[36:37], 0, v[168:169]
	s_add_i32 m0, s35, 0xe000
	s_nop 0
	global_load_lds_dwordx4 v[212:213], off
	s_waitcnt vmcnt(8)
	s_waitcnt lgkmcnt(0)
	s_barrier
	s_setprio 1
	s_waitcnt lgkmcnt(0)
	v_mfma_i32_16x16x64_i8 v[126:129], v[158:161], v[174:177], v[126:129]
	v_mfma_i32_16x16x64_i8 v[122:125], v[154:157], v[174:177], v[122:125]
	v_mfma_i32_16x16x64_i8 v[106:109], v[154:157], v[188:191], v[106:109]
	v_mfma_i32_16x16x64_i8 v[110:113], v[158:161], v[188:191], v[110:113]
	v_mfma_i32_16x16x64_i8 v[94:97], v[158:161], v[196:199], v[94:97]
	v_mfma_i32_16x16x64_i8 v[90:93], v[154:157], v[196:199], v[90:93]
	v_mfma_i32_16x16x64_i8 v[74:77], v[154:157], v[204:207], v[74:77]
	v_mfma_i32_16x16x64_i8 v[78:81], v[158:161], v[204:207], v[78:81]
	s_nop 0
	v_mfma_i32_16x16x64_i8 v[126:129], v[150:153], v[178:181], v[126:129]
	v_mfma_i32_16x16x64_i8 v[122:125], v[146:149], v[178:181], v[122:125]
	v_mfma_i32_16x16x64_i8 v[106:109], v[146:149], v[192:195], v[106:109]
	v_mfma_i32_16x16x64_i8 v[110:113], v[150:153], v[192:195], v[110:113]
	v_mfma_i32_16x16x64_i8 v[94:97], v[150:153], v[200:203], v[94:97]
	v_mfma_i32_16x16x64_i8 v[90:93], v[146:149], v[200:203], v[90:93]
	v_mfma_i32_16x16x64_i8 v[74:77], v[146:149], v[208:211], v[74:77]
	v_mfma_i32_16x16x64_i8 v[78:81], v[150:153], v[208:211], v[78:81]
	v_mfma_i32_16x16x64_i8 v[118:121], v[142:145], v[174:177], v[118:121]
	v_mfma_i32_16x16x64_i8 v[114:117], v[138:141], v[174:177], v[114:117]
	v_mfma_i32_16x16x64_i8 v[98:101], v[138:141], v[188:191], v[98:101]
	v_mfma_i32_16x16x64_i8 v[102:105], v[142:145], v[188:191], v[102:105]
	v_mfma_i32_16x16x64_i8 v[86:89], v[142:145], v[196:199], v[86:89]
	v_mfma_i32_16x16x64_i8 v[82:85], v[138:141], v[196:199], v[82:85]
	v_mfma_i32_16x16x64_i8 v[66:69], v[138:141], v[204:207], v[66:69]
	v_mfma_i32_16x16x64_i8 v[70:73], v[142:145], v[204:207], v[70:73]
	s_nop 0
	v_mfma_i32_16x16x64_i8 v[118:121], v[130:133], v[178:181], v[118:121]
	v_mfma_i32_16x16x64_i8 v[114:117], v[134:137], v[178:181], v[114:117]
	v_mfma_i32_16x16x64_i8 v[98:101], v[134:137], v[192:195], v[98:101]
	v_mfma_i32_16x16x64_i8 v[102:105], v[130:133], v[192:195], v[102:105]
	v_mfma_i32_16x16x64_i8 v[86:89], v[130:133], v[200:203], v[86:89]
	v_mfma_i32_16x16x64_i8 v[82:85], v[134:137], v[200:203], v[82:85]
	v_mfma_i32_16x16x64_i8 v[66:69], v[134:137], v[208:211], v[66:69]
	v_mfma_i32_16x16x64_i8 v[70:73], v[130:133], v[208:211], v[70:73]
	s_setprio 0
	s_barrier
	s_add_i32 s66, s51, s3
	v_lshl_add_u64 v[174:175], s[38:39], 0, v[164:165]
	s_mov_b32 m0, s66
	ds_read_b128 v[188:191], v186 offset:16384
	ds_read_b128 v[192:195], v186 offset:17408
	ds_read_b128 v[196:199], v186 offset:18432
	ds_read_b128 v[200:203], v186 offset:19456
	ds_read_b128 v[204:207], v186 offset:20480
	ds_read_b128 v[208:211], v186 offset:21504
	ds_read_b128 v[212:215], v186 offset:22528
	ds_read_b128 v[216:219], v186 offset:23552
	global_load_lds_dwordx4 v[174:175], off
	s_add_i32 m0, s66, 0x2000
	s_add_u32 s66, s38, 0x80000
	v_lshl_add_u64 v[176:177], s[38:39], 0, v[162:163]
	s_addc_u32 s67, s39, 0
	s_add_i32 s68, s58, s3
	global_load_lds_dwordx4 v[176:177], off
	v_lshl_add_u64 v[178:179], s[66:67], 0, v[164:165]
	s_mov_b32 m0, s68
	v_lshl_add_u64 v[180:181], s[40:41], 0, v[162:163]
	global_load_lds_dwordx4 v[178:179], off
	v_lshl_add_u64 v[178:179], s[66:67], 0, v[162:163]
	s_add_i32 m0, s68, 0x2000
	s_nop 0
	global_load_lds_dwordx4 v[178:179], off
	v_lshl_add_u64 v[178:179], s[40:41], 0, v[164:165]
	s_mov_b32 m0, s35
	s_nop 0
	global_load_lds_dwordx4 v[178:179], off
	s_mov_b32 m0, s42
	s_nop 0
	global_load_lds_dwordx4 v[180:181], off
	s_waitcnt vmcnt(8)
	s_waitcnt lgkmcnt(0)
	s_barrier
	s_setprio 1
	s_waitcnt lgkmcnt(0)
	v_mfma_i32_16x16x64_i8 v[62:65], v[158:161], v[188:191], v[62:65]
	v_mfma_i32_16x16x64_i8 v[58:61], v[154:157], v[188:191], v[58:61]
	v_mfma_i32_16x16x64_i8 v[42:45], v[154:157], v[196:199], v[42:45]
	v_mfma_i32_16x16x64_i8 v[46:49], v[158:161], v[196:199], v[46:49]
	v_mfma_i32_16x16x64_i8 v[30:33], v[158:161], v[204:207], v[30:33]
	v_mfma_i32_16x16x64_i8 v[26:29], v[154:157], v[204:207], v[26:29]
	v_mfma_i32_16x16x64_i8 v[10:13], v[154:157], v[212:215], v[10:13]
	v_mfma_i32_16x16x64_i8 v[14:17], v[158:161], v[212:215], v[14:17]
	s_nop 0
	v_mfma_i32_16x16x64_i8 v[62:65], v[150:153], v[192:195], v[62:65]
	v_mfma_i32_16x16x64_i8 v[58:61], v[146:149], v[192:195], v[58:61]
	v_mfma_i32_16x16x64_i8 v[42:45], v[146:149], v[200:203], v[42:45]
	v_mfma_i32_16x16x64_i8 v[46:49], v[150:153], v[200:203], v[46:49]
	v_mfma_i32_16x16x64_i8 v[30:33], v[150:153], v[208:211], v[30:33]
	v_mfma_i32_16x16x64_i8 v[26:29], v[146:149], v[208:211], v[26:29]
	v_mfma_i32_16x16x64_i8 v[10:13], v[146:149], v[216:219], v[10:13]
	v_mfma_i32_16x16x64_i8 v[14:17], v[150:153], v[216:219], v[14:17]
	v_mfma_i32_16x16x64_i8 v[54:57], v[142:145], v[188:191], v[54:57]
	v_mfma_i32_16x16x64_i8 v[50:53], v[138:141], v[188:191], v[50:53]
	v_mfma_i32_16x16x64_i8 v[34:37], v[138:141], v[196:199], v[34:37]
	v_mfma_i32_16x16x64_i8 v[38:41], v[142:145], v[196:199], v[38:41]
	v_mfma_i32_16x16x64_i8 v[22:25], v[142:145], v[204:207], v[22:25]
	v_mfma_i32_16x16x64_i8 v[18:21], v[138:141], v[204:207], v[18:21]
	v_mfma_i32_16x16x64_i8 v[2:5], v[138:141], v[212:215], v[2:5]
	v_mfma_i32_16x16x64_i8 v[6:9], v[142:145], v[212:215], v[6:9]
	s_nop 0
	v_mfma_i32_16x16x64_i8 v[54:57], v[130:133], v[192:195], v[54:57]
	v_mfma_i32_16x16x64_i8 v[50:53], v[134:137], v[192:195], v[50:53]
	v_mfma_i32_16x16x64_i8 v[34:37], v[134:137], v[200:203], v[34:37]
	v_mfma_i32_16x16x64_i8 v[38:41], v[130:133], v[200:203], v[38:41]
	v_mfma_i32_16x16x64_i8 v[22:25], v[130:133], v[208:211], v[22:25]
	v_mfma_i32_16x16x64_i8 v[18:21], v[134:137], v[208:211], v[18:21]
	v_mfma_i32_16x16x64_i8 v[2:5], v[134:137], v[216:219], v[2:5]
	v_mfma_i32_16x16x64_i8 v[6:9], v[130:133], v[216:219], v[6:9]
	s_setprio 0
	s_barrier
	s_add_i32 s66, 0, 0x18000
	s_add_i32 s67, 0, 0x1c000
	v_add_u32_e32 v142, s66, v182
	v_add_u32_e32 v158, s67, v182
	ds_read_b128 v[130:133], v142
	ds_read_b128 v[134:137], v142 offset:1024
	ds_read_b128 v[138:141], v142 offset:2048
	ds_read_b128 v[142:145], v142 offset:3072
	ds_read_b128 v[146:149], v158
	ds_read_b128 v[150:153], v158 offset:1024
	ds_read_b128 v[154:157], v158 offset:2048
	ds_read_b128 v[158:161], v158 offset:3072
	s_add_u32 s40, s40, 0x80000
	s_addc_u32 s41, s41, 0
	s_mov_b32 m0, s43
	v_lshl_add_u64 v[220:221], s[40:41], 0, v[164:165]
	ds_read_b128 v[188:191], v186 offset:32768
	ds_read_b128 v[192:195], v186 offset:33792
	ds_read_b128 v[196:199], v186 offset:34816
	ds_read_b128 v[200:203], v186 offset:35840
	ds_read_b128 v[204:207], v186 offset:36864
	ds_read_b128 v[208:211], v186 offset:37888
	ds_read_b128 v[212:215], v186 offset:38912
	ds_read_b128 v[216:219], v186 offset:39936
	global_load_lds_dwordx4 v[220:221], off
	v_lshl_add_u64 v[220:221], s[40:41], 0, v[162:163]
	s_mov_b32 m0, s44
	s_nop 0
	global_load_lds_dwordx4 v[220:221], off
	s_waitcnt vmcnt(8)
	s_waitcnt lgkmcnt(0)
	s_barrier
	s_setprio 1
	s_waitcnt lgkmcnt(0)
	v_mfma_i32_16x16x64_i8 v[126:129], v[130:133], v[188:191], v[126:129]
	v_mfma_i32_16x16x64_i8 v[122:125], v[138:141], v[188:191], v[122:125]
	v_mfma_i32_16x16x64_i8 v[106:109], v[138:141], v[196:199], v[106:109]
	v_mfma_i32_16x16x64_i8 v[110:113], v[130:133], v[196:199], v[110:113]
	v_mfma_i32_16x16x64_i8 v[94:97], v[130:133], v[204:207], v[94:97]
	v_mfma_i32_16x16x64_i8 v[90:93], v[138:141], v[204:207], v[90:93]
	v_mfma_i32_16x16x64_i8 v[74:77], v[138:141], v[212:215], v[74:77]
	v_mfma_i32_16x16x64_i8 v[78:81], v[130:133], v[212:215], v[78:81]
	s_nop 0
	v_mfma_i32_16x16x64_i8 v[126:129], v[134:137], v[192:195], v[126:129]
	v_mfma_i32_16x16x64_i8 v[122:125], v[142:145], v[192:195], v[122:125]
	v_mfma_i32_16x16x64_i8 v[106:109], v[142:145], v[200:203], v[106:109]
	v_mfma_i32_16x16x64_i8 v[110:113], v[134:137], v[200:203], v[110:113]
	v_mfma_i32_16x16x64_i8 v[94:97], v[134:137], v[208:211], v[94:97]
	v_mfma_i32_16x16x64_i8 v[90:93], v[142:145], v[208:211], v[90:93]
	v_mfma_i32_16x16x64_i8 v[74:77], v[142:145], v[216:219], v[74:77]
	v_mfma_i32_16x16x64_i8 v[78:81], v[134:137], v[216:219], v[78:81]
	v_mfma_i32_16x16x64_i8 v[118:121], v[146:149], v[188:191], v[118:121]
	v_mfma_i32_16x16x64_i8 v[114:117], v[154:157], v[188:191], v[114:117]
	v_mfma_i32_16x16x64_i8 v[98:101], v[154:157], v[196:199], v[98:101]
	v_mfma_i32_16x16x64_i8 v[102:105], v[146:149], v[196:199], v[102:105]
	v_mfma_i32_16x16x64_i8 v[86:89], v[146:149], v[204:207], v[86:89]
	v_mfma_i32_16x16x64_i8 v[82:85], v[154:157], v[204:207], v[82:85]
	v_mfma_i32_16x16x64_i8 v[66:69], v[154:157], v[212:215], v[66:69]
	v_mfma_i32_16x16x64_i8 v[70:73], v[146:149], v[212:215], v[70:73]
	s_nop 0
	v_mfma_i32_16x16x64_i8 v[118:121], v[150:153], v[192:195], v[118:121]
	v_mfma_i32_16x16x64_i8 v[114:117], v[158:161], v[192:195], v[114:117]
	v_mfma_i32_16x16x64_i8 v[98:101], v[158:161], v[200:203], v[98:101]
	v_mfma_i32_16x16x64_i8 v[102:105], v[150:153], v[200:203], v[102:105]
	v_mfma_i32_16x16x64_i8 v[86:89], v[150:153], v[208:211], v[86:89]
	v_mfma_i32_16x16x64_i8 v[82:85], v[158:161], v[208:211], v[82:85]
	v_mfma_i32_16x16x64_i8 v[66:69], v[158:161], v[216:219], v[66:69]
	v_mfma_i32_16x16x64_i8 v[70:73], v[150:153], v[216:219], v[70:73]
	s_setprio 0
	s_barrier
	s_add_i32 s40, s66, s3
	v_lshl_add_u64 v[174:175], v[174:175], 0, s[8:9]
	s_mov_b32 m0, s40
	ds_read_b128 v[188:191], v186 offset:49152
	ds_read_b128 v[192:195], v186 offset:50176
	ds_read_b128 v[196:199], v186 offset:51200
	ds_read_b128 v[200:203], v186 offset:52224
	ds_read_b128 v[204:207], v186 offset:53248
	ds_read_b128 v[208:211], v186 offset:54272
	ds_read_b128 v[212:215], v186 offset:55296
	ds_read_b128 v[216:219], v186 offset:56320
	global_load_lds_dwordx4 v[174:175], off
	s_add_i32 m0, s40, 0x2000
	s_add_u32 s38, s38, 0x80080
	v_lshl_add_u64 v[174:175], v[176:177], 0, s[8:9]
	s_addc_u32 s39, s39, 0
	s_add_i32 s40, s67, s3
	global_load_lds_dwordx4 v[174:175], off
	v_lshl_add_u64 v[174:175], s[38:39], 0, v[164:165]
	s_mov_b32 m0, s40
	s_nop 0
	global_load_lds_dwordx4 v[174:175], off
	v_lshl_add_u64 v[174:175], s[38:39], 0, v[162:163]
	s_add_i32 m0, s40, 0x2000
	s_nop 0
	global_load_lds_dwordx4 v[174:175], off
	v_lshl_add_u64 v[174:175], v[178:179], 0, s[8:9]
	s_mov_b32 m0, s49
	s_nop 0
	global_load_lds_dwordx4 v[174:175], off
	v_lshl_add_u64 v[174:175], v[180:181], 0, s[8:9]
	s_mov_b32 m0, s50
	s_nop 0
	global_load_lds_dwordx4 v[174:175], off
	s_waitcnt vmcnt(8)
	s_waitcnt lgkmcnt(0)
	s_barrier
	s_setprio 1
	s_waitcnt lgkmcnt(0)
	v_mfma_i32_16x16x64_i8 v[62:65], v[130:133], v[188:191], v[62:65]
	v_mfma_i32_16x16x64_i8 v[58:61], v[138:141], v[188:191], v[58:61]
	v_mfma_i32_16x16x64_i8 v[42:45], v[138:141], v[196:199], v[42:45]
	v_mfma_i32_16x16x64_i8 v[46:49], v[130:133], v[196:199], v[46:49]
	v_mfma_i32_16x16x64_i8 v[30:33], v[130:133], v[204:207], v[30:33]
	v_mfma_i32_16x16x64_i8 v[26:29], v[138:141], v[204:207], v[26:29]
	v_mfma_i32_16x16x64_i8 v[10:13], v[138:141], v[212:215], v[10:13]
	v_mfma_i32_16x16x64_i8 v[14:17], v[130:133], v[212:215], v[14:17]
	s_nop 0
	v_mfma_i32_16x16x64_i8 v[62:65], v[134:137], v[192:195], v[62:65]
	v_mfma_i32_16x16x64_i8 v[58:61], v[142:145], v[192:195], v[58:61]
	v_mfma_i32_16x16x64_i8 v[42:45], v[142:145], v[200:203], v[42:45]
	v_mfma_i32_16x16x64_i8 v[46:49], v[134:137], v[200:203], v[46:49]
	v_mfma_i32_16x16x64_i8 v[30:33], v[134:137], v[208:211], v[30:33]
	v_mfma_i32_16x16x64_i8 v[26:29], v[142:145], v[208:211], v[26:29]
	v_mfma_i32_16x16x64_i8 v[10:13], v[142:145], v[216:219], v[10:13]
	v_mfma_i32_16x16x64_i8 v[14:17], v[134:137], v[216:219], v[14:17]
	v_mfma_i32_16x16x64_i8 v[54:57], v[146:149], v[188:191], v[54:57]
	v_mfma_i32_16x16x64_i8 v[50:53], v[154:157], v[188:191], v[50:53]
	v_mfma_i32_16x16x64_i8 v[34:37], v[154:157], v[196:199], v[34:37]
	v_mfma_i32_16x16x64_i8 v[38:41], v[146:149], v[196:199], v[38:41]
	v_mfma_i32_16x16x64_i8 v[22:25], v[146:149], v[204:207], v[22:25]
	v_mfma_i32_16x16x64_i8 v[18:21], v[154:157], v[204:207], v[18:21]
	v_mfma_i32_16x16x64_i8 v[2:5], v[154:157], v[212:215], v[2:5]
	v_mfma_i32_16x16x64_i8 v[6:9], v[146:149], v[212:215], v[6:9]
	s_nop 0
	v_mfma_i32_16x16x64_i8 v[54:57], v[150:153], v[192:195], v[54:57]
	v_mfma_i32_16x16x64_i8 v[50:53], v[158:161], v[192:195], v[50:53]
	v_mfma_i32_16x16x64_i8 v[34:37], v[158:161], v[200:203], v[34:37]
	v_mfma_i32_16x16x64_i8 v[38:41], v[150:153], v[200:203], v[38:41]
	v_mfma_i32_16x16x64_i8 v[22:25], v[150:153], v[208:211], v[22:25]
	v_mfma_i32_16x16x64_i8 v[18:21], v[158:161], v[208:211], v[18:21]
	v_mfma_i32_16x16x64_i8 v[2:5], v[158:161], v[216:219], v[2:5]
	v_mfma_i32_16x16x64_i8 v[6:9], v[150:153], v[216:219], v[6:9]
	s_setprio 0
	s_barrier
	s_add_i32 s65, s65, 2
	s_add_u32 s36, s36, 0x100
	s_addc_u32 s37, s37, 0
	s_add_u32 s63, s63, 0x100
	s_addc_u32 s64, s64, 0
	s_cmp_gt_u32 s65, 29
	s_cbranch_scc0 .LBB0_1173
	s_and_b64 vcc, exec, s[12:13]
	s_cbranch_vccz .LBB0_1176
	s_barrier

.LBB0_1291:
	ds_read_b128 v[26:29], v184
	ds_read_b128 v[30:33], v184 offset:1024
	ds_read_b128 v[18:21], v184 offset:2048
	ds_read_b128 v[22:25], v184 offset:3072
	ds_read_b128 v[10:13], v185
	ds_read_b128 v[14:17], v185 offset:1024
	ds_read_b128 v[2:5], v185 offset:2048
	ds_read_b128 v[6:9], v185 offset:3072
	s_add_u32 s20, s14, s16
	s_addc_u32 s21, s15, s17
	s_add_u32 s20, s20, 0x2a800100
	s_addc_u32 s21, s21, 0
	s_add_u32 s48, s31, s16
	s_addc_u32 s49, s34, s17
	s_cmpk_eq_i32 s16, 0x700
	s_cselect_b32 s23, s9, s21
	s_cselect_b32 s22, s8, s20
	s_cselect_b32 s21, s5, s49
	s_cselect_b32 s20, s4, s48
	s_mov_b32 m0, s36
	v_lshl_add_u64 v[214:215], v[170:171], 0, s[16:17]
	ds_read_b128 v[174:177], v186
	ds_read_b128 v[178:181], v186 offset:1024
	ds_read_b128 v[190:193], v186 offset:2048
	ds_read_b128 v[194:197], v186 offset:3072
	ds_read_b128 v[198:201], v186 offset:4096
	ds_read_b128 v[202:205], v186 offset:5120
	ds_read_b128 v[206:209], v186 offset:6144
	ds_read_b128 v[210:213], v186 offset:7168
	global_load_lds_dwordx4 v[214:215], off
	v_lshl_add_u64 v[214:215], v[172:173], 0, s[16:17]
	s_mov_b32 m0, s37
	s_nop 0
	global_load_lds_dwordx4 v[214:215], off
	s_waitcnt vmcnt(8)
	s_waitcnt lgkmcnt(0)
	s_barrier
	s_setprio 1
	s_waitcnt lgkmcnt(0)
	v_mfma_f32_16x16x128_f8f6f4 v[158:161], v[26:33], v[174:181], v[158:161]
	v_mfma_f32_16x16x128_f8f6f4 v[154:157], v[18:25], v[174:181], v[154:157]
	v_mfma_f32_16x16x128_f8f6f4 v[138:141], v[18:25], v[190:197], v[138:141]
	v_mfma_f32_16x16x128_f8f6f4 v[146:149], v[26:33], v[190:197], v[146:149]
	v_mfma_f32_16x16x128_f8f6f4 v[130:133], v[26:33], v[198:205], v[130:133]
	v_mfma_f32_16x16x128_f8f6f4 v[122:125], v[18:25], v[198:205], v[122:125]
	v_mfma_f32_16x16x128_f8f6f4 v[106:109], v[18:25], v[206:213], v[106:109]
	v_mfma_f32_16x16x128_f8f6f4 v[114:117], v[26:33], v[206:213], v[114:117]
	v_mfma_f32_16x16x128_f8f6f4 v[102:105], v[10:17], v[206:213], v[102:105]
	v_mfma_f32_16x16x128_f8f6f4 v[98:101], v[2:9], v[206:213], v[98:101]
	v_mfma_f32_16x16x128_f8f6f4 v[142:145], v[2:9], v[174:181], v[142:145]
	v_mfma_f32_16x16x128_f8f6f4 v[150:153], v[10:17], v[174:181], v[150:153]
	v_mfma_f32_16x16x128_f8f6f4 v[134:137], v[10:17], v[190:197], v[134:137]
	v_mfma_f32_16x16x128_f8f6f4 v[126:129], v[2:9], v[190:197], v[126:129]
	v_mfma_f32_16x16x128_f8f6f4 v[110:113], v[2:9], v[198:205], v[110:113]
	v_mfma_f32_16x16x128_f8f6f4 v[118:121], v[10:17], v[198:205], v[118:121]
	s_setprio 0
	s_barrier
	s_mov_b32 m0, s38
	v_lshl_add_u64 v[174:175], s[20:21], 0, v[164:165]
	s_add_u32 s48, s20, 0x80000
	ds_read_b128 v[190:193], v186 offset:16384
	ds_read_b128 v[194:197], v186 offset:17408
	ds_read_b128 v[198:201], v186 offset:18432
	ds_read_b128 v[202:205], v186 offset:19456
	ds_read_b128 v[206:209], v186 offset:20480
	ds_read_b128 v[210:213], v186 offset:21504
	ds_read_b128 v[214:217], v186 offset:22528
	ds_read_b128 v[218:221], v186 offset:23552
	global_load_lds_dwordx4 v[174:175], off
	v_lshl_add_u64 v[176:177], s[20:21], 0, v[168:169]
	s_mov_b32 m0, s39
	s_addc_u32 s49, s21, 0
	global_load_lds_dwordx4 v[176:177], off
	v_lshl_add_u64 v[178:179], s[48:49], 0, v[164:165]
	s_mov_b32 m0, s40
	v_lshl_add_u64 v[180:181], s[22:23], 0, v[166:167]
	global_load_lds_dwordx4 v[178:179], off
	v_lshl_add_u64 v[178:179], s[48:49], 0, v[168:169]
	s_mov_b32 m0, s41
	s_nop 0
	global_load_lds_dwordx4 v[178:179], off
	v_lshl_add_u64 v[178:179], s[22:23], 0, v[162:163]
	s_mov_b32 m0, s24
	s_nop 0
	global_load_lds_dwordx4 v[178:179], off
	s_mov_b32 m0, s25
	s_nop 0
	global_load_lds_dwordx4 v[180:181], off
	s_waitcnt vmcnt(8)
	s_waitcnt lgkmcnt(0)
	s_barrier
	s_setprio 1
	s_waitcnt lgkmcnt(0)
	v_mfma_f32_16x16x128_f8f6f4 v[82:85], v[26:33], v[198:205], v[82:85]
	v_mfma_f32_16x16x128_f8f6f4 v[74:77], v[18:25], v[198:205], v[74:77]
	v_mfma_f32_16x16x128_f8f6f4 v[90:93], v[18:25], v[190:197], v[90:93]
	v_mfma_f32_16x16x128_f8f6f4 v[94:97], v[26:33], v[190:197], v[94:97]
	v_mfma_f32_16x16x128_f8f6f4 v[66:69], v[26:33], v[206:213], v[66:69]
	v_mfma_f32_16x16x128_f8f6f4 v[58:61], v[18:25], v[206:213], v[58:61]
	v_mfma_f32_16x16x128_f8f6f4 v[42:45], v[18:25], v[214:221], v[42:45]
	v_mfma_f32_16x16x128_f8f6f4 v[50:53], v[26:33], v[214:221], v[50:53]
	v_mfma_f32_16x16x128_f8f6f4 v[38:41], v[10:17], v[214:221], v[38:41]
	v_mfma_f32_16x16x128_f8f6f4 v[34:37], v[2:9], v[214:221], v[34:37]
	v_mfma_f32_16x16x128_f8f6f4 v[78:81], v[2:9], v[190:197], v[78:81]
	v_mfma_f32_16x16x128_f8f6f4 v[86:89], v[10:17], v[190:197], v[86:89]
	v_mfma_f32_16x16x128_f8f6f4 v[70:73], v[10:17], v[198:205], v[70:73]
	v_mfma_f32_16x16x128_f8f6f4 v[62:65], v[2:9], v[198:205], v[62:65]
	v_mfma_f32_16x16x128_f8f6f4 v[46:49], v[2:9], v[206:213], v[46:49]
	v_mfma_f32_16x16x128_f8f6f4 v[54:57], v[10:17], v[206:213], v[54:57]
	s_setprio 0
	s_barrier
	ds_read_b128 v[2:5], v187
	ds_read_b128 v[6:9], v187 offset:1024
	ds_read_b128 v[10:13], v187 offset:2048
	ds_read_b128 v[14:17], v187 offset:3072
	ds_read_b128 v[18:21], v188
	ds_read_b128 v[22:25], v188 offset:1024
	ds_read_b128 v[26:29], v188 offset:2048
	ds_read_b128 v[30:33], v188 offset:3072
	s_add_u32 s22, s22, 0x80000
	s_addc_u32 s23, s23, 0
	s_mov_b32 m0, s26
	v_lshl_add_u64 v[222:223], s[22:23], 0, v[162:163]
	ds_read_b128 v[190:193], v186 offset:32768
	ds_read_b128 v[194:197], v186 offset:33792
	ds_read_b128 v[198:201], v186 offset:34816
	ds_read_b128 v[202:205], v186 offset:35840
	ds_read_b128 v[206:209], v186 offset:36864
	ds_read_b128 v[210:213], v186 offset:37888
	ds_read_b128 v[214:217], v186 offset:38912
	ds_read_b128 v[218:221], v186 offset:39936
	global_load_lds_dwordx4 v[222:223], off
	v_lshl_add_u64 v[222:223], s[22:23], 0, v[166:167]
	s_mov_b32 m0, s27
	s_nop 0
	global_load_lds_dwordx4 v[222:223], off
	s_waitcnt vmcnt(8)
	s_waitcnt lgkmcnt(0)
	s_barrier
	s_setprio 1
	s_waitcnt lgkmcnt(0)
	v_mfma_f32_16x16x128_f8f6f4 v[122:125], v[10:17], v[206:213], v[122:125]
	v_mfma_f32_16x16x128_f8f6f4 v[130:133], v[2:9], v[206:213], v[130:133]
	v_mfma_f32_16x16x128_f8f6f4 v[158:161], v[2:9], v[190:197], v[158:161]
	v_mfma_f32_16x16x128_f8f6f4 v[154:157], v[10:17], v[190:197], v[154:157]
	v_mfma_f32_16x16x128_f8f6f4 v[138:141], v[10:17], v[198:205], v[138:141]
	v_mfma_f32_16x16x128_f8f6f4 v[146:149], v[2:9], v[198:205], v[146:149]
	v_mfma_f32_16x16x128_f8f6f4 v[114:117], v[2:9], v[214:221], v[114:117]
	v_mfma_f32_16x16x128_f8f6f4 v[106:109], v[10:17], v[214:221], v[106:109]
	v_mfma_f32_16x16x128_f8f6f4 v[102:105], v[18:25], v[214:221], v[102:105]
	v_mfma_f32_16x16x128_f8f6f4 v[98:101], v[26:33], v[214:221], v[98:101]
	v_mfma_f32_16x16x128_f8f6f4 v[142:145], v[26:33], v[190:197], v[142:145]
	v_mfma_f32_16x16x128_f8f6f4 v[150:153], v[18:25], v[190:197], v[150:153]
	v_mfma_f32_16x16x128_f8f6f4 v[134:137], v[18:25], v[198:205], v[134:137]
	v_mfma_f32_16x16x128_f8f6f4 v[126:129], v[26:33], v[198:205], v[126:129]
	v_mfma_f32_16x16x128_f8f6f4 v[110:113], v[26:33], v[206:213], v[110:113]
	v_mfma_f32_16x16x128_f8f6f4 v[118:121], v[18:25], v[206:213], v[118:121]
	s_setprio 0
	s_barrier
	s_mov_b32 m0, s42
	v_lshl_add_u64 v[174:175], v[174:175], 0, s[12:13]
	s_add_u32 s20, s20, 0x80080
	ds_read_b128 v[190:193], v186 offset:49152
	ds_read_b128 v[194:197], v186 offset:50176
	ds_read_b128 v[198:201], v186 offset:51200
	ds_read_b128 v[202:205], v186 offset:52224
	ds_read_b128 v[206:209], v186 offset:53248
	ds_read_b128 v[210:213], v186 offset:54272
	ds_read_b128 v[214:217], v186 offset:55296
	ds_read_b128 v[218:221], v186 offset:56320
	global_load_lds_dwordx4 v[174:175], off
	v_lshl_add_u64 v[174:175], v[176:177], 0, s[12:13]
	s_mov_b32 m0, s43
	s_addc_u32 s21, s21, 0
	global_load_lds_dwordx4 v[174:175], off
	v_lshl_add_u64 v[174:175], s[20:21], 0, v[164:165]
	s_mov_b32 m0, s44
	s_nop 0
	global_load_lds_dwordx4 v[174:175], off
	v_lshl_add_u64 v[174:175], s[20:21], 0, v[168:169]
	s_mov_b32 m0, s45
	s_nop 0
	global_load_lds_dwordx4 v[174:175], off
	v_lshl_add_u64 v[174:175], v[178:179], 0, s[12:13]
	s_mov_b32 m0, s29
	s_nop 0
	global_load_lds_dwordx4 v[174:175], off
	v_lshl_add_u64 v[174:175], v[180:181], 0, s[12:13]
	s_mov_b32 m0, s30
	s_nop 0
	global_load_lds_dwordx4 v[174:175], off
	s_waitcnt vmcnt(8)
	s_waitcnt lgkmcnt(0)
	s_barrier
	s_setprio 1
	s_waitcnt lgkmcnt(0)
	v_mfma_f32_16x16x128_f8f6f4 v[66:69], v[2:9], v[206:213], v[66:69]
	v_mfma_f32_16x16x128_f8f6f4 v[58:61], v[10:17], v[206:213], v[58:61]
	v_mfma_f32_16x16x128_f8f6f4 v[90:93], v[10:17], v[190:197], v[90:93]
	v_mfma_f32_16x16x128_f8f6f4 v[94:97], v[2:9], v[190:197], v[94:97]
	v_mfma_f32_16x16x128_f8f6f4 v[82:85], v[2:9], v[198:205], v[82:85]
	v_mfma_f32_16x16x128_f8f6f4 v[74:77], v[10:17], v[198:205], v[74:77]
	v_mfma_f32_16x16x128_f8f6f4 v[42:45], v[10:17], v[214:221], v[42:45]
	v_mfma_f32_16x16x128_f8f6f4 v[50:53], v[2:9], v[214:221], v[50:53]
	v_mfma_f32_16x16x128_f8f6f4 v[38:41], v[18:25], v[214:221], v[38:41]
	v_mfma_f32_16x16x128_f8f6f4 v[34:37], v[26:33], v[214:221], v[34:37]
	v_mfma_f32_16x16x128_f8f6f4 v[78:81], v[26:33], v[190:197], v[78:81]
	v_mfma_f32_16x16x128_f8f6f4 v[86:89], v[18:25], v[190:197], v[86:89]
	v_mfma_f32_16x16x128_f8f6f4 v[70:73], v[18:25], v[198:205], v[70:73]
	v_mfma_f32_16x16x128_f8f6f4 v[62:65], v[26:33], v[198:205], v[62:65]
	v_mfma_f32_16x16x128_f8f6f4 v[46:49], v[26:33], v[206:213], v[46:49]
	v_mfma_f32_16x16x128_f8f6f4 v[54:57], v[18:25], v[206:213], v[54:57]
	s_setprio 0
	s_barrier
	s_add_i32 s35, s35, 2
	s_add_u32 s16, s16, 0x100
	s_addc_u32 s17, s17, 0
	s_cmp_gt_u32 s35, 13
	s_cbranch_scc0 .LBB0_1291
	s_cmpk_lt_u32 s19, 0x100
	s_cbranch_scc0 .LBB0_1294
	s_barrier

.LBB0_1309:
	ds_read_b128 v[26:29], v189
	ds_read_b128 v[30:33], v189 offset:1024
	ds_read_b128 v[18:21], v189 offset:2048
	ds_read_b128 v[22:25], v189 offset:3072
	ds_read_b128 v[10:13], v190
	ds_read_b128 v[14:17], v190 offset:1024
	ds_read_b128 v[2:5], v190 offset:2048
	ds_read_b128 v[6:9], v190 offset:3072
	s_add_u32 s40, s38, 0xfff80080
	s_addc_u32 s41, s39, -1
	s_cmp_eq_u32 s72, 28
	s_cselect_b32 s43, s18, s41
	s_cselect_b32 s42, s19, s40
	s_cselect_b32 s41, s27, s71
	s_cselect_b32 s40, s29, s70
	v_lshl_add_u64 v[216:217], s[38:39], 0, v[170:171]
	s_add_i32 m0, s37, 0xc000
	ds_read_b128 v[178:181], v191
	ds_read_b128 v[182:185], v191 offset:1024
	ds_read_b128 v[192:195], v191 offset:2048
	ds_read_b128 v[196:199], v191 offset:3072
	ds_read_b128 v[200:203], v191 offset:4096
	ds_read_b128 v[204:207], v191 offset:5120
	ds_read_b128 v[208:211], v191 offset:6144
	ds_read_b128 v[212:215], v191 offset:7168
	global_load_lds_dwordx4 v[216:217], off
	v_lshl_add_u64 v[216:217], s[38:39], 0, v[172:173]
	s_add_i32 m0, s37, 0xe000
	s_nop 0
	global_load_lds_dwordx4 v[216:217], off
	s_waitcnt vmcnt(8)
	s_waitcnt lgkmcnt(0)
	s_barrier
	s_setprio 1
	s_waitcnt lgkmcnt(0)
	v_mfma_f32_16x16x128_f8f6f4 v[158:161], v[26:33], v[178:185], v[158:161]
	v_mfma_f32_16x16x128_f8f6f4 v[154:157], v[18:25], v[178:185], v[154:157]
	v_mfma_f32_16x16x128_f8f6f4 v[138:141], v[18:25], v[192:199], v[138:141]
	v_mfma_f32_16x16x128_f8f6f4 v[146:149], v[26:33], v[192:199], v[146:149]
	v_mfma_f32_16x16x128_f8f6f4 v[130:133], v[26:33], v[200:207], v[130:133]
	v_mfma_f32_16x16x128_f8f6f4 v[122:125], v[18:25], v[200:207], v[122:125]
	v_mfma_f32_16x16x128_f8f6f4 v[106:109], v[18:25], v[208:215], v[106:109]
	v_mfma_f32_16x16x128_f8f6f4 v[114:117], v[26:33], v[208:215], v[114:117]
	v_mfma_f32_16x16x128_f8f6f4 v[102:105], v[10:17], v[208:215], v[102:105]
	v_mfma_f32_16x16x128_f8f6f4 v[98:101], v[2:9], v[208:215], v[98:101]
	v_mfma_f32_16x16x128_f8f6f4 v[142:145], v[2:9], v[178:185], v[142:145]
	v_mfma_f32_16x16x128_f8f6f4 v[150:153], v[10:17], v[178:185], v[150:153]
	v_mfma_f32_16x16x128_f8f6f4 v[134:137], v[10:17], v[192:199], v[134:137]
	v_mfma_f32_16x16x128_f8f6f4 v[126:129], v[2:9], v[192:199], v[126:129]
	v_mfma_f32_16x16x128_f8f6f4 v[110:113], v[2:9], v[200:207], v[110:113]
	v_mfma_f32_16x16x128_f8f6f4 v[118:121], v[10:17], v[200:207], v[118:121]
	s_setprio 0
	s_barrier
	s_add_i32 s64, s59, s3
	v_lshl_add_u64 v[178:179], s[40:41], 0, v[166:167]
	s_mov_b32 m0, s64
	ds_read_b128 v[192:195], v191 offset:16384
	ds_read_b128 v[196:199], v191 offset:17408
	ds_read_b128 v[200:203], v191 offset:18432
	ds_read_b128 v[204:207], v191 offset:19456
	ds_read_b128 v[208:211], v191 offset:20480
	ds_read_b128 v[212:215], v191 offset:21504
	ds_read_b128 v[216:219], v191 offset:22528
	ds_read_b128 v[220:223], v191 offset:23552
	global_load_lds_dwordx4 v[178:179], off
	s_add_i32 m0, s64, 0x2000
	s_add_u32 s64, s40, 0x80000
	v_lshl_add_u64 v[180:181], s[40:41], 0, v[162:163]
	s_addc_u32 s65, s41, 0
	s_add_i32 s73, s62, s3
	global_load_lds_dwordx4 v[180:181], off
	v_lshl_add_u64 v[182:183], s[64:65], 0, v[166:167]
	s_mov_b32 m0, s73
	v_lshl_add_u64 v[184:185], s[42:43], 0, v[164:165]
	global_load_lds_dwordx4 v[182:183], off
	v_lshl_add_u64 v[182:183], s[64:65], 0, v[162:163]
	s_add_i32 m0, s73, 0x2000
	s_nop 0
	global_load_lds_dwordx4 v[182:183], off
	v_lshl_add_u64 v[182:183], s[42:43], 0, v[168:169]
	s_mov_b32 m0, s37
	s_nop 0
	global_load_lds_dwordx4 v[182:183], off
	s_mov_b32 m0, s44
	s_nop 0
	global_load_lds_dwordx4 v[184:185], off
	s_waitcnt vmcnt(8)
	s_waitcnt lgkmcnt(0)
	s_barrier
	s_setprio 1
	s_waitcnt lgkmcnt(0)
	v_mfma_f32_16x16x128_f8f6f4 v[82:85], v[26:33], v[200:207], v[82:85]
	v_mfma_f32_16x16x128_f8f6f4 v[74:77], v[18:25], v[200:207], v[74:77]
	v_mfma_f32_16x16x128_f8f6f4 v[90:93], v[18:25], v[192:199], v[90:93]
	v_mfma_f32_16x16x128_f8f6f4 v[94:97], v[26:33], v[192:199], v[94:97]
	v_mfma_f32_16x16x128_f8f6f4 v[66:69], v[26:33], v[208:215], v[66:69]
	v_mfma_f32_16x16x128_f8f6f4 v[58:61], v[18:25], v[208:215], v[58:61]
	v_mfma_f32_16x16x128_f8f6f4 v[42:45], v[18:25], v[216:223], v[42:45]
	v_mfma_f32_16x16x128_f8f6f4 v[50:53], v[26:33], v[216:223], v[50:53]
	v_mfma_f32_16x16x128_f8f6f4 v[38:41], v[10:17], v[216:223], v[38:41]
	v_mfma_f32_16x16x128_f8f6f4 v[34:37], v[2:9], v[216:223], v[34:37]
	v_mfma_f32_16x16x128_f8f6f4 v[78:81], v[2:9], v[192:199], v[78:81]
	v_mfma_f32_16x16x128_f8f6f4 v[86:89], v[10:17], v[192:199], v[86:89]
	v_mfma_f32_16x16x128_f8f6f4 v[70:73], v[10:17], v[200:207], v[70:73]
	v_mfma_f32_16x16x128_f8f6f4 v[62:65], v[2:9], v[200:207], v[62:65]
	v_mfma_f32_16x16x128_f8f6f4 v[46:49], v[2:9], v[208:215], v[46:49]
	v_mfma_f32_16x16x128_f8f6f4 v[54:57], v[10:17], v[208:215], v[54:57]
	s_setprio 0
	s_barrier
	s_add_i32 s64, 0, 0x18000
	s_add_i32 s65, 0, 0x1c000
	v_add_u32_e32 v14, s64, v187
	v_add_u32_e32 v30, s65, v187
	ds_read_b128 v[2:5], v14
	ds_read_b128 v[6:9], v14 offset:1024
	ds_read_b128 v[10:13], v14 offset:2048
	ds_read_b128 v[14:17], v14 offset:3072
	ds_read_b128 v[18:21], v30
	ds_read_b128 v[22:25], v30 offset:1024
	ds_read_b128 v[26:29], v30 offset:2048
	ds_read_b128 v[30:33], v30 offset:3072
	s_add_u32 s42, s42, 0x80000
	s_addc_u32 s43, s43, 0
	s_mov_b32 m0, s45
	v_lshl_add_u64 v[224:225], s[42:43], 0, v[168:169]
	ds_read_b128 v[192:195], v191 offset:32768
	ds_read_b128 v[196:199], v191 offset:33792
	ds_read_b128 v[200:203], v191 offset:34816
	ds_read_b128 v[204:207], v191 offset:35840
	ds_read_b128 v[208:211], v191 offset:36864
	ds_read_b128 v[212:215], v191 offset:37888
	ds_read_b128 v[216:219], v191 offset:38912
	ds_read_b128 v[220:223], v191 offset:39936
	global_load_lds_dwordx4 v[224:225], off
	v_lshl_add_u64 v[224:225], s[42:43], 0, v[164:165]
	s_mov_b32 m0, s48
	s_nop 0
	global_load_lds_dwordx4 v[224:225], off
	s_waitcnt vmcnt(8)
	s_waitcnt lgkmcnt(0)
	s_barrier
	s_setprio 1
	s_waitcnt lgkmcnt(0)
	v_mfma_f32_16x16x128_f8f6f4 v[122:125], v[10:17], v[208:215], v[122:125]
	v_mfma_f32_16x16x128_f8f6f4 v[130:133], v[2:9], v[208:215], v[130:133]
	v_mfma_f32_16x16x128_f8f6f4 v[158:161], v[2:9], v[192:199], v[158:161]
	v_mfma_f32_16x16x128_f8f6f4 v[154:157], v[10:17], v[192:199], v[154:157]
	v_mfma_f32_16x16x128_f8f6f4 v[138:141], v[10:17], v[200:207], v[138:141]
	v_mfma_f32_16x16x128_f8f6f4 v[146:149], v[2:9], v[200:207], v[146:149]
	v_mfma_f32_16x16x128_f8f6f4 v[114:117], v[2:9], v[216:223], v[114:117]
	v_mfma_f32_16x16x128_f8f6f4 v[106:109], v[10:17], v[216:223], v[106:109]
	v_mfma_f32_16x16x128_f8f6f4 v[102:105], v[18:25], v[216:223], v[102:105]
	v_mfma_f32_16x16x128_f8f6f4 v[98:101], v[26:33], v[216:223], v[98:101]
	v_mfma_f32_16x16x128_f8f6f4 v[142:145], v[26:33], v[192:199], v[142:145]
	v_mfma_f32_16x16x128_f8f6f4 v[150:153], v[18:25], v[192:199], v[150:153]
	v_mfma_f32_16x16x128_f8f6f4 v[134:137], v[18:25], v[200:207], v[134:137]
	v_mfma_f32_16x16x128_f8f6f4 v[126:129], v[26:33], v[200:207], v[126:129]
	v_mfma_f32_16x16x128_f8f6f4 v[110:113], v[26:33], v[208:215], v[110:113]
	v_mfma_f32_16x16x128_f8f6f4 v[118:121], v[18:25], v[208:215], v[118:121]
	s_setprio 0
	s_barrier
	s_add_i32 s42, s64, s3
	v_lshl_add_u64 v[178:179], v[178:179], 0, s[12:13]
	s_mov_b32 m0, s42
	ds_read_b128 v[192:195], v191 offset:49152
	ds_read_b128 v[196:199], v191 offset:50176
	ds_read_b128 v[200:203], v191 offset:51200
	ds_read_b128 v[204:207], v191 offset:52224
	ds_read_b128 v[208:211], v191 offset:53248
	ds_read_b128 v[212:215], v191 offset:54272
	ds_read_b128 v[216:219], v191 offset:55296
	ds_read_b128 v[220:223], v191 offset:56320
	global_load_lds_dwordx4 v[178:179], off
	s_add_i32 m0, s42, 0x2000
	s_add_u32 s40, s40, 0x80080
	v_lshl_add_u64 v[178:179], v[180:181], 0, s[12:13]
	s_addc_u32 s41, s41, 0
	s_add_i32 s42, s65, s3
	global_load_lds_dwordx4 v[178:179], off
	v_lshl_add_u64 v[178:179], s[40:41], 0, v[166:167]
	s_mov_b32 m0, s42
	s_nop 0
	global_load_lds_dwordx4 v[178:179], off
	v_lshl_add_u64 v[178:179], s[40:41], 0, v[162:163]
	s_add_i32 m0, s42, 0x2000
	s_nop 0
	global_load_lds_dwordx4 v[178:179], off
	v_lshl_add_u64 v[178:179], v[182:183], 0, s[12:13]
	s_mov_b32 m0, s51
	s_nop 0
	global_load_lds_dwordx4 v[178:179], off
	v_lshl_add_u64 v[178:179], v[184:185], 0, s[12:13]
	s_mov_b32 m0, s58
	s_nop 0
	global_load_lds_dwordx4 v[178:179], off
	s_waitcnt vmcnt(8)
	s_waitcnt lgkmcnt(0)
	s_barrier
	s_setprio 1
	s_waitcnt lgkmcnt(0)
	v_mfma_f32_16x16x128_f8f6f4 v[66:69], v[2:9], v[208:215], v[66:69]
	v_mfma_f32_16x16x128_f8f6f4 v[58:61], v[10:17], v[208:215], v[58:61]
	v_mfma_f32_16x16x128_f8f6f4 v[90:93], v[10:17], v[192:199], v[90:93]
	v_mfma_f32_16x16x128_f8f6f4 v[94:97], v[2:9], v[192:199], v[94:97]
	v_mfma_f32_16x16x128_f8f6f4 v[82:85], v[2:9], v[200:207], v[82:85]
	v_mfma_f32_16x16x128_f8f6f4 v[74:77], v[10:17], v[200:207], v[74:77]
	v_mfma_f32_16x16x128_f8f6f4 v[42:45], v[10:17], v[216:223], v[42:45]
	v_mfma_f32_16x16x128_f8f6f4 v[50:53], v[2:9], v[216:223], v[50:53]
	v_mfma_f32_16x16x128_f8f6f4 v[38:41], v[18:25], v[216:223], v[38:41]
	v_mfma_f32_16x16x128_f8f6f4 v[34:37], v[26:33], v[216:223], v[34:37]
	v_mfma_f32_16x16x128_f8f6f4 v[78:81], v[26:33], v[192:199], v[78:81]
	v_mfma_f32_16x16x128_f8f6f4 v[86:89], v[18:25], v[192:199], v[86:89]
	v_mfma_f32_16x16x128_f8f6f4 v[70:73], v[18:25], v[200:207], v[70:73]
	v_mfma_f32_16x16x128_f8f6f4 v[62:65], v[26:33], v[200:207], v[62:65]
	v_mfma_f32_16x16x128_f8f6f4 v[46:49], v[26:33], v[208:215], v[46:49]
	v_mfma_f32_16x16x128_f8f6f4 v[54:57], v[18:25], v[208:215], v[54:57]
	s_setprio 0
	s_barrier
	s_add_i32 s72, s72, 2
	s_add_u32 s38, s38, 0x100
	s_addc_u32 s39, s39, 0
	s_add_u32 s70, s70, 0x100
	s_addc_u32 s71, s71, 0
	s_cmp_gt_u32 s72, 29
	s_cbranch_scc0 .LBB0_1309
	s_and_b64 vcc, exec, s[14:15]
	s_cbranch_vccz .LBB0_1312
	s_barrier

.LBB0_1437:
	v_and_b32_e32 v188, 15, v189
	v_and_b32_e32 v2, 48, v189
	v_lshlrev_b32_e32 v3, 2, v189
	s_and_b32 s8, s6, 3
	s_lshl_b32 s9, s7, 13
	v_lshl_or_b32 v2, v188, 6, v2
	v_and_b32_e32 v3, 32, v3
	v_bitop3_b32 v4, v2, s9, v3 bitop3:0xde
	s_lshl_b32 s9, s8, 12
	v_lshl_add_u64 v[180:181], s[20:21], 0, v[154:155]
	v_bitop3_b32 v2, v2, s9, v3 bitop3:0xde
	s_add_i32 s9, s60, s72
	v_lshl_add_u64 v[178:179], s[20:21], 0, v[182:183]
	v_lshl_add_u64 v[72:73], v[180:181], 0, s[36:37]
	s_mov_b32 m0, s9
	s_add_i32 s19, s9, 0x2000
	s_waitcnt vmcnt(2)
	s_barrier
	global_load_lds_dwordx4 v[72:73], off
	v_lshl_add_u64 v[158:159], v[178:179], 0, s[36:37]
	s_mov_b32 m0, s19
	s_add_i32 s18, s67, 0x8000
	global_load_lds_dwordx4 v[158:159], off
	v_lshl_add_u64 v[70:71], v[172:173], 0, s[36:37]
	s_mov_b32 m0, s18
	s_add_i32 s43, s67, 0xa000
	global_load_lds_dwordx4 v[70:71], off
	v_lshl_add_u64 v[160:161], v[170:171], 0, s[36:37]
	s_mov_b32 m0, s43
	s_add_i32 s44, s61, s72
	global_load_lds_dwordx4 v[160:161], off
	v_lshl_add_u64 v[162:163], s[24:25], 0, v[154:155]
	s_mov_b32 m0, s44
	s_add_i32 s45, s44, 0x2000
	global_load_lds_dwordx4 v[162:163], off
	v_lshl_add_u64 v[164:165], s[24:25], 0, v[182:183]
	s_mov_b32 m0, s45
	s_add_i32 s73, 0, 0x10000
	global_load_lds_dwordx4 v[164:165], off
	v_add_u32_e32 v195, s73, v2
	s_add_i32 s75, 0, 0x14000
	s_waitcnt vmcnt(6)
	s_barrier
	v_add_u32_e32 v194, s75, v2
	v_add_u32_e32 v191, 0, v4
	v_add_u32_e32 v193, s60, v2
	v_add_u32_e32 v192, s61, v2
	ds_read_b128 v[54:57], v195
	ds_read_b128 v[58:61], v195 offset:1024
	ds_read_b128 v[196:199], v195 offset:2048
	ds_read_b128 v[200:203], v195 offset:3072
	ds_read_b128 v[10:13], v194
	ds_read_b128 v[14:17], v194 offset:1024
	ds_read_b128 v[2:5], v194 offset:2048
	ds_read_b128 v[6:9], v194 offset:3072
	s_lshl_b32 s66, s7, 6
	v_lshl_add_u64 v[176:177], s[22:23], 0, v[154:155]
	v_lshl_add_u64 v[174:175], s[22:23], 0, v[182:183]
	s_add_u32 s70, s4, 0x10080
	s_addc_u32 s71, s5, 0
	s_add_i32 s74, s67, 0xc000
	v_lshl_add_u64 v[30:31], s[70:71], 0, v[154:155]
	s_mov_b32 m0, s74
	s_add_i32 s69, s67, 0xe000
	ds_read_b128 v[22:25], v191
	ds_read_b128 v[26:29], v191 offset:1024
	ds_read_b128 v[34:37], v191 offset:2048
	ds_read_b128 v[38:41], v191 offset:3072
	ds_read_b128 v[82:85], v191 offset:4096
	ds_read_b128 v[86:89], v191 offset:5120
	ds_read_b128 v[94:97], v191 offset:6144
	ds_read_b128 v[98:101], v191 offset:7168
	global_load_lds_dwordx4 v[30:31], off
	v_lshl_add_u64 v[30:31], s[70:71], 0, v[182:183]
	s_mov_b32 m0, s69
	s_nop 0
	global_load_lds_dwordx4 v[30:31], off
	s_waitcnt vmcnt(8)
	s_waitcnt lgkmcnt(0)
	s_barrier
	s_setprio 1
	v_mov_b64_e32 v[32:33], v[20:21]
	v_mov_b64_e32 v[152:153], v[20:21]
	v_mov_b64_e32 v[92:93], v[20:21]
	v_mov_b64_e32 v[44:45], v[20:21]
	v_mov_b64_e32 v[116:117], v[20:21]
	v_mov_b64_e32 v[64:65], v[20:21]
	v_mov_b64_e32 v[80:81], v[20:21]
	v_mov_b64_e32 v[52:53], v[20:21]
	v_mov_b64_e32 v[30:31], v[18:19]
	v_mov_b64_e32 v[150:151], v[18:19]
	v_mov_b64_e32 v[90:91], v[18:19]
	v_mov_b64_e32 v[42:43], v[18:19]
	v_mov_b64_e32 v[114:115], v[18:19]
	v_mov_b64_e32 v[62:63], v[18:19]
	v_mov_b64_e32 v[78:79], v[18:19]
	v_mov_b64_e32 v[50:51], v[18:19]
	s_waitcnt lgkmcnt(0)
	v_mfma_f32_16x16x128_f8f6f4 v[30:33], v[54:61], v[22:29], v[30:33]
	v_mfma_f32_16x16x128_f8f6f4 v[150:153], v[196:203], v[22:29], v[150:153]
	v_mfma_f32_16x16x128_f8f6f4 v[42:45], v[196:203], v[34:41], v[42:45]
	v_mfma_f32_16x16x128_f8f6f4 v[90:93], v[54:61], v[34:41], v[90:93]
	v_mfma_f32_16x16x128_f8f6f4 v[114:117], v[54:61], v[82:89], v[114:117]
	v_mfma_f32_16x16x128_f8f6f4 v[62:65], v[196:203], v[82:89], v[62:65]
	v_mfma_f32_16x16x128_f8f6f4 v[50:53], v[196:203], v[94:101], v[50:53]
	v_mfma_f32_16x16x128_f8f6f4 v[78:81], v[54:61], v[94:101], v[78:81]
	v_mov_b64_e32 v[144:145], v[20:21]
	v_mov_b64_e32 v[148:149], v[20:21]
	v_mov_b64_e32 v[142:143], v[18:19]
	v_mov_b64_e32 v[146:147], v[18:19]
	v_mfma_f32_16x16x128_f8f6f4 v[142:145], v[10:17], v[22:29], v[142:145]
	v_mfma_f32_16x16x128_f8f6f4 v[146:149], v[2:9], v[22:29], v[146:149]
	v_mov_b64_e32 v[28:29], v[20:21]
	v_mov_b64_e32 v[140:141], v[20:21]
	v_mov_b64_e32 v[26:27], v[18:19]
	v_mov_b64_e32 v[138:139], v[18:19]
	v_mfma_f32_16x16x128_f8f6f4 v[26:29], v[10:17], v[34:41], v[26:29]
	v_mfma_f32_16x16x128_f8f6f4 v[138:141], v[2:9], v[34:41], v[138:141]
	v_mov_b64_e32 v[40:41], v[20:21]
	v_mov_b64_e32 v[128:129], v[20:21]
	v_mov_b64_e32 v[24:25], v[20:21]
	v_mov_b64_e32 v[76:77], v[20:21]
	v_mov_b64_e32 v[38:39], v[18:19]
	v_mov_b64_e32 v[126:127], v[18:19]
	v_mov_b64_e32 v[22:23], v[18:19]
	v_mov_b64_e32 v[74:75], v[18:19]
	v_mfma_f32_16x16x128_f8f6f4 v[38:41], v[10:17], v[82:89], v[38:41]
	v_mfma_f32_16x16x128_f8f6f4 v[126:129], v[2:9], v[82:89], v[126:129]
	v_mfma_f32_16x16x128_f8f6f4 v[22:25], v[10:17], v[94:101], v[22:25]
	v_mfma_f32_16x16x128_f8f6f4 v[74:77], v[2:9], v[94:101], v[74:77]
	s_setprio 0
	s_barrier
	s_add_i32 s70, s73, s72
	v_lshl_add_u64 v[34:35], v[180:181], 0, s[14:15]
	s_mov_b32 m0, s70
	s_add_i32 s71, s70, 0x2000
	ds_read_b128 v[204:207], v191 offset:16384
	ds_read_b128 v[208:211], v191 offset:17408
	ds_read_b128 v[212:215], v191 offset:18432
	ds_read_b128 v[216:219], v191 offset:19456
	ds_read_b128 v[220:223], v191 offset:20480
	ds_read_b128 v[224:227], v191 offset:21504
	ds_read_b128 v[228:231], v191 offset:22528
	ds_read_b128 v[232:235], v191 offset:23552
	global_load_lds_dwordx4 v[34:35], off
	v_lshl_add_u64 v[34:35], v[178:179], 0, s[14:15]
	s_mov_b32 m0, s71
	s_add_i32 s72, s75, s72
	global_load_lds_dwordx4 v[34:35], off
	v_lshl_add_u64 v[34:35], s[26:27], 0, v[154:155]
	s_mov_b32 m0, s72
	s_add_i32 s73, s72, 0x2000
	global_load_lds_dwordx4 v[34:35], off
	v_lshl_add_u64 v[34:35], s[26:27], 0, v[182:183]
	s_mov_b32 m0, s73
	s_nop 0
	global_load_lds_dwordx4 v[34:35], off
	v_lshl_add_u64 v[34:35], v[172:173], 0, s[14:15]
	s_mov_b32 m0, s67
	s_nop 0
	global_load_lds_dwordx4 v[34:35], off
	v_lshl_add_u64 v[34:35], v[170:171], 0, s[14:15]
	s_mov_b32 m0, s68
	s_nop 0
	global_load_lds_dwordx4 v[34:35], off
	s_waitcnt vmcnt(8)
	s_waitcnt lgkmcnt(0)
	s_barrier
	s_setprio 1
	v_mov_b64_e32 v[136:137], v[20:21]
	v_mov_b64_e32 v[104:105], v[20:21]
	v_mov_b64_e32 v[124:125], v[20:21]
	v_mov_b64_e32 v[100:101], v[20:21]
	v_mov_b64_e32 v[112:113], v[20:21]
	v_mov_b64_e32 v[108:109], v[20:21]
	v_mov_b64_e32 v[88:89], v[20:21]
	v_mov_b64_e32 v[84:85], v[20:21]
	v_mov_b64_e32 v[134:135], v[18:19]
	v_mov_b64_e32 v[102:103], v[18:19]
	v_mov_b64_e32 v[122:123], v[18:19]
	v_mov_b64_e32 v[98:99], v[18:19]
	v_mov_b64_e32 v[110:111], v[18:19]
	v_mov_b64_e32 v[106:107], v[18:19]
	v_mov_b64_e32 v[86:87], v[18:19]
	v_mov_b64_e32 v[82:83], v[18:19]
	s_waitcnt lgkmcnt(0)
	v_mfma_f32_16x16x128_f8f6f4 v[134:137], v[54:61], v[204:211], v[134:137]
	v_mfma_f32_16x16x128_f8f6f4 v[102:105], v[196:203], v[204:211], v[102:105]
	v_mfma_f32_16x16x128_f8f6f4 v[98:101], v[196:203], v[212:219], v[98:101]
	v_mfma_f32_16x16x128_f8f6f4 v[122:125], v[54:61], v[212:219], v[122:125]
	v_mfma_f32_16x16x128_f8f6f4 v[110:113], v[54:61], v[220:227], v[110:113]
	v_mfma_f32_16x16x128_f8f6f4 v[106:109], v[196:203], v[220:227], v[106:109]
	v_mfma_f32_16x16x128_f8f6f4 v[82:85], v[196:203], v[228:235], v[82:85]
	v_mfma_f32_16x16x128_f8f6f4 v[86:89], v[54:61], v[228:235], v[86:89]
	v_mov_b64_e32 v[36:37], v[20:21]
	v_mov_b64_e32 v[132:133], v[20:21]
	v_mov_b64_e32 v[48:49], v[20:21]
	v_mov_b64_e32 v[120:121], v[20:21]
	v_mov_b64_e32 v[68:69], v[20:21]
	v_mov_b64_e32 v[96:97], v[20:21]
	v_mov_b64_e32 v[56:57], v[20:21]
	v_mov_b64_e32 v[60:61], v[20:21]
	v_mov_b64_e32 v[34:35], v[18:19]
	v_mov_b64_e32 v[130:131], v[18:19]
	v_mov_b64_e32 v[46:47], v[18:19]
	v_mov_b64_e32 v[118:119], v[18:19]
	v_mov_b64_e32 v[66:67], v[18:19]
	v_mov_b64_e32 v[94:95], v[18:19]
	v_mov_b64_e32 v[54:55], v[18:19]
	v_mov_b64_e32 v[58:59], v[18:19]
	v_mfma_f32_16x16x128_f8f6f4 v[54:57], v[10:17], v[228:235], v[54:57]
	v_mfma_f32_16x16x128_f8f6f4 v[58:61], v[2:9], v[228:235], v[58:61]
	v_mfma_f32_16x16x128_f8f6f4 v[130:133], v[2:9], v[204:211], v[130:133]
	v_mfma_f32_16x16x128_f8f6f4 v[34:37], v[10:17], v[204:211], v[34:37]
	v_mfma_f32_16x16x128_f8f6f4 v[46:49], v[10:17], v[212:219], v[46:49]
	v_mfma_f32_16x16x128_f8f6f4 v[118:121], v[2:9], v[212:219], v[118:121]
	v_mfma_f32_16x16x128_f8f6f4 v[94:97], v[2:9], v[220:227], v[94:97]
	v_mfma_f32_16x16x128_f8f6f4 v[66:69], v[10:17], v[220:227], v[66:69]
	s_setprio 0
	s_barrier
	ds_read_b128 v[2:5], v193
	ds_read_b128 v[6:9], v193 offset:1024
	ds_read_b128 v[10:13], v193 offset:2048
	ds_read_b128 v[14:17], v193 offset:3072
	ds_read_b128 v[196:199], v192
	ds_read_b128 v[200:203], v192 offset:1024
	ds_read_b128 v[204:207], v192 offset:2048
	ds_read_b128 v[208:211], v192 offset:3072
	s_add_u32 s76, s4, 0x10100
	s_addc_u32 s77, s5, 0
	s_mov_b32 m0, s48
	v_lshl_add_u64 v[244:245], s[76:77], 0, v[154:155]
	ds_read_b128 v[212:215], v191 offset:32768
	ds_read_b128 v[216:219], v191 offset:33792
	ds_read_b128 v[220:223], v191 offset:34816
	ds_read_b128 v[224:227], v191 offset:35840
	ds_read_b128 v[228:231], v191 offset:36864
	ds_read_b128 v[232:235], v191 offset:37888
	ds_read_b128 v[236:239], v191 offset:38912
	ds_read_b128 v[240:243], v191 offset:39936
	global_load_lds_dwordx4 v[244:245], off
	v_lshl_add_u64 v[244:245], s[76:77], 0, v[182:183]
	s_mov_b32 m0, s49
	s_nop 0
	global_load_lds_dwordx4 v[244:245], off
	s_waitcnt vmcnt(8)
	s_waitcnt lgkmcnt(0)
	s_barrier
	s_setprio 1
	s_waitcnt lgkmcnt(0)
	v_mfma_f32_16x16x128_f8f6f4 v[42:45], v[10:17], v[220:227], v[42:45]
	v_mfma_f32_16x16x128_f8f6f4 v[90:93], v[2:9], v[220:227], v[90:93]
	v_mfma_f32_16x16x128_f8f6f4 v[30:33], v[2:9], v[212:219], v[30:33]
	v_mfma_f32_16x16x128_f8f6f4 v[150:153], v[10:17], v[212:219], v[150:153]
	v_mfma_f32_16x16x128_f8f6f4 v[62:65], v[10:17], v[228:235], v[62:65]
	v_mfma_f32_16x16x128_f8f6f4 v[114:117], v[2:9], v[228:235], v[114:117]
	v_mfma_f32_16x16x128_f8f6f4 v[78:81], v[2:9], v[236:243], v[78:81]
	v_mfma_f32_16x16x128_f8f6f4 v[50:53], v[10:17], v[236:243], v[50:53]
	v_mfma_f32_16x16x128_f8f6f4 v[22:25], v[196:203], v[236:243], v[22:25]
	v_mfma_f32_16x16x128_f8f6f4 v[74:77], v[204:211], v[236:243], v[74:77]
	v_mfma_f32_16x16x128_f8f6f4 v[146:149], v[204:211], v[212:219], v[146:149]
	v_mfma_f32_16x16x128_f8f6f4 v[142:145], v[196:203], v[212:219], v[142:145]
	v_mfma_f32_16x16x128_f8f6f4 v[26:29], v[196:203], v[220:227], v[26:29]
	v_mfma_f32_16x16x128_f8f6f4 v[138:141], v[204:211], v[220:227], v[138:141]
	v_mfma_f32_16x16x128_f8f6f4 v[126:129], v[204:211], v[228:235], v[126:129]
	v_mfma_f32_16x16x128_f8f6f4 v[38:41], v[196:203], v[228:235], v[38:41]
	s_setprio 0
	s_barrier
	s_mov_b32 m0, s9
	v_lshl_add_u64 v[244:245], v[180:181], 0, s[38:39]
	ds_read_b128 v[212:215], v191 offset:49152
	ds_read_b128 v[216:219], v191 offset:50176
	ds_read_b128 v[220:223], v191 offset:51200
	ds_read_b128 v[224:227], v191 offset:52224
	ds_read_b128 v[228:231], v191 offset:53248
	ds_read_b128 v[232:235], v191 offset:54272
	ds_read_b128 v[236:239], v191 offset:55296
	ds_read_b128 v[240:243], v191 offset:56320
	global_load_lds_dwordx4 v[244:245], off
	v_lshl_add_u64 v[244:245], v[178:179], 0, s[38:39]
	s_mov_b32 m0, s19
	s_nop 0
	global_load_lds_dwordx4 v[244:245], off
	v_lshl_add_u64 v[244:245], s[28:29], 0, v[154:155]
	s_mov_b32 m0, s44
	s_nop 0
	global_load_lds_dwordx4 v[244:245], off
	v_lshl_add_u64 v[244:245], s[28:29], 0, v[182:183]
	s_mov_b32 m0, s45
	s_nop 0
	global_load_lds_dwordx4 v[244:245], off
	v_lshl_add_u64 v[244:245], v[172:173], 0, s[38:39]
	s_mov_b32 m0, s18
	s_nop 0
	global_load_lds_dwordx4 v[244:245], off
	v_lshl_add_u64 v[244:245], v[170:171], 0, s[38:39]
	s_mov_b32 m0, s43
	s_nop 0
	global_load_lds_dwordx4 v[244:245], off
	s_waitcnt vmcnt(8)
	s_waitcnt lgkmcnt(0)
	s_barrier
	s_setprio 1
	s_waitcnt lgkmcnt(0)
	v_mfma_f32_16x16x128_f8f6f4 v[110:113], v[2:9], v[228:235], v[110:113]
	v_mfma_f32_16x16x128_f8f6f4 v[106:109], v[10:17], v[228:235], v[106:109]
	v_mfma_f32_16x16x128_f8f6f4 v[102:105], v[10:17], v[212:219], v[102:105]
	v_mfma_f32_16x16x128_f8f6f4 v[134:137], v[2:9], v[212:219], v[134:137]
	v_mfma_f32_16x16x128_f8f6f4 v[122:125], v[2:9], v[220:227], v[122:125]
	v_mfma_f32_16x16x128_f8f6f4 v[98:101], v[10:17], v[220:227], v[98:101]
	v_mfma_f32_16x16x128_f8f6f4 v[82:85], v[10:17], v[236:243], v[82:85]
	v_mfma_f32_16x16x128_f8f6f4 v[86:89], v[2:9], v[236:243], v[86:89]
	v_mfma_f32_16x16x128_f8f6f4 v[54:57], v[196:203], v[236:243], v[54:57]
	v_mfma_f32_16x16x128_f8f6f4 v[58:61], v[204:211], v[236:243], v[58:61]
	v_mfma_f32_16x16x128_f8f6f4 v[130:133], v[204:211], v[212:219], v[130:133]
	v_mfma_f32_16x16x128_f8f6f4 v[34:37], v[196:203], v[212:219], v[34:37]
	v_mfma_f32_16x16x128_f8f6f4 v[46:49], v[196:203], v[220:227], v[46:49]
	v_mfma_f32_16x16x128_f8f6f4 v[118:121], v[204:211], v[220:227], v[118:121]
	v_mfma_f32_16x16x128_f8f6f4 v[94:97], v[204:211], v[228:235], v[94:97]
	v_mfma_f32_16x16x128_f8f6f4 v[66:69], v[196:203], v[228:235], v[66:69]
	s_setprio 0
	s_barrier
	ds_read_b128 v[2:5], v195
	ds_read_b128 v[6:9], v195 offset:1024
	ds_read_b128 v[10:13], v195 offset:2048
	ds_read_b128 v[14:17], v195 offset:3072
	ds_read_b128 v[196:199], v194
	ds_read_b128 v[200:203], v194 offset:1024
	ds_read_b128 v[204:207], v194 offset:2048
	ds_read_b128 v[208:211], v194 offset:3072
	s_add_u32 s4, s4, 0x10180
	s_addc_u32 s5, s5, 0
	s_mov_b32 m0, s74
	v_lshl_add_u64 v[194:195], s[4:5], 0, v[154:155]
	ds_read_b128 v[212:215], v191
	ds_read_b128 v[216:219], v191 offset:1024
	ds_read_b128 v[220:223], v191 offset:2048
	ds_read_b128 v[224:227], v191 offset:3072
	ds_read_b128 v[228:231], v191 offset:4096
	ds_read_b128 v[232:235], v191 offset:5120
	ds_read_b128 v[236:239], v191 offset:6144
	ds_read_b128 v[240:243], v191 offset:7168
	global_load_lds_dwordx4 v[194:195], off
	v_lshl_add_u64 v[182:183], s[4:5], 0, v[182:183]
	s_mov_b32 m0, s69
	s_nop 0
	global_load_lds_dwordx4 v[182:183], off
	s_waitcnt vmcnt(8)
	s_waitcnt lgkmcnt(0)
	s_barrier
	s_setprio 1
	s_waitcnt lgkmcnt(0)
	v_mfma_f32_16x16x128_f8f6f4 v[114:117], v[2:9], v[228:235], v[114:117]
	v_mfma_f32_16x16x128_f8f6f4 v[62:65], v[10:17], v[228:235], v[62:65]
	v_mfma_f32_16x16x128_f8f6f4 v[150:153], v[10:17], v[212:219], v[150:153]
	v_mfma_f32_16x16x128_f8f6f4 v[30:33], v[2:9], v[212:219], v[30:33]
	v_mfma_f32_16x16x128_f8f6f4 v[90:93], v[2:9], v[220:227], v[90:93]
	v_mfma_f32_16x16x128_f8f6f4 v[42:45], v[10:17], v[220:227], v[42:45]
	v_mfma_f32_16x16x128_f8f6f4 v[50:53], v[10:17], v[236:243], v[50:53]
	v_mfma_f32_16x16x128_f8f6f4 v[78:81], v[2:9], v[236:243], v[78:81]
	v_mfma_f32_16x16x128_f8f6f4 v[22:25], v[196:203], v[236:243], v[22:25]
	v_mfma_f32_16x16x128_f8f6f4 v[74:77], v[204:211], v[236:243], v[74:77]
	v_mfma_f32_16x16x128_f8f6f4 v[146:149], v[204:211], v[212:219], v[146:149]
	v_mfma_f32_16x16x128_f8f6f4 v[142:145], v[196:203], v[212:219], v[142:145]
	v_mfma_f32_16x16x128_f8f6f4 v[26:29], v[196:203], v[220:227], v[26:29]
	v_mfma_f32_16x16x128_f8f6f4 v[138:141], v[204:211], v[220:227], v[138:141]
	v_mfma_f32_16x16x128_f8f6f4 v[126:129], v[204:211], v[228:235], v[126:129]
	v_mfma_f32_16x16x128_f8f6f4 v[38:41], v[196:203], v[228:235], v[38:41]
	s_setprio 0
	s_barrier
	s_mov_b32 m0, s70
	ds_read_b128 v[212:215], v191 offset:16384
	ds_read_b128 v[216:219], v191 offset:17408
	ds_read_b128 v[220:223], v191 offset:18432
	ds_read_b128 v[224:227], v191 offset:19456
	ds_read_b128 v[228:231], v191 offset:20480
	ds_read_b128 v[232:235], v191 offset:21504
	ds_read_b128 v[236:239], v191 offset:22528
	ds_read_b128 v[240:243], v191 offset:23552
	global_load_lds_dwordx4 v[180:181], off
	s_mov_b32 m0, s71
	s_nop 0
	global_load_lds_dwordx4 v[178:179], off
	s_mov_b32 m0, s72
	s_nop 0
	global_load_lds_dwordx4 v[176:177], off
	s_mov_b32 m0, s73
	s_nop 0
	global_load_lds_dwordx4 v[174:175], off
	s_mov_b32 m0, s67
	s_nop 0
	global_load_lds_dwordx4 v[172:173], off
	s_mov_b32 m0, s68
	s_nop 0
	global_load_lds_dwordx4 v[170:171], off
	s_waitcnt vmcnt(8)
	s_waitcnt lgkmcnt(0)
	s_barrier
	s_setprio 1
	s_waitcnt lgkmcnt(0)
	v_mfma_f32_16x16x128_f8f6f4 v[110:113], v[2:9], v[228:235], v[110:113]
	v_mfma_f32_16x16x128_f8f6f4 v[106:109], v[10:17], v[228:235], v[106:109]
	v_mfma_f32_16x16x128_f8f6f4 v[102:105], v[10:17], v[212:219], v[102:105]
	v_mfma_f32_16x16x128_f8f6f4 v[134:137], v[2:9], v[212:219], v[134:137]
	v_mfma_f32_16x16x128_f8f6f4 v[122:125], v[2:9], v[220:227], v[122:125]
	v_mfma_f32_16x16x128_f8f6f4 v[98:101], v[10:17], v[220:227], v[98:101]
	v_mfma_f32_16x16x128_f8f6f4 v[82:85], v[10:17], v[236:243], v[82:85]
	v_mfma_f32_16x16x128_f8f6f4 v[86:89], v[2:9], v[236:243], v[86:89]
	v_mfma_f32_16x16x128_f8f6f4 v[54:57], v[196:203], v[236:243], v[54:57]
	v_mfma_f32_16x16x128_f8f6f4 v[58:61], v[204:211], v[236:243], v[58:61]
	v_mfma_f32_16x16x128_f8f6f4 v[130:133], v[204:211], v[212:219], v[130:133]
	v_mfma_f32_16x16x128_f8f6f4 v[34:37], v[196:203], v[212:219], v[34:37]
	v_mfma_f32_16x16x128_f8f6f4 v[46:49], v[196:203], v[220:227], v[46:49]
	v_mfma_f32_16x16x128_f8f6f4 v[118:121], v[204:211], v[220:227], v[118:121]
	v_mfma_f32_16x16x128_f8f6f4 v[94:97], v[204:211], v[228:235], v[94:97]
	v_mfma_f32_16x16x128_f8f6f4 v[66:69], v[196:203], v[228:235], v[66:69]
	s_setprio 0
	s_barrier
	ds_read_b128 v[2:5], v193
	ds_read_b128 v[6:9], v193 offset:1024
	ds_read_b128 v[10:13], v193 offset:2048
	ds_read_b128 v[14:17], v193 offset:3072
	ds_read_b128 v[170:173], v192
	ds_read_b128 v[174:177], v192 offset:1024
	ds_read_b128 v[194:197], v192 offset:2048
	ds_read_b128 v[198:201], v192 offset:3072
	s_mov_b32 m0, s48
	ds_read_b128 v[202:205], v191 offset:32768
	ds_read_b128 v[206:209], v191 offset:33792
	ds_read_b128 v[210:213], v191 offset:34816
	ds_read_b128 v[214:217], v191 offset:35840
	ds_read_b128 v[218:221], v191 offset:36864
	ds_read_b128 v[222:225], v191 offset:37888
	ds_read_b128 v[226:229], v191 offset:38912
	ds_read_b128 v[230:233], v191 offset:39936
	global_load_lds_dwordx4 v[166:167], off
	s_mov_b32 m0, s49
	s_nop 0
	global_load_lds_dwordx4 v[168:169], off
	s_waitcnt vmcnt(8)
	s_waitcnt lgkmcnt(0)
	s_barrier
	s_setprio 1
	s_waitcnt lgkmcnt(0)
	v_mfma_f32_16x16x128_f8f6f4 v[30:33], v[2:9], v[202:209], v[30:33]
	v_mfma_f32_16x16x128_f8f6f4 v[150:153], v[10:17], v[202:209], v[150:153]
	v_mfma_f32_16x16x128_f8f6f4 v[42:45], v[10:17], v[210:217], v[42:45]
	v_mfma_f32_16x16x128_f8f6f4 v[90:93], v[2:9], v[210:217], v[90:93]
	v_mfma_f32_16x16x128_f8f6f4 v[114:117], v[2:9], v[218:225], v[114:117]
	v_mfma_f32_16x16x128_f8f6f4 v[62:65], v[10:17], v[218:225], v[62:65]
	v_mfma_f32_16x16x128_f8f6f4 v[50:53], v[10:17], v[226:233], v[50:53]
	v_mfma_f32_16x16x128_f8f6f4 v[78:81], v[2:9], v[226:233], v[78:81]
	v_mfma_f32_16x16x128_f8f6f4 v[22:25], v[170:177], v[226:233], v[22:25]
	v_mfma_f32_16x16x128_f8f6f4 v[74:77], v[194:201], v[226:233], v[74:77]
	v_mfma_f32_16x16x128_f8f6f4 v[146:149], v[194:201], v[202:209], v[146:149]
	v_mfma_f32_16x16x128_f8f6f4 v[142:145], v[170:177], v[202:209], v[142:145]
	v_mfma_f32_16x16x128_f8f6f4 v[26:29], v[170:177], v[210:217], v[26:29]
	v_mfma_f32_16x16x128_f8f6f4 v[138:141], v[194:201], v[210:217], v[138:141]
	v_mfma_f32_16x16x128_f8f6f4 v[126:129], v[194:201], v[218:225], v[126:129]
	v_mfma_f32_16x16x128_f8f6f4 v[38:41], v[170:177], v[218:225], v[38:41]
	s_setprio 0
	s_barrier
	s_mov_b32 m0, s9
	ds_read_b128 v[202:205], v191 offset:49152
	ds_read_b128 v[206:209], v191 offset:50176
	ds_read_b128 v[210:213], v191 offset:51200
	ds_read_b128 v[214:217], v191 offset:52224
	ds_read_b128 v[218:221], v191 offset:53248
	ds_read_b128 v[222:225], v191 offset:54272
	ds_read_b128 v[226:229], v191 offset:55296
	ds_read_b128 v[230:233], v191 offset:56320
	global_load_lds_dwordx4 v[72:73], off
	s_mov_b32 m0, s19
	s_nop 0
	global_load_lds_dwordx4 v[158:159], off
	s_mov_b32 m0, s44
	s_nop 0
	global_load_lds_dwordx4 v[162:163], off
	s_mov_b32 m0, s45
	s_nop 0
	global_load_lds_dwordx4 v[164:165], off
	s_mov_b32 m0, s18
	s_nop 0
	global_load_lds_dwordx4 v[70:71], off
	s_mov_b32 m0, s43
	s_nop 0
	global_load_lds_dwordx4 v[160:161], off
	s_waitcnt vmcnt(8)
	s_waitcnt lgkmcnt(0)
	s_barrier
	s_setprio 1
	s_waitcnt lgkmcnt(0)
	v_mfma_f32_16x16x128_f8f6f4 v[110:113], v[2:9], v[218:225], v[110:113]
	v_mfma_f32_16x16x128_f8f6f4 v[106:109], v[10:17], v[218:225], v[106:109]
	v_mfma_f32_16x16x128_f8f6f4 v[102:105], v[10:17], v[202:209], v[102:105]
	v_mfma_f32_16x16x128_f8f6f4 v[134:137], v[2:9], v[202:209], v[134:137]
	v_mfma_f32_16x16x128_f8f6f4 v[122:125], v[2:9], v[210:217], v[122:125]
	v_mfma_f32_16x16x128_f8f6f4 v[98:101], v[10:17], v[210:217], v[98:101]
	v_mfma_f32_16x16x128_f8f6f4 v[82:85], v[10:17], v[226:233], v[82:85]
	v_mfma_f32_16x16x128_f8f6f4 v[86:89], v[2:9], v[226:233], v[86:89]
	v_mfma_f32_16x16x128_f8f6f4 v[54:57], v[170:177], v[226:233], v[54:57]
	v_mfma_f32_16x16x128_f8f6f4 v[58:61], v[194:201], v[226:233], v[58:61]
	v_mfma_f32_16x16x128_f8f6f4 v[130:133], v[194:201], v[202:209], v[130:133]
	v_mfma_f32_16x16x128_f8f6f4 v[34:37], v[170:177], v[202:209], v[34:37]
	v_mfma_f32_16x16x128_f8f6f4 v[46:49], v[170:177], v[210:217], v[46:49]
	v_mfma_f32_16x16x128_f8f6f4 v[118:121], v[194:201], v[210:217], v[118:121]
	v_mfma_f32_16x16x128_f8f6f4 v[94:97], v[194:201], v[218:225], v[94:97]
	v_mfma_f32_16x16x128_f8f6f4 v[66:69], v[170:177], v[218:225], v[66:69]
	s_setprio 0
	s_barrier
	s_waitcnt vmcnt(0)
	s_cmpk_gt_u32 s65, 0xff
	s_cbranch_scc1 .LBB0_1439
	s_barrier

.LBB0_1558:
	s_add_u32 s39, s30, s38
	s_addc_u32 s44, s31, 0
	s_add_u32 s42, s39, 0x100
	s_addc_u32 s43, s44, 0
	s_and_b64 s[40:41], s[36:37], exec
	s_cselect_b32 s41, s18, s43
	s_cselect_b32 s40, s19, s42
	s_add_u32 s38, s28, s38
	s_addc_u32 s42, s29, 0
	s_add_u32 s38, s38, 0x100
	s_addc_u32 s42, s42, 0
	s_and_b64 s[36:37], s[36:37], exec
	s_cselect_b32 s43, s17, s42
	s_cselect_b32 s42, s21, s38
	s_add_u32 s76, s39, 0x10080
	ds_read_b128 v[26:29], v181
	ds_read_b128 v[30:33], v181 offset:1024
	ds_read_b128 v[18:21], v181 offset:2048
	ds_read_b128 v[22:25], v181 offset:3072
	ds_read_b128 v[10:13], v182
	ds_read_b128 v[14:17], v182 offset:1024
	ds_read_b128 v[2:5], v182 offset:2048
	ds_read_b128 v[6:9], v182 offset:3072
	s_addc_u32 s77, s44, 0
	s_add_i32 s75, s63, s15
	s_add_i32 m0, s27, 0xc000
	s_add_i32 s78, s27, 0xe000
	s_add_i32 s72, s75, 0x2000
	s_add_u32 s44, s42, 0x10000
	s_addc_u32 s45, s43, 0
	s_add_i32 s74, s64, s15
	s_add_i32 s73, s74, 0x2000
	s_add_i32 s71, 0, 0x18000
	s_add_i32 s70, 0, 0x1c000
	s_add_u32 s38, s40, 0x10000
	s_addc_u32 s39, s41, 0
	s_add_i32 s69, s71, s15
	s_add_i32 s67, s69, 0x2000
	s_add_u32 s36, s42, 0x10080
	s_addc_u32 s37, s43, 0
	s_add_i32 s68, s70, s15
	s_add_i32 s66, s68, 0x2000
	v_lshl_add_u64 v[208:209], s[76:77], 0, v[164:165]
	ds_read_b128 v[170:173], v183
	ds_read_b128 v[174:177], v183 offset:1024
	ds_read_b128 v[184:187], v183 offset:2048
	ds_read_b128 v[188:191], v183 offset:3072
	ds_read_b128 v[192:195], v183 offset:4096
	ds_read_b128 v[196:199], v183 offset:5120
	ds_read_b128 v[200:203], v183 offset:6144
	ds_read_b128 v[204:207], v183 offset:7168
	global_load_lds_dwordx4 v[208:209], off
	v_lshl_add_u64 v[208:209], s[76:77], 0, v[162:163]
	s_mov_b32 m0, s78
	s_nop 0
	global_load_lds_dwordx4 v[208:209], off
	s_waitcnt vmcnt(8)
	s_waitcnt lgkmcnt(0)
	s_barrier
	s_setprio 1
	s_waitcnt lgkmcnt(0)
	v_mfma_f32_16x16x128_f8f6f4 v[158:161], v[26:33], v[170:177], v[158:161]
	v_mfma_f32_16x16x128_f8f6f4 v[154:157], v[18:25], v[170:177], v[154:157]
	v_mfma_f32_16x16x128_f8f6f4 v[138:141], v[18:25], v[184:191], v[138:141]
	v_mfma_f32_16x16x128_f8f6f4 v[142:145], v[26:33], v[184:191], v[142:145]
	v_mfma_f32_16x16x128_f8f6f4 v[126:129], v[26:33], v[192:199], v[126:129]
	v_mfma_f32_16x16x128_f8f6f4 v[122:125], v[18:25], v[192:199], v[122:125]
	v_mfma_f32_16x16x128_f8f6f4 v[106:109], v[18:25], v[200:207], v[106:109]
	v_mfma_f32_16x16x128_f8f6f4 v[110:113], v[26:33], v[200:207], v[110:113]
	v_mfma_f32_16x16x128_f8f6f4 v[102:105], v[10:17], v[200:207], v[102:105]
	v_mfma_f32_16x16x128_f8f6f4 v[98:101], v[2:9], v[200:207], v[98:101]
	v_mfma_f32_16x16x128_f8f6f4 v[146:149], v[2:9], v[170:177], v[146:149]
	v_mfma_f32_16x16x128_f8f6f4 v[150:153], v[10:17], v[170:177], v[150:153]
	v_mfma_f32_16x16x128_f8f6f4 v[134:137], v[10:17], v[184:191], v[134:137]
	v_mfma_f32_16x16x128_f8f6f4 v[130:133], v[2:9], v[184:191], v[130:133]
	v_mfma_f32_16x16x128_f8f6f4 v[114:117], v[2:9], v[192:199], v[114:117]
	v_mfma_f32_16x16x128_f8f6f4 v[118:121], v[10:17], v[192:199], v[118:121]
	s_setprio 0
	s_barrier
	s_mov_b32 m0, s75
	v_lshl_add_u64 v[170:171], s[42:43], 0, v[164:165]
	ds_read_b128 v[184:187], v183 offset:16384
	ds_read_b128 v[188:191], v183 offset:17408
	ds_read_b128 v[192:195], v183 offset:18432
	ds_read_b128 v[196:199], v183 offset:19456
	ds_read_b128 v[200:203], v183 offset:20480
	ds_read_b128 v[204:207], v183 offset:21504
	ds_read_b128 v[208:211], v183 offset:22528
	ds_read_b128 v[212:215], v183 offset:23552
	global_load_lds_dwordx4 v[170:171], off
	v_lshl_add_u64 v[172:173], s[42:43], 0, v[162:163]
	s_mov_b32 m0, s72
	v_lshl_add_u64 v[174:175], s[44:45], 0, v[164:165]
	global_load_lds_dwordx4 v[172:173], off
	s_mov_b32 m0, s74
	v_lshl_add_u64 v[176:177], s[40:41], 0, v[162:163]
	global_load_lds_dwordx4 v[174:175], off
	v_lshl_add_u64 v[174:175], s[44:45], 0, v[162:163]
	s_mov_b32 m0, s73
	s_nop 0
	global_load_lds_dwordx4 v[174:175], off
	v_lshl_add_u64 v[174:175], s[40:41], 0, v[164:165]
	s_mov_b32 m0, s27
	s_nop 0
	global_load_lds_dwordx4 v[174:175], off
	s_mov_b32 m0, s49
	s_nop 0
	global_load_lds_dwordx4 v[176:177], off
	s_waitcnt vmcnt(8)
	s_waitcnt lgkmcnt(0)
	s_barrier
	s_setprio 1
	s_waitcnt lgkmcnt(0)
	v_mfma_f32_16x16x128_f8f6f4 v[78:81], v[26:33], v[192:199], v[78:81]
	v_mfma_f32_16x16x128_f8f6f4 v[74:77], v[18:25], v[192:199], v[74:77]
	v_mfma_f32_16x16x128_f8f6f4 v[90:93], v[18:25], v[184:191], v[90:93]
	v_mfma_f32_16x16x128_f8f6f4 v[94:97], v[26:33], v[184:191], v[94:97]
	v_mfma_f32_16x16x128_f8f6f4 v[62:65], v[26:33], v[200:207], v[62:65]
	v_mfma_f32_16x16x128_f8f6f4 v[58:61], v[18:25], v[200:207], v[58:61]
	v_mfma_f32_16x16x128_f8f6f4 v[42:45], v[18:25], v[208:215], v[42:45]
	v_mfma_f32_16x16x128_f8f6f4 v[54:57], v[26:33], v[208:215], v[54:57]
	v_mfma_f32_16x16x128_f8f6f4 v[38:41], v[10:17], v[208:215], v[38:41]
	v_mfma_f32_16x16x128_f8f6f4 v[34:37], v[2:9], v[208:215], v[34:37]
	v_mfma_f32_16x16x128_f8f6f4 v[82:85], v[2:9], v[184:191], v[82:85]
	v_mfma_f32_16x16x128_f8f6f4 v[86:89], v[10:17], v[184:191], v[86:89]
	v_mfma_f32_16x16x128_f8f6f4 v[70:73], v[10:17], v[192:199], v[70:73]
	v_mfma_f32_16x16x128_f8f6f4 v[66:69], v[2:9], v[192:199], v[66:69]
	v_mfma_f32_16x16x128_f8f6f4 v[46:49], v[2:9], v[200:207], v[46:49]
	v_mfma_f32_16x16x128_f8f6f4 v[50:53], v[10:17], v[200:207], v[50:53]
	s_setprio 0
	s_barrier
	v_add_u32_e32 v14, s71, v179
	v_add_u32_e32 v30, s70, v179
	ds_read_b128 v[2:5], v14
	ds_read_b128 v[6:9], v14 offset:1024
	ds_read_b128 v[10:13], v14 offset:2048
	ds_read_b128 v[14:17], v14 offset:3072
	ds_read_b128 v[18:21], v30
	ds_read_b128 v[22:25], v30 offset:1024
	ds_read_b128 v[26:29], v30 offset:2048
	ds_read_b128 v[30:33], v30 offset:3072
	s_mov_b32 m0, s50
	v_lshl_add_u64 v[216:217], s[38:39], 0, v[164:165]
	ds_read_b128 v[184:187], v183 offset:32768
	ds_read_b128 v[188:191], v183 offset:33792
	ds_read_b128 v[192:195], v183 offset:34816
	ds_read_b128 v[196:199], v183 offset:35840
	ds_read_b128 v[200:203], v183 offset:36864
	ds_read_b128 v[204:207], v183 offset:37888
	ds_read_b128 v[208:211], v183 offset:38912
	ds_read_b128 v[212:215], v183 offset:39936
	global_load_lds_dwordx4 v[216:217], off
	v_lshl_add_u64 v[216:217], s[38:39], 0, v[162:163]
	s_mov_b32 m0, s51
	s_nop 0
	global_load_lds_dwordx4 v[216:217], off
	s_waitcnt vmcnt(8)
	s_waitcnt lgkmcnt(0)
	s_barrier
	s_setprio 1
	s_waitcnt lgkmcnt(0)
	v_mfma_f32_16x16x128_f8f6f4 v[122:125], v[10:17], v[200:207], v[122:125]
	v_mfma_f32_16x16x128_f8f6f4 v[126:129], v[2:9], v[200:207], v[126:129]
	v_mfma_f32_16x16x128_f8f6f4 v[158:161], v[2:9], v[184:191], v[158:161]
	v_mfma_f32_16x16x128_f8f6f4 v[154:157], v[10:17], v[184:191], v[154:157]
	v_mfma_f32_16x16x128_f8f6f4 v[138:141], v[10:17], v[192:199], v[138:141]
	v_mfma_f32_16x16x128_f8f6f4 v[142:145], v[2:9], v[192:199], v[142:145]
	v_mfma_f32_16x16x128_f8f6f4 v[110:113], v[2:9], v[208:215], v[110:113]
	v_mfma_f32_16x16x128_f8f6f4 v[106:109], v[10:17], v[208:215], v[106:109]
	v_mfma_f32_16x16x128_f8f6f4 v[102:105], v[18:25], v[208:215], v[102:105]
	v_mfma_f32_16x16x128_f8f6f4 v[98:101], v[26:33], v[208:215], v[98:101]
	v_mfma_f32_16x16x128_f8f6f4 v[146:149], v[26:33], v[184:191], v[146:149]
	v_mfma_f32_16x16x128_f8f6f4 v[150:153], v[18:25], v[184:191], v[150:153]
	v_mfma_f32_16x16x128_f8f6f4 v[134:137], v[18:25], v[192:199], v[134:137]
	v_mfma_f32_16x16x128_f8f6f4 v[130:133], v[26:33], v[192:199], v[130:133]
	v_mfma_f32_16x16x128_f8f6f4 v[114:117], v[26:33], v[200:207], v[114:117]
	v_mfma_f32_16x16x128_f8f6f4 v[118:121], v[18:25], v[200:207], v[118:121]
	s_setprio 0
	s_barrier
	s_mov_b32 m0, s69
	v_lshl_add_u64 v[170:171], v[170:171], 0, s[8:9]
	ds_read_b128 v[184:187], v183 offset:49152
	ds_read_b128 v[188:191], v183 offset:50176
	ds_read_b128 v[192:195], v183 offset:51200
	ds_read_b128 v[196:199], v183 offset:52224
	ds_read_b128 v[200:203], v183 offset:53248
	ds_read_b128 v[204:207], v183 offset:54272
	ds_read_b128 v[208:211], v183 offset:55296
	ds_read_b128 v[212:215], v183 offset:56320
	global_load_lds_dwordx4 v[170:171], off
	v_lshl_add_u64 v[170:171], v[172:173], 0, s[8:9]
	s_mov_b32 m0, s67
	s_nop 0
	global_load_lds_dwordx4 v[170:171], off
	v_lshl_add_u64 v[170:171], s[36:37], 0, v[164:165]
	s_mov_b32 m0, s68
	s_nop 0
	global_load_lds_dwordx4 v[170:171], off
	v_lshl_add_u64 v[170:171], s[36:37], 0, v[162:163]
	s_mov_b32 m0, s66
	s_nop 0
	global_load_lds_dwordx4 v[170:171], off
	v_lshl_add_u64 v[170:171], v[174:175], 0, s[8:9]
	s_mov_b32 m0, s61
	s_nop 0
	global_load_lds_dwordx4 v[170:171], off
	v_lshl_add_u64 v[170:171], v[176:177], 0, s[8:9]
	s_mov_b32 m0, s62
	s_nop 0
	global_load_lds_dwordx4 v[170:171], off
	s_waitcnt vmcnt(8)
	s_waitcnt lgkmcnt(0)
	s_barrier
	s_setprio 1
	s_waitcnt lgkmcnt(0)
	v_mfma_f32_16x16x128_f8f6f4 v[62:65], v[2:9], v[200:207], v[62:65]
	v_mfma_f32_16x16x128_f8f6f4 v[58:61], v[10:17], v[200:207], v[58:61]
	v_mfma_f32_16x16x128_f8f6f4 v[90:93], v[10:17], v[184:191], v[90:93]
	v_mfma_f32_16x16x128_f8f6f4 v[94:97], v[2:9], v[184:191], v[94:97]
	v_mfma_f32_16x16x128_f8f6f4 v[78:81], v[2:9], v[192:199], v[78:81]
	v_mfma_f32_16x16x128_f8f6f4 v[74:77], v[10:17], v[192:199], v[74:77]
	v_mfma_f32_16x16x128_f8f6f4 v[42:45], v[10:17], v[208:215], v[42:45]
	v_mfma_f32_16x16x128_f8f6f4 v[54:57], v[2:9], v[208:215], v[54:57]
	v_mfma_f32_16x16x128_f8f6f4 v[38:41], v[18:25], v[208:215], v[38:41]
	v_mfma_f32_16x16x128_f8f6f4 v[34:37], v[26:33], v[208:215], v[34:37]
	v_mfma_f32_16x16x128_f8f6f4 v[82:85], v[26:33], v[184:191], v[82:85]
	v_mfma_f32_16x16x128_f8f6f4 v[86:89], v[18:25], v[184:191], v[86:89]
	v_mfma_f32_16x16x128_f8f6f4 v[70:73], v[18:25], v[192:199], v[70:73]
	v_mfma_f32_16x16x128_f8f6f4 v[66:69], v[26:33], v[192:199], v[66:69]
	v_mfma_f32_16x16x128_f8f6f4 v[46:49], v[26:33], v[200:207], v[46:49]
	v_mfma_f32_16x16x128_f8f6f4 v[50:53], v[18:25], v[200:207], v[50:53]
	s_setprio 0
	s_barrier
	s_movk_i32 s38, 0x100
	s_andn2_b64 vcc, exec, s[34:35]
	s_mov_b64 s[36:37], -1
	s_mov_b64 s[34:35], 0
	s_cbranch_vccz .LBB0_1558
	s_and_b64 vcc, exec, s[12:13]
	s_cbranch_vccz .LBB0_1561
	s_barrier

.LBB0_1681:
	ds_read_b128 v[26:29], v189
	ds_read_b128 v[30:33], v189 offset:1024
	ds_read_b128 v[18:21], v189 offset:2048
	ds_read_b128 v[22:25], v189 offset:3072
	ds_read_b128 v[10:13], v190
	ds_read_b128 v[14:17], v190 offset:1024
	ds_read_b128 v[2:5], v190 offset:2048
	ds_read_b128 v[6:9], v190 offset:3072
	s_add_u32 s34, s30, 0xfff80080
	s_addc_u32 s35, s31, -1
	s_cmp_eq_u32 s60, 28
	s_cselect_b32 s37, s18, s35
	s_cselect_b32 s36, s19, s34
	s_cselect_b32 s35, s21, s59
	s_cselect_b32 s34, s23, s58
	s_mov_b32 m0, s43
	s_nop 0
	global_load_lds_dwordx4 v168, s[100:101]
	s_mov_b32 m0, s44
	s_nop 0
	global_load_lds_dwordx4 v164, s[100:101]
	s_add_i32 m0, s29, 0xc000
	ds_read_b128 v[178:181], v191
	ds_read_b128 v[182:185], v191 offset:1024
	ds_read_b128 v[194:197], v191 offset:2048
	ds_read_b128 v[198:201], v191 offset:3072
	ds_read_b128 v[202:205], v191 offset:4096
	ds_read_b128 v[206:209], v191 offset:5120
	ds_read_b128 v[210:213], v191 offset:6144
	ds_read_b128 v[214:217], v191 offset:7168
	global_load_lds_dwordx4 v170, s[30:31]
	s_add_i32 m0, s29, 0xe000
	s_nop 0
	global_load_lds_dwordx4 v172, s[30:31]
	s_waitcnt vmcnt(8)
	s_waitcnt lgkmcnt(0)
	s_barrier
	s_setprio 1
	s_waitcnt lgkmcnt(0)
	v_mfma_f32_16x16x128_f8f6f4 v[158:161], v[26:33], v[178:185], v[158:161]
	v_mfma_f32_16x16x128_f8f6f4 v[154:157], v[18:25], v[178:185], v[154:157]
	v_mfma_f32_16x16x128_f8f6f4 v[138:141], v[18:25], v[194:201], v[138:141]
	v_mfma_f32_16x16x128_f8f6f4 v[142:145], v[26:33], v[194:201], v[142:145]
	v_mfma_f32_16x16x128_f8f6f4 v[126:129], v[26:33], v[202:209], v[126:129]
	v_mfma_f32_16x16x128_f8f6f4 v[122:125], v[18:25], v[202:209], v[122:125]
	v_mfma_f32_16x16x128_f8f6f4 v[106:109], v[18:25], v[210:217], v[106:109]
	v_mfma_f32_16x16x128_f8f6f4 v[110:113], v[26:33], v[210:217], v[110:113]
	v_mfma_f32_16x16x128_f8f6f4 v[102:105], v[10:17], v[210:217], v[102:105]
	v_mfma_f32_16x16x128_f8f6f4 v[98:101], v[2:9], v[210:217], v[98:101]
	v_mfma_f32_16x16x128_f8f6f4 v[146:149], v[2:9], v[178:185], v[146:149]
	v_mfma_f32_16x16x128_f8f6f4 v[150:153], v[10:17], v[178:185], v[150:153]
	v_mfma_f32_16x16x128_f8f6f4 v[134:137], v[10:17], v[194:201], v[134:137]
	v_mfma_f32_16x16x128_f8f6f4 v[130:133], v[2:9], v[194:201], v[130:133]
	v_mfma_f32_16x16x128_f8f6f4 v[114:117], v[2:9], v[202:209], v[114:117]
	v_mfma_f32_16x16x128_f8f6f4 v[118:121], v[10:17], v[202:209], v[118:121]
	s_setprio 0
	s_barrier
	s_add_i32 s61, s45, s3
	s_mov_b32 m0, s61
	ds_read_b128 v[194:197], v191 offset:16384
	ds_read_b128 v[198:201], v191 offset:17408
	ds_read_b128 v[202:205], v191 offset:18432
	ds_read_b128 v[206:209], v191 offset:19456
	ds_read_b128 v[210:213], v191 offset:20480
	ds_read_b128 v[214:217], v191 offset:21504
	ds_read_b128 v[218:221], v191 offset:22528
	ds_read_b128 v[222:225], v191 offset:23552
	global_load_lds_dwordx4 v166, s[34:35]
	s_add_i32 m0, s61, 0x2000
	s_add_u32 s62, s34, 0x80000
	s_addc_u32 s63, s35, 0
	s_add_i32 s61, s48, s3
	global_load_lds_dwordx4 v162, s[34:35]
	s_mov_b32 m0, s61
	s_nop 0
	global_load_lds_dwordx4 v166, s[62:63]
	s_add_i32 m0, s61, 0x2000
	s_nop 0
	global_load_lds_dwordx4 v162, s[62:63]
	s_waitcnt vmcnt(6)
	s_waitcnt lgkmcnt(0)
	s_barrier
	s_setprio 1
	s_waitcnt lgkmcnt(0)
	v_mfma_f32_16x16x128_f8f6f4 v[78:81], v[26:33], v[202:209], v[78:81]
	v_mfma_f32_16x16x128_f8f6f4 v[74:77], v[18:25], v[202:209], v[74:77]
	v_mfma_f32_16x16x128_f8f6f4 v[90:93], v[18:25], v[194:201], v[90:93]
	v_mfma_f32_16x16x128_f8f6f4 v[94:97], v[26:33], v[194:201], v[94:97]
	v_mfma_f32_16x16x128_f8f6f4 v[62:65], v[26:33], v[210:217], v[62:65]
	v_mfma_f32_16x16x128_f8f6f4 v[58:61], v[18:25], v[210:217], v[58:61]
	v_mfma_f32_16x16x128_f8f6f4 v[42:45], v[18:25], v[218:225], v[42:45]
	v_mfma_f32_16x16x128_f8f6f4 v[46:49], v[26:33], v[218:225], v[46:49]
	v_mfma_f32_16x16x128_f8f6f4 v[38:41], v[10:17], v[218:225], v[38:41]
	v_mfma_f32_16x16x128_f8f6f4 v[34:37], v[2:9], v[218:225], v[34:37]
	v_mfma_f32_16x16x128_f8f6f4 v[82:85], v[2:9], v[194:201], v[82:85]
	v_mfma_f32_16x16x128_f8f6f4 v[86:89], v[10:17], v[194:201], v[86:89]
	v_mfma_f32_16x16x128_f8f6f4 v[70:73], v[10:17], v[202:209], v[70:73]
	v_mfma_f32_16x16x128_f8f6f4 v[66:69], v[2:9], v[202:209], v[66:69]
	v_mfma_f32_16x16x128_f8f6f4 v[50:53], v[2:9], v[210:217], v[50:53]
	v_mfma_f32_16x16x128_f8f6f4 v[54:57], v[10:17], v[210:217], v[54:57]
	s_setprio 0
	s_barrier
	s_add_i32 s61, 0, 0x18000
	s_add_i32 s62, 0, 0x1c000
	v_add_u32_e32 v14, s61, v187
	v_add_u32_e32 v30, s62, v187
	ds_read_b128 v[2:5], v14
	ds_read_b128 v[6:9], v14 offset:1024
	ds_read_b128 v[10:13], v14 offset:2048
	ds_read_b128 v[14:17], v14 offset:3072
	ds_read_b128 v[18:21], v30
	ds_read_b128 v[22:25], v30 offset:1024
	ds_read_b128 v[26:29], v30 offset:2048
	ds_read_b128 v[30:33], v30 offset:3072
	s_mov_b32 m0, s29
	s_nop 0
	global_load_lds_dwordx4 v168, s[36:37]
	s_mov_b32 m0, s38
	s_nop 0
	global_load_lds_dwordx4 v164, s[36:37]
	s_add_u32 s36, s36, 0x80000
	s_addc_u32 s37, s37, 0
	s_add_u32 s100, s36, 0xfff80080
	s_addc_u32 s101, s37, -1
	s_mov_b32 m0, s39
	ds_read_b128 v[194:197], v191 offset:32768
	ds_read_b128 v[198:201], v191 offset:33792
	ds_read_b128 v[202:205], v191 offset:34816
	ds_read_b128 v[206:209], v191 offset:35840
	ds_read_b128 v[210:213], v191 offset:36864
	ds_read_b128 v[214:217], v191 offset:37888
	ds_read_b128 v[218:221], v191 offset:38912
	ds_read_b128 v[222:225], v191 offset:39936
	global_load_lds_dwordx4 v168, s[36:37]
	s_mov_b32 m0, s40
	s_nop 0
	global_load_lds_dwordx4 v164, s[36:37]
	s_waitcnt vmcnt(8)
	s_waitcnt lgkmcnt(0)
	s_barrier
	s_setprio 1
	s_waitcnt lgkmcnt(0)
	v_mfma_f32_16x16x128_f8f6f4 v[122:125], v[10:17], v[210:217], v[122:125]
	v_mfma_f32_16x16x128_f8f6f4 v[126:129], v[2:9], v[210:217], v[126:129]
	v_mfma_f32_16x16x128_f8f6f4 v[158:161], v[2:9], v[194:201], v[158:161]
	v_mfma_f32_16x16x128_f8f6f4 v[154:157], v[10:17], v[194:201], v[154:157]
	v_mfma_f32_16x16x128_f8f6f4 v[138:141], v[10:17], v[202:209], v[138:141]
	v_mfma_f32_16x16x128_f8f6f4 v[142:145], v[2:9], v[202:209], v[142:145]
	v_mfma_f32_16x16x128_f8f6f4 v[110:113], v[2:9], v[218:225], v[110:113]
	v_mfma_f32_16x16x128_f8f6f4 v[106:109], v[10:17], v[218:225], v[106:109]
	v_mfma_f32_16x16x128_f8f6f4 v[102:105], v[18:25], v[218:225], v[102:105]
	v_mfma_f32_16x16x128_f8f6f4 v[98:101], v[26:33], v[218:225], v[98:101]
	v_mfma_f32_16x16x128_f8f6f4 v[146:149], v[26:33], v[194:201], v[146:149]
	v_mfma_f32_16x16x128_f8f6f4 v[150:153], v[18:25], v[194:201], v[150:153]
	v_mfma_f32_16x16x128_f8f6f4 v[134:137], v[18:25], v[202:209], v[134:137]
	v_mfma_f32_16x16x128_f8f6f4 v[130:133], v[26:33], v[202:209], v[130:133]
	v_mfma_f32_16x16x128_f8f6f4 v[114:117], v[26:33], v[210:217], v[114:117]
	v_mfma_f32_16x16x128_f8f6f4 v[118:121], v[18:25], v[210:217], v[118:121]
	s_setprio 0
	s_barrier
	s_add_i32 s36, s61, s3
	s_mov_b32 m0, s36
	s_add_u32 s98, s34, 0x80
	s_addc_u32 s99, s35, 0
	ds_read_b128 v[194:197], v191 offset:49152
	ds_read_b128 v[198:201], v191 offset:50176
	ds_read_b128 v[202:205], v191 offset:51200
	ds_read_b128 v[206:209], v191 offset:52224
	ds_read_b128 v[210:213], v191 offset:53248
	ds_read_b128 v[214:217], v191 offset:54272
	ds_read_b128 v[218:221], v191 offset:55296
	ds_read_b128 v[222:225], v191 offset:56320
	global_load_lds_dwordx4 v166, s[98:99]
	s_add_i32 m0, s36, 0x2000
	s_add_u32 s34, s34, 0x80080
	s_addc_u32 s35, s35, 0
	s_add_i32 s36, s62, s3
	global_load_lds_dwordx4 v162, s[98:99]
	s_mov_b32 m0, s36
	s_nop 0
	global_load_lds_dwordx4 v166, s[34:35]
	s_add_i32 m0, s36, 0x2000
	s_nop 0
	global_load_lds_dwordx4 v162, s[34:35]
	s_waitcnt vmcnt(6)
	s_waitcnt lgkmcnt(0)
	s_barrier
	s_setprio 1
	s_waitcnt lgkmcnt(0)
	v_mfma_f32_16x16x128_f8f6f4 v[62:65], v[2:9], v[210:217], v[62:65]
	v_mfma_f32_16x16x128_f8f6f4 v[58:61], v[10:17], v[210:217], v[58:61]
	v_mfma_f32_16x16x128_f8f6f4 v[90:93], v[10:17], v[194:201], v[90:93]
	v_mfma_f32_16x16x128_f8f6f4 v[94:97], v[2:9], v[194:201], v[94:97]
	v_mfma_f32_16x16x128_f8f6f4 v[78:81], v[2:9], v[202:209], v[78:81]
	v_mfma_f32_16x16x128_f8f6f4 v[74:77], v[10:17], v[202:209], v[74:77]
	v_mfma_f32_16x16x128_f8f6f4 v[42:45], v[10:17], v[218:225], v[42:45]
	v_mfma_f32_16x16x128_f8f6f4 v[46:49], v[2:9], v[218:225], v[46:49]
	v_mfma_f32_16x16x128_f8f6f4 v[38:41], v[18:25], v[218:225], v[38:41]
	v_mfma_f32_16x16x128_f8f6f4 v[34:37], v[26:33], v[218:225], v[34:37]
	v_mfma_f32_16x16x128_f8f6f4 v[82:85], v[26:33], v[194:201], v[82:85]
	v_mfma_f32_16x16x128_f8f6f4 v[86:89], v[18:25], v[194:201], v[86:89]
	v_mfma_f32_16x16x128_f8f6f4 v[70:73], v[18:25], v[202:209], v[70:73]
	v_mfma_f32_16x16x128_f8f6f4 v[66:69], v[26:33], v[202:209], v[66:69]
	v_mfma_f32_16x16x128_f8f6f4 v[50:53], v[26:33], v[210:217], v[50:53]
	v_mfma_f32_16x16x128_f8f6f4 v[54:57], v[18:25], v[210:217], v[54:57]
	s_setprio 0
	s_barrier
	s_add_i32 s60, s60, 2
	s_add_u32 s30, s30, 0x100
	s_addc_u32 s31, s31, 0
	s_add_u32 s58, s58, 0x100
	s_addc_u32 s59, s59, 0
	s_cmp_gt_u32 s60, 29
	s_cbranch_scc0 .LBB0_1681
	s_and_b64 vcc, exec, s[12:13]
	s_cbranch_vccz .LBB0_1684
	s_barrier

.LBB0_1745:
	s_add_u32 s8, s49, s6
	s_addc_u32 s9, s50, s7
	s_add_u32 s8, s8, 0x32800100
	s_addc_u32 s9, s9, 0
	s_add_u32 s73, s51, s6
	s_addc_u32 s74, s54, s7
	s_add_i32 s72, 0, 0x10000
	s_cmpk_eq_i32 s6, 0x2a00
	s_cselect_b32 s37, s5, s9
	s_cselect_b32 s36, s4, s8
	s_cselect_b32 s9, s13, s74
	s_cselect_b32 s8, s12, s73
	s_add_i32 s73, 0, 0x14000
	v_add_u32_e32 v2, s72, v188
	v_add_u32_e32 v6, s73, v188
	ds_read_b128 v[26:29], v2
	ds_read_b128 v[30:33], v2 offset:1024
	ds_read_b128 v[18:21], v2 offset:2048
	ds_read_b128 v[22:25], v2 offset:3072
	ds_read_b128 v[10:13], v6
	ds_read_b128 v[14:17], v6 offset:1024
	ds_read_b128 v[2:5], v6 offset:2048
	ds_read_b128 v[6:9], v6 offset:3072
	v_lshl_add_u64 v[214:215], v[168:169], 0, s[6:7]
	s_add_i32 m0, s64, 0xc000
	ds_read_b128 v[172:175], v189
	ds_read_b128 v[176:179], v189 offset:1024
	ds_read_b128 v[190:193], v189 offset:2048
	ds_read_b128 v[194:197], v189 offset:3072
	ds_read_b128 v[198:201], v189 offset:4096
	ds_read_b128 v[202:205], v189 offset:5120
	ds_read_b128 v[206:209], v189 offset:6144
	ds_read_b128 v[210:213], v189 offset:7168
	global_load_lds_dwordx4 v[214:215], off
	v_lshl_add_u64 v[214:215], v[170:171], 0, s[6:7]
	s_add_i32 m0, s64, 0xe000
	s_nop 0
	global_load_lds_dwordx4 v[214:215], off
	s_waitcnt vmcnt(8)
	s_waitcnt lgkmcnt(0)
	s_barrier
	s_setprio 1
	s_waitcnt lgkmcnt(0)
	v_mfma_f32_16x16x128_f8f6f4 v[158:161], v[26:33], v[172:179], v[158:161]
	v_mfma_f32_16x16x128_f8f6f4 v[154:157], v[18:25], v[172:179], v[154:157]
	v_mfma_f32_16x16x128_f8f6f4 v[118:121], v[18:25], v[190:197], v[118:121]
	v_mfma_f32_16x16x128_f8f6f4 v[122:125], v[26:33], v[190:197], v[122:125]
	v_mfma_f32_16x16x128_f8f6f4 v[126:129], v[26:33], v[198:205], v[126:129]
	v_mfma_f32_16x16x128_f8f6f4 v[114:117], v[18:25], v[198:205], v[114:117]
	v_mfma_f32_16x16x128_f8f6f4 v[106:109], v[18:25], v[206:213], v[106:109]
	v_mfma_f32_16x16x128_f8f6f4 v[110:113], v[26:33], v[206:213], v[110:113]
	v_mfma_f32_16x16x128_f8f6f4 v[102:105], v[10:17], v[206:213], v[102:105]
	v_mfma_f32_16x16x128_f8f6f4 v[98:101], v[2:9], v[206:213], v[98:101]
	v_mfma_f32_16x16x128_f8f6f4 v[146:149], v[2:9], v[172:179], v[146:149]
	v_mfma_f32_16x16x128_f8f6f4 v[150:153], v[10:17], v[172:179], v[150:153]
	v_mfma_f32_16x16x128_f8f6f4 v[142:145], v[10:17], v[190:197], v[142:145]
	v_mfma_f32_16x16x128_f8f6f4 v[138:141], v[2:9], v[190:197], v[138:141]
	v_mfma_f32_16x16x128_f8f6f4 v[130:133], v[2:9], v[198:205], v[130:133]
	v_mfma_f32_16x16x128_f8f6f4 v[134:137], v[10:17], v[198:205], v[134:137]
	s_setprio 0
	s_barrier
	s_add_i32 s72, s72, s43
	v_lshl_add_u64 v[172:173], s[8:9], 0, v[162:163]
	s_mov_b32 m0, s72
	ds_read_b128 v[190:193], v189 offset:16384
	ds_read_b128 v[194:197], v189 offset:17408
	ds_read_b128 v[198:201], v189 offset:18432
	ds_read_b128 v[202:205], v189 offset:19456
	ds_read_b128 v[206:209], v189 offset:20480
	ds_read_b128 v[210:213], v189 offset:21504
	ds_read_b128 v[214:217], v189 offset:22528
	ds_read_b128 v[218:221], v189 offset:23552
	global_load_lds_dwordx4 v[172:173], off
	s_add_i32 m0, s72, 0x2000
	s_add_u32 s74, s8, 0x158000
	v_lshl_add_u64 v[174:175], s[8:9], 0, v[166:167]
	s_addc_u32 s75, s9, 0
	s_add_i32 s72, s73, s43
	global_load_lds_dwordx4 v[174:175], off
	v_lshl_add_u64 v[176:177], s[74:75], 0, v[162:163]
	s_mov_b32 m0, s72
	v_lshl_add_u64 v[178:179], s[36:37], 0, v[166:167]
	global_load_lds_dwordx4 v[176:177], off
	v_lshl_add_u64 v[176:177], s[74:75], 0, v[166:167]
	s_add_i32 m0, s72, 0x2000
	s_nop 0
	global_load_lds_dwordx4 v[176:177], off
	v_lshl_add_u64 v[176:177], s[36:37], 0, v[162:163]
	s_mov_b32 m0, s64
	s_nop 0
	global_load_lds_dwordx4 v[176:177], off
	s_mov_b32 m0, s65
	s_nop 0
	global_load_lds_dwordx4 v[178:179], off
	s_waitcnt vmcnt(8)
	s_waitcnt lgkmcnt(0)
	s_barrier
	s_setprio 1
	s_waitcnt lgkmcnt(0)
	v_mfma_f32_16x16x128_f8f6f4 v[78:81], v[26:33], v[198:205], v[78:81]
	v_mfma_f32_16x16x128_f8f6f4 v[74:77], v[18:25], v[198:205], v[74:77]
	v_mfma_f32_16x16x128_f8f6f4 v[90:93], v[18:25], v[190:197], v[90:93]
	v_mfma_f32_16x16x128_f8f6f4 v[94:97], v[26:33], v[190:197], v[94:97]
	v_mfma_f32_16x16x128_f8f6f4 v[62:65], v[26:33], v[206:213], v[62:65]
	v_mfma_f32_16x16x128_f8f6f4 v[58:61], v[18:25], v[206:213], v[58:61]
	v_mfma_f32_16x16x128_f8f6f4 v[42:45], v[18:25], v[214:221], v[42:45]
	v_mfma_f32_16x16x128_f8f6f4 v[46:49], v[26:33], v[214:221], v[46:49]
	v_mfma_f32_16x16x128_f8f6f4 v[38:41], v[10:17], v[214:221], v[38:41]
	v_mfma_f32_16x16x128_f8f6f4 v[34:37], v[2:9], v[214:221], v[34:37]
	v_mfma_f32_16x16x128_f8f6f4 v[82:85], v[2:9], v[190:197], v[82:85]
	v_mfma_f32_16x16x128_f8f6f4 v[86:89], v[10:17], v[190:197], v[86:89]
	v_mfma_f32_16x16x128_f8f6f4 v[70:73], v[10:17], v[198:205], v[70:73]
	v_mfma_f32_16x16x128_f8f6f4 v[66:69], v[2:9], v[198:205], v[66:69]
	v_mfma_f32_16x16x128_f8f6f4 v[50:53], v[2:9], v[206:213], v[50:53]
	v_mfma_f32_16x16x128_f8f6f4 v[54:57], v[10:17], v[206:213], v[54:57]
	s_setprio 0
	s_barrier
	s_add_i32 s72, 0, 0x18000
	s_add_i32 s73, 0, 0x1c000
	v_add_u32_e32 v14, s72, v188
	v_add_u32_e32 v30, s73, v188
	ds_read_b128 v[2:5], v14
	ds_read_b128 v[6:9], v14 offset:1024
	ds_read_b128 v[10:13], v14 offset:2048
	ds_read_b128 v[14:17], v14 offset:3072
	ds_read_b128 v[18:21], v30
	ds_read_b128 v[22:25], v30 offset:1024
	ds_read_b128 v[26:29], v30 offset:2048
	ds_read_b128 v[30:33], v30 offset:3072
	s_add_u32 s36, s36, 0x158000
	s_addc_u32 s37, s37, 0
	s_mov_b32 m0, s66
	v_lshl_add_u64 v[222:223], s[36:37], 0, v[162:163]
	ds_read_b128 v[190:193], v189 offset:32768
	ds_read_b128 v[194:197], v189 offset:33792
	ds_read_b128 v[198:201], v189 offset:34816
	ds_read_b128 v[202:205], v189 offset:35840
	ds_read_b128 v[206:209], v189 offset:36864
	ds_read_b128 v[210:213], v189 offset:37888
	ds_read_b128 v[214:217], v189 offset:38912
	ds_read_b128 v[218:221], v189 offset:39936
	global_load_lds_dwordx4 v[222:223], off
	v_lshl_add_u64 v[222:223], s[36:37], 0, v[166:167]
	s_mov_b32 m0, s67
	s_nop 0
	global_load_lds_dwordx4 v[222:223], off
	s_waitcnt vmcnt(8)
	s_waitcnt lgkmcnt(0)
	s_barrier
	s_setprio 1
	s_waitcnt lgkmcnt(0)
	v_mfma_f32_16x16x128_f8f6f4 v[114:117], v[10:17], v[206:213], v[114:117]
	v_mfma_f32_16x16x128_f8f6f4 v[126:129], v[2:9], v[206:213], v[126:129]
	v_mfma_f32_16x16x128_f8f6f4 v[158:161], v[2:9], v[190:197], v[158:161]
	v_mfma_f32_16x16x128_f8f6f4 v[154:157], v[10:17], v[190:197], v[154:157]
	v_mfma_f32_16x16x128_f8f6f4 v[118:121], v[10:17], v[198:205], v[118:121]
	v_mfma_f32_16x16x128_f8f6f4 v[122:125], v[2:9], v[198:205], v[122:125]
	v_mfma_f32_16x16x128_f8f6f4 v[110:113], v[2:9], v[214:221], v[110:113]
	v_mfma_f32_16x16x128_f8f6f4 v[106:109], v[10:17], v[214:221], v[106:109]
	v_mfma_f32_16x16x128_f8f6f4 v[102:105], v[18:25], v[214:221], v[102:105]
	v_mfma_f32_16x16x128_f8f6f4 v[98:101], v[26:33], v[214:221], v[98:101]
	v_mfma_f32_16x16x128_f8f6f4 v[146:149], v[26:33], v[190:197], v[146:149]
	v_mfma_f32_16x16x128_f8f6f4 v[150:153], v[18:25], v[190:197], v[150:153]
	v_mfma_f32_16x16x128_f8f6f4 v[142:145], v[18:25], v[198:205], v[142:145]
	v_mfma_f32_16x16x128_f8f6f4 v[138:141], v[26:33], v[198:205], v[138:141]
	v_mfma_f32_16x16x128_f8f6f4 v[130:133], v[26:33], v[206:213], v[130:133]
	v_mfma_f32_16x16x128_f8f6f4 v[134:137], v[18:25], v[206:213], v[134:137]
	s_setprio 0
	s_barrier
	s_add_i32 s36, s72, s43
	v_lshl_add_u64 v[172:173], v[172:173], 0, s[22:23]
	s_mov_b32 m0, s36
	ds_read_b128 v[190:193], v189 offset:49152
	ds_read_b128 v[194:197], v189 offset:50176
	ds_read_b128 v[198:201], v189 offset:51200
	ds_read_b128 v[202:205], v189 offset:52224
	ds_read_b128 v[206:209], v189 offset:53248
	ds_read_b128 v[210:213], v189 offset:54272
	ds_read_b128 v[214:217], v189 offset:55296
	ds_read_b128 v[218:221], v189 offset:56320
	global_load_lds_dwordx4 v[172:173], off
	s_add_i32 m0, s36, 0x2000
	s_add_u32 s8, s8, 0x158080
	v_lshl_add_u64 v[172:173], v[174:175], 0, s[22:23]
	s_addc_u32 s9, s9, 0
	s_add_i32 s36, s73, s43
	global_load_lds_dwordx4 v[172:173], off
	v_lshl_add_u64 v[172:173], s[8:9], 0, v[162:163]
	s_mov_b32 m0, s36
	s_nop 0
	global_load_lds_dwordx4 v[172:173], off
	v_lshl_add_u64 v[172:173], s[8:9], 0, v[166:167]
	s_add_i32 m0, s36, 0x2000
	s_nop 0
	global_load_lds_dwordx4 v[172:173], off
	v_lshl_add_u64 v[172:173], v[176:177], 0, s[22:23]
	s_mov_b32 m0, s69
	s_nop 0
	global_load_lds_dwordx4 v[172:173], off
	v_lshl_add_u64 v[172:173], v[178:179], 0, s[22:23]
	s_mov_b32 m0, s70
	s_nop 0
	global_load_lds_dwordx4 v[172:173], off
	s_waitcnt vmcnt(8)
	s_waitcnt lgkmcnt(0)
	s_barrier
	s_setprio 1
	s_waitcnt lgkmcnt(0)
	v_mfma_f32_16x16x128_f8f6f4 v[62:65], v[2:9], v[206:213], v[62:65]
	v_mfma_f32_16x16x128_f8f6f4 v[58:61], v[10:17], v[206:213], v[58:61]
	v_mfma_f32_16x16x128_f8f6f4 v[90:93], v[10:17], v[190:197], v[90:93]
	v_mfma_f32_16x16x128_f8f6f4 v[94:97], v[2:9], v[190:197], v[94:97]
	v_mfma_f32_16x16x128_f8f6f4 v[78:81], v[2:9], v[198:205], v[78:81]
	v_mfma_f32_16x16x128_f8f6f4 v[74:77], v[10:17], v[198:205], v[74:77]
	v_mfma_f32_16x16x128_f8f6f4 v[42:45], v[10:17], v[214:221], v[42:45]
	v_mfma_f32_16x16x128_f8f6f4 v[46:49], v[2:9], v[214:221], v[46:49]
	v_mfma_f32_16x16x128_f8f6f4 v[38:41], v[18:25], v[214:221], v[38:41]
	v_mfma_f32_16x16x128_f8f6f4 v[34:37], v[26:33], v[214:221], v[34:37]
	v_mfma_f32_16x16x128_f8f6f4 v[82:85], v[26:33], v[190:197], v[82:85]
	v_mfma_f32_16x16x128_f8f6f4 v[86:89], v[18:25], v[190:197], v[86:89]
	v_mfma_f32_16x16x128_f8f6f4 v[70:73], v[18:25], v[198:205], v[70:73]
	v_mfma_f32_16x16x128_f8f6f4 v[66:69], v[26:33], v[198:205], v[66:69]
	v_mfma_f32_16x16x128_f8f6f4 v[50:53], v[26:33], v[206:213], v[50:53]
	v_mfma_f32_16x16x128_f8f6f4 v[54:57], v[18:25], v[206:213], v[54:57]
	s_setprio 0
	s_barrier
	s_add_i32 s71, s71, 2
	s_add_u32 s6, s6, 0x100
	s_addc_u32 s7, s7, 0
	s_cmpk_lt_u32 s71, 0x54
	s_cbranch_scc1 .LBB0_1745
	s_waitcnt vmcnt(0)
	s_cmpk_gt_u32 s40, 0xff
	s_cbranch_scc1 .LBB0_1748
	s_barrier

.LBB0_1807:
	ds_read_b128 v[26:29], v185
	ds_read_b128 v[30:33], v185 offset:1024
	ds_read_b128 v[18:21], v185 offset:2048
	ds_read_b128 v[22:25], v185 offset:3072
	ds_read_b128 v[10:13], v186
	ds_read_b128 v[14:17], v186 offset:1024
	ds_read_b128 v[2:5], v186 offset:2048
	ds_read_b128 v[6:9], v186 offset:3072
	s_add_u32 s28, s26, 0xffea8080
	s_addc_u32 s29, s27, -1
	s_cmpk_eq_i32 s58, 0x52
	s_cselect_b32 s31, s5, s29
	s_cselect_b32 s30, s4, s28
	s_cselect_b32 s29, s25, s57
	s_cselect_b32 s28, s24, s56
	v_lshl_add_u64 v[212:213], s[26:27], 0, v[166:167]
	s_add_i32 m0, s34, 0xc000
	ds_read_b128 v[174:177], v187
	ds_read_b128 v[178:181], v187 offset:1024
	ds_read_b128 v[188:191], v187 offset:2048
	ds_read_b128 v[192:195], v187 offset:3072
	ds_read_b128 v[196:199], v187 offset:4096
	ds_read_b128 v[200:203], v187 offset:5120
	ds_read_b128 v[204:207], v187 offset:6144
	ds_read_b128 v[208:211], v187 offset:7168
	global_load_lds_dwordx4 v[212:213], off
	v_lshl_add_u64 v[212:213], s[26:27], 0, v[168:169]
	s_add_i32 m0, s34, 0xe000
	s_nop 0
	global_load_lds_dwordx4 v[212:213], off
	s_waitcnt vmcnt(8)
	s_waitcnt lgkmcnt(0)
	s_barrier
	s_setprio 1
	s_waitcnt lgkmcnt(0)
	v_mfma_f32_16x16x128_f8f6f4 v[158:161], v[26:33], v[174:181], v[158:161]
	v_mfma_f32_16x16x128_f8f6f4 v[154:157], v[18:25], v[174:181], v[154:157]
	v_mfma_f32_16x16x128_f8f6f4 v[138:141], v[18:25], v[188:195], v[138:141]
	v_mfma_f32_16x16x128_f8f6f4 v[142:145], v[26:33], v[188:195], v[142:145]
	v_mfma_f32_16x16x128_f8f6f4 v[126:129], v[26:33], v[196:203], v[126:129]
	v_mfma_f32_16x16x128_f8f6f4 v[122:125], v[18:25], v[196:203], v[122:125]
	v_mfma_f32_16x16x128_f8f6f4 v[106:109], v[18:25], v[204:211], v[106:109]
	v_mfma_f32_16x16x128_f8f6f4 v[110:113], v[26:33], v[204:211], v[110:113]
	v_mfma_f32_16x16x128_f8f6f4 v[102:105], v[10:17], v[204:211], v[102:105]
	v_mfma_f32_16x16x128_f8f6f4 v[98:101], v[2:9], v[204:211], v[98:101]
	v_mfma_f32_16x16x128_f8f6f4 v[146:149], v[2:9], v[174:181], v[146:149]
	v_mfma_f32_16x16x128_f8f6f4 v[150:153], v[10:17], v[174:181], v[150:153]
	v_mfma_f32_16x16x128_f8f6f4 v[134:137], v[10:17], v[188:195], v[134:137]
	v_mfma_f32_16x16x128_f8f6f4 v[130:133], v[2:9], v[188:195], v[130:133]
	v_mfma_f32_16x16x128_f8f6f4 v[114:117], v[2:9], v[196:203], v[114:117]
	v_mfma_f32_16x16x128_f8f6f4 v[118:121], v[10:17], v[196:203], v[118:121]
	s_setprio 0
	s_barrier
	s_add_i32 s59, s42, s3
	v_lshl_add_u64 v[174:175], s[28:29], 0, v[164:165]
	s_mov_b32 m0, s59
	ds_read_b128 v[188:191], v187 offset:16384
	ds_read_b128 v[192:195], v187 offset:17408
	ds_read_b128 v[196:199], v187 offset:18432
	ds_read_b128 v[200:203], v187 offset:19456
	ds_read_b128 v[204:207], v187 offset:20480
	ds_read_b128 v[208:211], v187 offset:21504
	ds_read_b128 v[212:215], v187 offset:22528
	ds_read_b128 v[216:219], v187 offset:23552
	global_load_lds_dwordx4 v[174:175], off
	s_add_i32 m0, s59, 0x2000
	s_add_u32 s60, s28, 0x158000
	v_lshl_add_u64 v[176:177], s[28:29], 0, v[162:163]
	s_addc_u32 s61, s29, 0
	s_add_i32 s59, s43, s3
	global_load_lds_dwordx4 v[176:177], off
	v_lshl_add_u64 v[178:179], s[60:61], 0, v[164:165]
	s_mov_b32 m0, s59
	v_lshl_add_u64 v[180:181], s[30:31], 0, v[162:163]
	global_load_lds_dwordx4 v[178:179], off
	v_lshl_add_u64 v[178:179], s[60:61], 0, v[162:163]
	s_add_i32 m0, s59, 0x2000
	s_nop 0
	global_load_lds_dwordx4 v[178:179], off
	v_lshl_add_u64 v[178:179], s[30:31], 0, v[164:165]
	s_mov_b32 m0, s34
	s_nop 0
	global_load_lds_dwordx4 v[178:179], off
	s_mov_b32 m0, s35
	s_nop 0
	global_load_lds_dwordx4 v[180:181], off
	s_waitcnt vmcnt(8)
	s_waitcnt lgkmcnt(0)
	s_barrier
	s_setprio 1
	s_waitcnt lgkmcnt(0)
	v_mfma_f32_16x16x128_f8f6f4 v[78:81], v[26:33], v[196:203], v[78:81]
	v_mfma_f32_16x16x128_f8f6f4 v[74:77], v[18:25], v[196:203], v[74:77]
	v_mfma_f32_16x16x128_f8f6f4 v[90:93], v[18:25], v[188:195], v[90:93]
	v_mfma_f32_16x16x128_f8f6f4 v[94:97], v[26:33], v[188:195], v[94:97]
	v_mfma_f32_16x16x128_f8f6f4 v[62:65], v[26:33], v[204:211], v[62:65]
	v_mfma_f32_16x16x128_f8f6f4 v[58:61], v[18:25], v[204:211], v[58:61]
	v_mfma_f32_16x16x128_f8f6f4 v[42:45], v[18:25], v[212:219], v[42:45]
	v_mfma_f32_16x16x128_f8f6f4 v[54:57], v[26:33], v[212:219], v[54:57]
	v_mfma_f32_16x16x128_f8f6f4 v[38:41], v[10:17], v[212:219], v[38:41]
	v_mfma_f32_16x16x128_f8f6f4 v[34:37], v[2:9], v[212:219], v[34:37]
	v_mfma_f32_16x16x128_f8f6f4 v[82:85], v[2:9], v[188:195], v[82:85]
	v_mfma_f32_16x16x128_f8f6f4 v[86:89], v[10:17], v[188:195], v[86:89]
	v_mfma_f32_16x16x128_f8f6f4 v[70:73], v[10:17], v[196:203], v[70:73]
	v_mfma_f32_16x16x128_f8f6f4 v[66:69], v[2:9], v[196:203], v[66:69]
	v_mfma_f32_16x16x128_f8f6f4 v[46:49], v[2:9], v[204:211], v[46:49]
	v_mfma_f32_16x16x128_f8f6f4 v[50:53], v[10:17], v[204:211], v[50:53]
	s_setprio 0
	s_barrier
	s_add_i32 s59, 0, 0x18000
	s_add_i32 s60, 0, 0x1c000
	v_add_u32_e32 v14, s59, v183
	v_add_u32_e32 v30, s60, v183
	ds_read_b128 v[2:5], v14
	ds_read_b128 v[6:9], v14 offset:1024
	ds_read_b128 v[10:13], v14 offset:2048
	ds_read_b128 v[14:17], v14 offset:3072
	ds_read_b128 v[18:21], v30
	ds_read_b128 v[22:25], v30 offset:1024
	ds_read_b128 v[26:29], v30 offset:2048
	ds_read_b128 v[30:33], v30 offset:3072
	s_add_u32 s30, s30, 0x158000
	s_addc_u32 s31, s31, 0
	s_mov_b32 m0, s36
	v_lshl_add_u64 v[220:221], s[30:31], 0, v[164:165]
	ds_read_b128 v[188:191], v187 offset:32768
	ds_read_b128 v[192:195], v187 offset:33792
	ds_read_b128 v[196:199], v187 offset:34816
	ds_read_b128 v[200:203], v187 offset:35840
	ds_read_b128 v[204:207], v187 offset:36864
	ds_read_b128 v[208:211], v187 offset:37888
	ds_read_b128 v[212:215], v187 offset:38912
	ds_read_b128 v[216:219], v187 offset:39936
	global_load_lds_dwordx4 v[220:221], off
	v_lshl_add_u64 v[220:221], s[30:31], 0, v[162:163]
	s_mov_b32 m0, s37
	s_nop 0
	global_load_lds_dwordx4 v[220:221], off
	s_waitcnt vmcnt(8)
	s_waitcnt lgkmcnt(0)
	s_barrier
	s_setprio 1
	s_waitcnt lgkmcnt(0)
	v_mfma_f32_16x16x128_f8f6f4 v[122:125], v[10:17], v[204:211], v[122:125]
	v_mfma_f32_16x16x128_f8f6f4 v[126:129], v[2:9], v[204:211], v[126:129]
	v_mfma_f32_16x16x128_f8f6f4 v[158:161], v[2:9], v[188:195], v[158:161]
	v_mfma_f32_16x16x128_f8f6f4 v[154:157], v[10:17], v[188:195], v[154:157]
	v_mfma_f32_16x16x128_f8f6f4 v[138:141], v[10:17], v[196:203], v[138:141]
	v_mfma_f32_16x16x128_f8f6f4 v[142:145], v[2:9], v[196:203], v[142:145]
	v_mfma_f32_16x16x128_f8f6f4 v[110:113], v[2:9], v[212:219], v[110:113]
	v_mfma_f32_16x16x128_f8f6f4 v[106:109], v[10:17], v[212:219], v[106:109]
	v_mfma_f32_16x16x128_f8f6f4 v[102:105], v[18:25], v[212:219], v[102:105]
	v_mfma_f32_16x16x128_f8f6f4 v[98:101], v[26:33], v[212:219], v[98:101]
	v_mfma_f32_16x16x128_f8f6f4 v[146:149], v[26:33], v[188:195], v[146:149]
	v_mfma_f32_16x16x128_f8f6f4 v[150:153], v[18:25], v[188:195], v[150:153]
	v_mfma_f32_16x16x128_f8f6f4 v[134:137], v[18:25], v[196:203], v[134:137]
	v_mfma_f32_16x16x128_f8f6f4 v[130:133], v[26:33], v[196:203], v[130:133]
	v_mfma_f32_16x16x128_f8f6f4 v[114:117], v[26:33], v[204:211], v[114:117]
	v_mfma_f32_16x16x128_f8f6f4 v[118:121], v[18:25], v[204:211], v[118:121]
	s_setprio 0
	s_barrier
	s_add_i32 s30, s59, s3
	v_lshl_add_u64 v[174:175], v[174:175], 0, s[10:11]
	s_mov_b32 m0, s30
	ds_read_b128 v[188:191], v187 offset:49152
	ds_read_b128 v[192:195], v187 offset:50176
	ds_read_b128 v[196:199], v187 offset:51200
	ds_read_b128 v[200:203], v187 offset:52224
	ds_read_b128 v[204:207], v187 offset:53248
	ds_read_b128 v[208:211], v187 offset:54272
	ds_read_b128 v[212:215], v187 offset:55296
	ds_read_b128 v[216:219], v187 offset:56320
	global_load_lds_dwordx4 v[174:175], off
	s_add_i32 m0, s30, 0x2000
	s_add_u32 s28, s28, 0x158080
	v_lshl_add_u64 v[174:175], v[176:177], 0, s[10:11]
	s_addc_u32 s29, s29, 0
	s_add_i32 s30, s60, s3
	global_load_lds_dwordx4 v[174:175], off
	v_lshl_add_u64 v[174:175], s[28:29], 0, v[164:165]
	s_mov_b32 m0, s30
	s_nop 0
	global_load_lds_dwordx4 v[174:175], off
	v_lshl_add_u64 v[174:175], s[28:29], 0, v[162:163]
	s_add_i32 m0, s30, 0x2000
	s_nop 0
	global_load_lds_dwordx4 v[174:175], off
	v_lshl_add_u64 v[174:175], v[178:179], 0, s[10:11]
	s_mov_b32 m0, s40
	s_nop 0
	global_load_lds_dwordx4 v[174:175], off
	v_lshl_add_u64 v[174:175], v[180:181], 0, s[10:11]
	s_mov_b32 m0, s41
	s_nop 0
	global_load_lds_dwordx4 v[174:175], off
	s_waitcnt vmcnt(8)
	s_waitcnt lgkmcnt(0)
	s_barrier
	s_setprio 1
	s_waitcnt lgkmcnt(0)
	v_mfma_f32_16x16x128_f8f6f4 v[62:65], v[2:9], v[204:211], v[62:65]
	v_mfma_f32_16x16x128_f8f6f4 v[58:61], v[10:17], v[204:211], v[58:61]
	v_mfma_f32_16x16x128_f8f6f4 v[90:93], v[10:17], v[188:195], v[90:93]
	v_mfma_f32_16x16x128_f8f6f4 v[94:97], v[2:9], v[188:195], v[94:97]
	v_mfma_f32_16x16x128_f8f6f4 v[78:81], v[2:9], v[196:203], v[78:81]
	v_mfma_f32_16x16x128_f8f6f4 v[74:77], v[10:17], v[196:203], v[74:77]
	v_mfma_f32_16x16x128_f8f6f4 v[42:45], v[10:17], v[212:219], v[42:45]
	v_mfma_f32_16x16x128_f8f6f4 v[54:57], v[2:9], v[212:219], v[54:57]
	v_mfma_f32_16x16x128_f8f6f4 v[38:41], v[18:25], v[212:219], v[38:41]
	v_mfma_f32_16x16x128_f8f6f4 v[34:37], v[26:33], v[212:219], v[34:37]
	v_mfma_f32_16x16x128_f8f6f4 v[82:85], v[26:33], v[188:195], v[82:85]
	v_mfma_f32_16x16x128_f8f6f4 v[86:89], v[18:25], v[188:195], v[86:89]
	v_mfma_f32_16x16x128_f8f6f4 v[70:73], v[18:25], v[196:203], v[70:73]
	v_mfma_f32_16x16x128_f8f6f4 v[66:69], v[26:33], v[196:203], v[66:69]
	v_mfma_f32_16x16x128_f8f6f4 v[46:49], v[26:33], v[204:211], v[46:49]
	v_mfma_f32_16x16x128_f8f6f4 v[50:53], v[18:25], v[204:211], v[50:53]
	s_setprio 0
	s_barrier
	s_add_i32 s58, s58, 2
	s_add_u32 s26, s26, 0x100
	s_addc_u32 s27, s27, 0
	s_add_u32 s56, s56, 0x100
	s_addc_u32 s57, s57, 0
	s_cmpk_gt_u32 s58, 0x53
	s_cbranch_scc0 .LBB0_1807
	s_and_b64 vcc, exec, s[12:13]
	s_cbranch_vccz .LBB0_1810
	s_barrier
